# v21 + hand-written grid-barrier body with the acquire invalidate issued at arrival (workgroup quiescent until release), overlapped with the leader's write-back
# baseline (speedup 1.0000x reference)
; __device__ __forceinline__ unsigned xb_add(unsigned* p, unsigned v) { return __hip_atomic_fetch_add(p, v, __ATOMIC_RELAXED, __HIP_MEMORY_SCOPE_AGENT); }
; __device__ __forceinline__ void xcd_barrier(const XcdBarrier& b) {
;     ...
;     if (threadIdx.x == 0) {
;         unsigned* bar = b.bar;
;         __builtin_amdgcn_s_waitcnt(0);
;         unsigned nloc = b.st[0], nx = b.st[1];
;         if (nloc == 0u) { xcd_barrier_complete(bar, b.x, nloc, nx); b.st[0] = nloc; b.st[1] = nx; }
;         const unsigned old = xb_add(&bar[XB_XSUB(b.x)], 1u);
;         const unsigned gen = old / nloc;
;         if (old + 1u == (gen + 1u) * nloc) {
;             __builtin_amdgcn_fence(__ATOMIC_RELEASE, "agent");
;             asm volatile("s_waitcnt vmcnt(0)" ::: "memory");
;             const unsigned og = xb_add(&bar[XB_TOP], 1u);
;             const unsigned tg = og / nx;
;             if (og + 1u == (tg + 1u) * nx) xb_add(&bar[XB_TOPGEN], 1u);
.LBB0_228:
	s_waitcnt lgkmcnt(0)
	v_readfirstlane_b32 s8, v3
	v_readfirstlane_b32 s9, v1
	v_readlane_b32 s0, v252, 4
	s_lshl_b32 s0, s0, 8
	v_readlane_b32 s2, v252, 2
	v_readlane_b32 s3, v252, 3
	s_add_u32 s6, s2, s0
	s_addc_u32 s7, s3, 0
	s_mul_i32 s10, s8, 1
	s_mul_i32 s11, s9, 1
	v_mov_b32_e32 v4, 0x1000
	v_mov_b32_e32 v5, 1
	global_atomic_add v4, v4, v5, s[6:7] offset:1024 sc0
	v_mov_b32_e32 v1, 0x3400
	s_waitcnt vmcnt(0)
	v_readfirstlane_b32 s0, v4
	s_add_u32 s0, s0, 1
	s_cmp_lg_u32 s0, s10
	buffer_inv sc1
	s_cbranch_scc1 .Lgbw_0
	buffer_wbl2 sc1
	s_waitcnt vmcnt(0)
	global_atomic_add v1, v5, s[2:3]

; __device__ __forceinline__ int otid() { int t = threadIdx.x; asm volatile("" : "+v"(t)); return t; }
; template <bool GATHER, class Unit, class Epi, class Sched>
; __device__ __forceinline__ void gemm_phase(LAS unsigned char* lds, const int K, const Sched& S, const Epi& E) {
;     const int tid = otid(), wid = __builtin_amdgcn_readfirstlane(tid >> 6), lane = tid & 63, wr = wid >> 2, wc = wid & 3, fr = lane & 15, fq = lane >> 4;
;     const int nt = K / BK;
;     int R0, C0, R1, C1; stage_rc(tid * 16, R0, C0); stage_rc(tid * 16 + 8192, R1, C1);
;     const int Rb0 = (R0 & ~31) + 8 * ((R0 & 15) >> 2) + 4 * ((R0 >> 4) & 1) + (R0 & 3), Rb1 = (R1 & ~31) + 8 * ((R1 & 15) >> 2) + 4 * ((R1 >> 4) & 1) + (R1 & 3);
;     const unsigned voffB0 = (unsigned)(Rb0 * K + C0) * 2u, voffB1 = (unsigned)(Rb1 * K + C1) * 2u;
;     const size_t kstep = (size_t)(BK * 2);
;     const size_t hstepB = (size_t)HALF * K * 2;
;     const unsigned ldsw = (unsigned)wid * 1024u;
;     const int aoff = lds_byte(wr * 64 + fr, fq * 8), boff = lds_byte(wc * 32 + fr, fq * 8);
;     ...
;     Unit cur, nxt; int ui = 0;
;     if (!S.next(0, cur)) return;
;     f32x4 acc[2][2][4][2];
; #pragma unroll
;     for (int a = 0; a < 2; ++a)
; #pragma unroll
;         for (int b = 0; b < 2; ++b)
; #pragma unroll
;             for (int m = 0; m < 4; ++m)
; #pragma unroll
;                 for (int n = 0; n < 2; ++n) acc[a][b][m][n] = (f32x4){0.f, 0.f, 0.f, 0.f};
;     bf16x8 At[4][2], B0[2][2], B1[2][2];
;     const char* cA = S.a_base(cur); const char* cB = S.b_base(cur);
;     unsigned vA00 = S.a_voff(cur, R0, C0), vA01 = S.a_voff(cur, R1, C1), vA10 = S.a_voff(cur, HALF + R0, C0), vA11 = S.a_voff(cur, HALF + R1, C1);
;     unsigned vN00 = vA00, vN01 = vA01, vN10 = vA10, vN11 = vA11;
;     bool hi_on = !S.lo_only(cur);
;     FG_STAGE(FG_SB(0, 0), cB, voffB0, voffB1); FG_STAGE(FG_SB(0, 1), cB + hstepB, voffB0, voffB1); FG_STAGE(FG_SA(0, 0), cA, vA00, vA01); FG_STAGE(FG_SA(0, 1), cA, vA10, vA11);
;     if (wr == 1) FG_BAR;
;     FG_WAIT_V(2); FG_BAR;
;     FG_STAGE(FG_SB(1, 0), cB + kstep, voffB0, voffB1); FG_STAGE(FG_SA(1, 0), cA + kstep, vA00, vA01); FG_STAGE(FG_SB(1, 1), cB + hstepB + kstep, voffB0, voffB1);
;     FG_WAIT_V(6); FG_BAR;
;     __device__ __forceinline__ bool next(int i, DUnit& u) const {
;         long L = (long)i * G + c; const int nwg0 = nM * nN0, nwg1 = nM * nN1;
.Lgbd_0:
.LBB0_264:
	s_or_b64 exec, exec, s[4:5]
	s_mov_b32 s0, 30
	s_waitcnt lgkmcnt(0)
	s_barrier
	s_ashr_i32 s1, s0, 31
	s_lshl_b64 s[0:1], s[0:1], 3
	s_add_u32 s0, s80, s0
	s_addc_u32 s1, s81, s1
	s_load_dwordx2 s[6:7], s[0:1], 0x0
	v_mov_b32_e32 v1, v0
	s_mov_b32 s0, s78
	s_mov_b32 s1, s79
	s_waitcnt lgkmcnt(0)
	s_add_u32 s2, s6, 0x1be00000
	s_addc_u32 s3, s7, 0
	s_ashr_i32 s22, s1, 31
	v_mov_b32_e32 v1, v0
	s_cmpk_lt_i32 s1, 0x100
	s_cselect_b64 s[8:9], -1, 0
	s_cmpk_gt_i32 s1, 0xff
	v_readfirstlane_b32 s5, v1
	s_cbranch_scc1 .LBB0_280
	v_lshlrev_b32_e32 v2, 4, v1
	v_add_u32_e32 v3, 0x2000, v2
	v_ashrrev_i32_e32 v4, 31, v3
	v_lshrrev_b32_e32 v4, 22, v4
	v_add_u32_e32 v4, v3, v4
	v_ashrrev_i32_e32 v10, 10, v4
	v_mul_i32_i24_e32 v4, 0x400, v10
	v_sub_u32_e32 v3, v3, v4
	v_lshrrev_b32_e32 v4, 4, v3
	v_bitop3_b32 v3, v4, v3, 32 bitop3:0x6c
	v_ashrrev_i32_e32 v4, 31, v3
	v_lshrrev_b32_e32 v4, 26, v4
	v_add_u32_e32 v4, v3, v4
	v_lshlrev_b32_e32 v5, 3, v10
	v_ashrrev_i32_e32 v11, 6, v4
	v_and_b32_e32 v5, -16, v5
	v_add_u32_e32 v5, v11, v5
	v_and_b32_e32 v6, 3, v11
	s_mov_b32 s4, 0xfffe0
	v_lshlrev_b32_e32 v7, 1, v5
	v_lshrrev_b32_e32 v8, 2, v5
	v_and_or_b32 v6, v5, s4, v6
	v_and_b32_e32 v7, 24, v7
	v_and_b32_e32 v8, 4, v8
	v_and_b32_e32 v4, 0xc0, v4
	v_or3_b32 v6, v6, v7, v8
	v_lshlrev_b32_e32 v7, 5, v10
	v_sub_u32_e32 v3, v3, v4
	v_mov_b32_e32 v4, 1
	v_and_b32_e32 v12, 32, v7
	v_ashrrev_i16_sdwa v13, v4, sext(v3) dst_sel:DWORD dst_unused:UNUSED_PAD src0_sel:DWORD src1_sel:BYTE_0
	v_add_u32_sdwa v3, v12, sext(v13) dst_sel:DWORD dst_unused:UNUSED_PAD src0_sel:DWORD src1_sel:WORD_0
	v_lshlrev_b32_e32 v7, 1, v3
	v_lshl_add_u32 v130, v6, 12, v7
	v_bfe_i32 v6, v1, 27, 1
	v_lshrrev_b32_e32 v6, 22, v6
	v_add_u32_e32 v6, v2, v6
	v_and_b32_e32 v6, 0xfffffc00, v6
	v_sub_u32_e32 v2, v2, v6
	v_lshrrev_b32_e32 v6, 4, v2
	v_bitop3_b32 v6, v6, v2, 32 bitop3:0x6c
	v_ashrrev_i32_e32 v2, 31, v2
	v_lshrrev_b32_e32 v2, 26, v2
	v_add_u32_e32 v2, v6, v2
	v_ashrrev_i32_e32 v14, 6, v2
	v_ashrrev_i32_e32 v2, 31, v1
	v_lshrrev_b32_e32 v2, 26, v2
	v_add_u32_e32 v2, v1, v2
	v_ashrrev_i32_e32 v15, 6, v2
	v_lshlrev_b32_e32 v2, 3, v15
	v_and_b32_e32 v2, -16, v2
	s_add_u32 s23, s6, 0x100000
	v_add_u32_e32 v2, v14, v2
	v_and_b32_e32 v8, 3, v14
	s_addc_u32 s26, s7, 0
	v_and_or_b32 v8, v2, s4, v8
	s_lshr_b32 s4, s22, 29
	s_add_i32 s4, s1, s4
	s_ashr_i32 s10, s4, 3
	s_and_b32 s4, s4, -8
	s_sub_i32 s4, s1, s4
	s_lshr_b32 s11, s4, 31
	s_or_b32 s11, s11, 32
	s_mul_i32 s4, s11, s4
	s_add_i32 s4, s4, s10
	s_ashr_i32 s10, s4, 31
	s_lshr_b32 s10, s10, 27
	s_add_i32 s10, s4, s10
	s_ashr_i32 s11, s10, 5
	v_lshlrev_b32_e32 v9, 1, v2
	v_lshrrev_b32_e32 v16, 2, v2
	s_lshl_b32 s14, s11, 3
	v_and_b32_e32 v9, 24, v9
	v_and_b32_e32 v16, 4, v16
	s_sub_i32 s11, 64, s14
	v_or3_b32 v8, v8, v9, v16
	v_lshlrev_b32_e32 v9, 5, v15
	s_min_u32 s15, s11, 8
	s_andn2_b32 s10, s10, 31
	v_and_b32_e32 v16, 32, v9
	v_mul_i32_i24_e32 v9, 64, v14
	s_sub_i32 s16, s4, s10
	v_cvt_f32_ubyte0_e32 v18, s15
	v_sub_u32_e32 v6, v6, v9
	v_cvt_f32_i32_e32 v9, s16
	v_rcp_iflag_f32_e32 v19, v18
	v_ashrrev_i16_sdwa v17, v4, sext(v6) dst_sel:DWORD dst_unused:UNUSED_PAD src0_sel:DWORD src1_sel:BYTE_0
	v_add_u32_sdwa v4, v16, sext(v17) dst_sel:DWORD dst_unused:UNUSED_PAD src0_sel:DWORD src1_sel:WORD_0
	v_lshlrev_b32_e32 v6, 1, v4
	v_lshl_add_u32 v132, v8, 12, v6
	v_mul_f32_e32 v8, v9, v19
	v_trunc_f32_e32 v8, v8
	v_fma_f32 v9, -v8, v18, v9
	v_cvt_i32_f32_e32 v8, v8
	s_ashr_i32 s12, s5, 6
	s_ashr_i32 s4, s16, 30
	s_ashr_i32 s13, s5, 8
	s_lshl_b32 s27, s12, 10
	s_or_b32 s4, s4, 1
	v_cmp_ge_f32_e64 s[10:11], |v9|, v18
	s_and_b64 s[10:11], s[10:11], exec
	s_cselect_b32 s4, s4, 0
	v_readfirstlane_b32 s10, v8
	s_add_i32 s4, s10, s4
	s_mul_i32 s10, s4, s15
	s_sub_i32 s10, s16, s10
	s_sext_i32_i8 s10, s10
	s_add_i32 s42, s14, s10
	s_ashr_i32 s43, s42, 31
	s_lshl_b64 s[10:11], s[42:43], 20
	s_add_u32 s44, s2, s10
	s_addc_u32 s45, s3, s11
	s_bfe_i64 s[10:11], s[4:5], 0x80000
	s_lshl_b64 s[10:11], s[10:11], 20
	s_add_u32 s46, s23, s10
	s_addc_u32 s47, s26, s11
	s_add_i32 s28, s27, 0
	s_add_i32 m0, s28, 0x10000
	v_lshl_add_u32 v134, v2, 12, v6
	global_load_lds_dwordx4 v132, s[46:47]
	s_add_i32 m0, s28, 0x12000
	s_add_u32 s10, s46, 0x80000
	global_load_lds_dwordx4 v130, s[46:47]
	s_addc_u32 s11, s47, 0
	s_add_i32 m0, s28, 0x14000
	s_add_i32 s29, s28, 0x2000
	global_load_lds_dwordx4 v132, s[10:11]
	s_add_i32 m0, s28, 0x16000
	v_lshl_add_u32 v136, v5, 12, v7
	global_load_lds_dwordx4 v130, s[10:11]
	s_mov_b32 m0, s28
	v_lshl_add_u32 v2, v2, 11, v4
	v_mov_b32_e32 v18, 0x80000
	global_load_lds_dwordx4 v134, s[44:45]
	s_mov_b32 m0, s29
	s_add_i32 s30, s28, 0x4000
	v_lshl_add_u32 v138, v2, 1, v18
	v_lshl_add_u32 v2, v5, 11, v3
	global_load_lds_dwordx4 v136, s[44:45]
	s_mov_b32 m0, s30
	s_add_i32 s31, s28, 0x6000
	v_lshl_add_u32 v140, v2, 1, v18
	global_load_lds_dwordx4 v138, s[44:45]
	s_mov_b32 m0, s31
	v_mov_b32_e32 v143, 0
	global_load_lds_dwordx4 v140, s[44:45]
	v_mov_b32_e32 v133, v143
	v_mov_b32_e32 v131, v143
	v_mov_b32_e32 v135, v143
	v_mov_b32_e32 v137, v143
	s_cmp_eq_u32 s13, 1
	s_mov_b32 s33, 0
	v_lshl_add_u64 v[8:9], s[46:47], 0, v[132:133]
	v_lshl_add_u64 v[6:7], s[46:47], 0, v[130:131]
	v_lshl_add_u64 v[2:3], s[44:45], 0, v[134:135]
	s_cselect_b64 s[10:11], -1, 0
	s_cmp_lg_u32 s13, 1
	v_lshl_add_u64 v[4:5], s[44:45], 0, v[136:137]
	s_cbranch_scc1 .LBB0_267
	s_barrier

; __device__ __forceinline__ unsigned xb_add(unsigned* p, unsigned v) { return __hip_atomic_fetch_add(p, v, __ATOMIC_RELAXED, __HIP_MEMORY_SCOPE_AGENT); }
; __device__ __forceinline__ void xcd_barrier(const XcdBarrier& b) {
;     ...
;     if (threadIdx.x == 0) {
;         unsigned* bar = b.bar;
;         __builtin_amdgcn_s_waitcnt(0);
;         unsigned nloc = b.st[0], nx = b.st[1];
;         if (nloc == 0u) { xcd_barrier_complete(bar, b.x, nloc, nx); b.st[0] = nloc; b.st[1] = nx; }
;         const unsigned old = xb_add(&bar[XB_XSUB(b.x)], 1u);
;         const unsigned gen = old / nloc;
;         if (old + 1u == (gen + 1u) * nloc) {
;             __builtin_amdgcn_fence(__ATOMIC_RELEASE, "agent");
;             asm volatile("s_waitcnt vmcnt(0)" ::: "memory");
;             const unsigned og = xb_add(&bar[XB_TOP], 1u);
;             const unsigned tg = og / nx;
;             if (og + 1u == (tg + 1u) * nx) xb_add(&bar[XB_TOPGEN], 1u);
.LBB0_312:
	s_waitcnt lgkmcnt(0)
	v_readfirstlane_b32 s8, v3
	v_readfirstlane_b32 s9, v1
	v_readlane_b32 s0, v252, 4
	s_lshl_b32 s0, s0, 8
	v_readlane_b32 s2, v252, 2
	v_readlane_b32 s3, v252, 3
	s_add_u32 s6, s2, s0
	s_addc_u32 s7, s3, 0
	s_mul_i32 s10, s8, 2
	s_mul_i32 s11, s9, 2
	v_mov_b32_e32 v4, 0x1000
	v_mov_b32_e32 v5, 1
	global_atomic_add v4, v4, v5, s[6:7] offset:1024 sc0
	v_mov_b32_e32 v1, 0x3400
	s_waitcnt vmcnt(0)
	v_readfirstlane_b32 s0, v4
	s_add_u32 s0, s0, 1
	s_cmp_lg_u32 s0, s10
	buffer_inv sc1
	s_cbranch_scc1 .Lgbw_1
	buffer_wbl2 sc1
	s_waitcnt vmcnt(0)
	global_atomic_add v1, v5, s[2:3]

; #define INF(i) ((const float*)arg_ptr(i))
; __device__ __forceinline__ void ph_mla_prep() {
;     PH_BEGIN;
;     const bf16* Z = WSP(bf16, WS_Z); bf16* CQN = WSP(bf16, WS_CQN); bf16* CKVN = WSP(bf16, WS_CKVN); bf16* KR = WSP(bf16, WS_KR); const float* PK = WSP(float, WS_PK);
;     const float* gq = INF(4); const float* gkv = INF(5); const float* qkg = INF(8); const int* positions = (const int*)arg_ptr(1);
;     const f32x4 gq0 = *(const f32x4*)(gq + 8 * lane), gq1 = *(const f32x4*)(gq + 8 * lane + 4), gk0 = *(const f32x4*)(gkv + 8 * lane), gk1 = *(const f32x4*)(gkv + 8 * lane + 4); const float gr = qkg[192 + 128 + lane];
;     for (int t0 = gw; t0 < T; t0 += 8 * ngw) {
;         u32x4 rq_[8], rk_[8]; float pk_[8][4]; int pos_[8];
; #pragma unroll
;         for (int i = 0; i < 8; ++i) { const int t = t0 + i * ngw; if (t < T) { const bf16* zr = Z + (size_t)t * 1024;
;             rq_[i] = *(const u32x4*)(zr + 8 * lane); rk_[i] = *(const u32x4*)(zr + 512 + 8 * lane);
;             const float* pk = PK + (size_t)t * 64 + lane;
;             pk_[i][0] = pk[0]; pk_[i][1] = pk[(size_t)T * 64]; pk_[i][2] = pk[(size_t)2 * T * 64]; pk_[i][3] = pk[(size_t)3 * T * 64]; pos_[i] = positions[t]; } }
.Lgbd_1:
.LBB0_348:
	s_or_b64 exec, exec, s[4:5]
	s_mov_b32 s10, 30
	v_mov_b32_e32 v19, v0
	s_mov_b32 s2, s78
	s_mov_b32 s0, s79
	s_waitcnt lgkmcnt(0)
	s_barrier
	s_lshl_b32 s0, s0, 3
	v_ashrrev_i32_e32 v18, 6, v19
	v_add_u32_e32 v82, s0, v18
	s_movk_i32 s1, 0x4000
	s_mov_b32 s12, 4
	s_mov_b32 s8, 5
	s_mov_b32 s6, 8
	s_mov_b32 s4, 1
	v_cmp_gt_i32_e32 vcc, s1, v82
	s_and_saveexec_b64 s[20:21], vcc
	s_cbranch_execz .LBB0_379
	s_ashr_i32 s11, s10, 31
	s_lshl_b64 s[10:11], s[10:11], 3
	s_add_u32 s10, s80, s10
	s_addc_u32 s11, s81, s11
	s_ashr_i32 s13, s12, 31
	s_lshl_b32 s24, s2, 3
	s_lshl_b64 s[12:13], s[12:13], 3
	s_add_u32 s12, s80, s12
	s_addc_u32 s13, s81, s13
	s_ashr_i32 s9, s8, 31
	s_lshl_b64 s[8:9], s[8:9], 3
	s_add_u32 s8, s80, s8
	s_addc_u32 s9, s81, s9
	s_ashr_i32 s7, s6, 31
	s_lshl_b64 s[6:7], s[6:7], 3
	s_add_u32 s6, s80, s6
	s_addc_u32 s7, s81, s7
	s_load_dwordx2 s[34:35], s[10:11], 0x0
	s_load_dwordx2 s[14:15], s[12:13], 0x0
	s_load_dwordx2 s[16:17], s[8:9], 0x0
	s_load_dwordx2 s[18:19], s[6:7], 0x0
	s_ashr_i32 s5, s4, 31
	s_lshl_b64 s[4:5], s[4:5], 3
	v_and_b32_e32 v30, 63, v19
	s_add_u32 s4, s80, s4
	s_addc_u32 s5, s81, s5
	v_lshlrev_b32_e32 v20, 2, v30
	v_lshlrev_b32_e32 v22, 5, v30
	s_load_dwordx2 s[36:37], s[4:5], 0x0
	s_waitcnt lgkmcnt(0)
	global_load_dword v1, v20, s[18:19] offset:1280
	global_load_dwordx4 v[2:5], v22, s[16:17]
	global_load_dwordx4 v[6:9], v22, s[16:17] offset:16
	global_load_dwordx4 v[10:13], v22, s[14:15]
	global_load_dwordx4 v[14:17], v22, s[14:15] offset:16
	v_mov_b32_e32 v21, 0
	v_and_b32_e32 v19, 31, v19
	v_lshl_add_u64 v[22:23], s[34:35], 0, v[20:21]
	s_mov_b64 s[4:5], 0x6c700000
	v_cvt_f32_ubyte0_e32 v19, v19
	v_lshl_add_u64 v[84:85], v[22:23], 0, s[4:5]
	v_lshlrev_b32_e32 v22, 4, v30
	v_mov_b32_e32 v23, v21
	v_mov_b32_e32 v27, v21
	v_mul_f32_e32 v21, 0xbed49a78, v19
	s_mov_b32 s3, 0xc2fc0000
	v_lshl_add_u64 v[24:25], s[34:35], 0, v[22:23]
	v_mov_b32_e32 v23, 0x42800000
	v_cmp_gt_f32_e32 vcc, s3, v21
	s_mov_b64 s[8:9], 0x1fe00000
	v_lshl_add_u64 v[92:93], v[24:25], 0, s[8:9]
	v_cndmask_b32_e32 v21, 0, v23, vcc
	v_fmac_f32_e32 v21, 0xbed49a78, v19
	v_exp_f32_e32 v19, v21
	v_not_b32_e32 v21, 63
	v_cndmask_b32_e32 v21, 0, v21, vcc
	v_ashrrev_i32_e32 v83, 31, v82
	v_ldexp_f32 v158, v19, v21
	v_mbcnt_hi_u32_b32 v19, -1, v236
	v_and_b32_e32 v21, 64, v19
	v_add_u32_e32 v21, 64, v21
	v_xor_b32_e32 v23, 1, v19
	v_cmp_lt_i32_e32 vcc, v23, v21
	s_mov_b64 s[4:5], 0x2fe00000
	v_lshlrev_b32_e32 v26, 1, v30
	v_cndmask_b32_e32 v23, v19, v23, vcc
	v_lshlrev_b32_e32 v159, 2, v23
	v_xor_b32_e32 v23, 2, v19
	v_cmp_lt_i32_e32 vcc, v23, v21
	s_lshl_b32 s38, s2, 6
	v_lshl_add_u32 v165, s2, 4, v18
	v_cndmask_b32_e32 v23, v19, v23, vcc
	v_lshlrev_b32_e32 v160, 2, v23
	v_xor_b32_e32 v23, 4, v19
	v_cmp_lt_i32_e32 vcc, v23, v21
	v_lshl_add_u64 v[86:87], v[24:25], 0, s[4:5]
	s_mov_b64 s[4:5], 0x30e00000
	v_cndmask_b32_e32 v23, v19, v23, vcc
	v_lshlrev_b32_e32 v161, 2, v23
	v_xor_b32_e32 v23, 8, v19
	v_cmp_lt_i32_e32 vcc, v23, v21
	v_lshl_add_u64 v[28:29], s[34:35], 0, v[26:27]
	s_mov_b64 s[6:7], 0x31e00000
	v_cndmask_b32_e32 v23, v19, v23, vcc
	v_lshlrev_b32_e32 v162, 2, v23
	v_xor_b32_e32 v23, 16, v19
	v_cmp_lt_i32_e32 vcc, v23, v21
	s_ashr_i32 s25, s24, 31
	v_lshlrev_b64 v[102:103], 10, v[82:83]
	v_cndmask_b32_e32 v23, v19, v23, vcc
	v_lshlrev_b32_e32 v163, 2, v23
	v_xor_b32_e32 v23, 32, v19
	v_cmp_lt_i32_e32 vcc, v23, v21
	s_ashr_i32 s39, s38, 31
	v_lshlrev_b64 v[108:109], 8, v[82:83]
	v_cndmask_b32_e32 v19, v19, v23, vcc
	v_mad_u64_u32 v[94:95], s[8:9], s2, 24, v[18:19]
	v_mad_u64_u32 v[96:97], s[8:9], s2, 40, v[18:19]
	v_lshlrev_b32_e32 v164, 2, v19
	v_lshl_add_u32 v95, s2, 5, v18
	v_mad_u64_u32 v[98:99], s[8:9], s2, 48, v[18:19]
	v_mad_u64_u32 v[100:101], s[2:3], s2, 56, v[18:19]
	v_add_u32_e32 v97, s24, v18
	v_lshlrev_b64 v[18:19], 7, v[82:83]
	v_or_b32_e32 v18, v18, v26
	v_lshlrev_b64 v[110:111], 11, v[82:83]
	v_lshl_add_u64 v[88:89], v[24:25], 0, s[4:5]
	v_lshl_add_u64 v[90:91], v[28:29], 0, s[6:7]
	v_cmp_gt_u32_e64 s[4:5], 32, v30
	v_or_b32_e32 v102, v102, v22
	s_lshl_b64 s[40:41], s[38:39], 10
	v_lshl_add_u64 v[104:105], v[18:19], 0, s[6:7]
	s_lshl_b64 s[42:43], s[38:39], 7
	s_lshl_b64 s[44:45], s[24:25], 2
	v_lshl_add_u64 v[106:107], v[82:83], 2, s[36:37]
	s_lshl_b64 s[46:47], s[38:39], 2
	v_or_b32_e32 v108, v108, v20
	s_lshl_b64 s[48:49], s[38:39], 8
	v_or_b32_e32 v110, v110, v22
	s_lshl_b64 s[50:51], s[38:39], 11
	s_mov_b64 s[52:53], 0
	s_mov_b32 s2, 0x1fe00000
	s_mov_b32 s3, 0x6c700000
	s_mov_b32 s22, 0x6cb00000
	v_mov_b32_e32 v83, 0x358637bd
	s_mov_b32 s23, 0x2fe00000
	s_mov_b32 s25, 0x30e00000
	s_movk_i32 s26, 0x7fff
	s_movk_i32 s27, 0x3fff
	s_branch .LBB0_351

; __device__ __forceinline__ unsigned xb_add(unsigned* p, unsigned v) { return __hip_atomic_fetch_add(p, v, __ATOMIC_RELAXED, __HIP_MEMORY_SCOPE_AGENT); }
; __device__ __forceinline__ void xcd_barrier(const XcdBarrier& b) {
;     ...
;     if (threadIdx.x == 0) {
;         unsigned* bar = b.bar;
;         __builtin_amdgcn_s_waitcnt(0);
;         unsigned nloc = b.st[0], nx = b.st[1];
;         if (nloc == 0u) { xcd_barrier_complete(bar, b.x, nloc, nx); b.st[0] = nloc; b.st[1] = nx; }
;         const unsigned old = xb_add(&bar[XB_XSUB(b.x)], 1u);
;         const unsigned gen = old / nloc;
;         if (old + 1u == (gen + 1u) * nloc) {
;             __builtin_amdgcn_fence(__ATOMIC_RELEASE, "agent");
;             asm volatile("s_waitcnt vmcnt(0)" ::: "memory");
;             const unsigned og = xb_add(&bar[XB_TOP], 1u);
;             const unsigned tg = og / nx;
;             if (og + 1u == (tg + 1u) * nx) xb_add(&bar[XB_TOPGEN], 1u);
.LBB0_395:
	s_waitcnt lgkmcnt(0)
	v_readfirstlane_b32 s8, v3
	v_readfirstlane_b32 s9, v1
	v_readlane_b32 s0, v252, 4
	s_lshl_b32 s0, s0, 8
	v_readlane_b32 s2, v252, 2
	v_readlane_b32 s3, v252, 3
	s_add_u32 s6, s2, s0
	s_addc_u32 s7, s3, 0
	s_mul_i32 s10, s8, 3
	s_mul_i32 s11, s9, 3
	v_mov_b32_e32 v4, 0x1000
	v_mov_b32_e32 v5, 1
	global_atomic_add v4, v4, v5, s[6:7] offset:1024 sc0
	v_mov_b32_e32 v1, 0x3400
	s_waitcnt vmcnt(0)
	v_readfirstlane_b32 s0, v4
	s_add_u32 s0, s0, 1
	s_cmp_lg_u32 s0, s10
	buffer_inv sc1
	s_cbranch_scc1 .Lgbw_2
	buffer_wbl2 sc1
	s_waitcnt vmcnt(0)
	global_atomic_add v1, v5, s[2:3]

; #define LAS __attribute__((address_space(3)))
;     __device__ __forceinline__ bool next(int i, SkUnit& u) const { const int L = i * G + c; if (L >= (T / 256) * 4) return false; u.pm = L >> 2; u.ks = L & 3; return true; }
;     __device__ __forceinline__ bool next(int i, DUnit& u) const {
;         long L = (long)i * G + c; const int nwg0 = nM * nN0, nwg1 = nM * nN1;
;         int nN, nwg; if (L < nwg0) { u.p = 0; nN = nN0; nwg = nwg0; } else { L -= nwg0; if (L >= nwg1) return false; u.p = 1; nN = nN1; nwg = nwg1; }
; __device__ __forceinline__ void ph_gemm_qkv(LAS unsigned char* lds) {
;     PH_BEGIN;
;     bf16* QL = WSP(bf16, WS_QL); bf16* KVL = WSP(bf16, WS_KVL);
;     fg::DenseSched S{WSP(bf16, WS_CQN), WSP(bf16, WS_W_UQT), 12, WSP(bf16, WS_CKVN), WSP(bf16, WS_W_UKVT), 16, 512, G, bx};
.Lgbd_2:
.LBB0_431:
	s_or_b64 exec, exec, s[4:5]
	s_mov_b32 s0, 30
	s_waitcnt lgkmcnt(0)
	s_barrier
	s_ashr_i32 s1, s0, 31
	s_lshl_b64 s[0:1], s[0:1], 3
	s_add_u32 s4, s80, s0
	v_mov_b32_e32 v1, v0
	s_mov_b32 s0, s78
	s_mov_b32 s6, s79
	s_mov_b32 s2, 8
	s_addc_u32 s5, s81, s1
	s_ashr_i32 s3, s2, 31
	s_lshl_b64 s[2:3], s[2:3], 3
	s_add_u32 s10, s80, s2
	s_addc_u32 s11, s81, s3
	s_ashr_i32 s1, s6, 31
	s_cmpk_lt_i32 s6, 0x300
	v_mov_b32_e32 v1, v0
	s_cselect_b64 s[12:13], -1, 0
	s_and_b64 vcc, exec, s[12:13]
	v_readfirstlane_b32 s14, v1
	s_cbranch_vccnz .LBB0_434
	s_add_u32 s8, s6, 0xfffffd00
	s_addc_u32 s9, s1, -1
	v_mov_b64_e32 v[2:3], 0x400
	v_cmp_lt_u64_e64 s[12:13], s[8:9], v[2:3]
	s_mov_b32 s71, 1
	s_movk_i32 s2, 0x80
	s_andn2_b64 vcc, exec, s[12:13]
	s_cbranch_vccz .LBB0_435

; __device__ __forceinline__ unsigned xb_add(unsigned* p, unsigned v) { return __hip_atomic_fetch_add(p, v, __ATOMIC_RELAXED, __HIP_MEMORY_SCOPE_AGENT); }
; __device__ __forceinline__ void xcd_barrier(const XcdBarrier& b) {
;     ...
;     if (threadIdx.x == 0) {
;         unsigned* bar = b.bar;
;         __builtin_amdgcn_s_waitcnt(0);
;         unsigned nloc = b.st[0], nx = b.st[1];
;         if (nloc == 0u) { xcd_barrier_complete(bar, b.x, nloc, nx); b.st[0] = nloc; b.st[1] = nx; }
;         const unsigned old = xb_add(&bar[XB_XSUB(b.x)], 1u);
;         const unsigned gen = old / nloc;
;         if (old + 1u == (gen + 1u) * nloc) {
;             __builtin_amdgcn_fence(__ATOMIC_RELEASE, "agent");
;             asm volatile("s_waitcnt vmcnt(0)" ::: "memory");
;             const unsigned og = xb_add(&bar[XB_TOP], 1u);
;             const unsigned tg = og / nx;
;             if (og + 1u == (tg + 1u) * nx) xb_add(&bar[XB_TOPGEN], 1u);
.LBB0_489:
	s_waitcnt lgkmcnt(0)
	v_readfirstlane_b32 s8, v3
	v_readfirstlane_b32 s9, v1
	v_readlane_b32 s0, v252, 4
	s_lshl_b32 s0, s0, 8
	v_readlane_b32 s2, v252, 2
	v_readlane_b32 s3, v252, 3
	s_add_u32 s6, s2, s0
	s_addc_u32 s7, s3, 0
	s_mul_i32 s10, s8, 4
	s_mul_i32 s11, s9, 4
	v_mov_b32_e32 v4, 0x1000
	v_mov_b32_e32 v5, 1
	global_atomic_add v4, v4, v5, s[6:7] offset:1024 sc0
	v_mov_b32_e32 v1, 0x3400
	s_waitcnt vmcnt(0)
	v_readfirstlane_b32 s0, v4
	s_add_u32 s0, s0, 1
	s_cmp_lg_u32 s0, s10
	buffer_inv sc1
	s_cbranch_scc1 .Lgbw_3
	buffer_wbl2 sc1
	s_waitcnt vmcnt(0)
	global_atomic_add v1, v5, s[2:3]

; template <int layer>
; __device__ __forceinline__ void attn_phase(LAS unsigned char* lds) {
;     PH_BEGIN;
;     constexpr int DK = layer == 0 ? 192 : 128, NQ = DK / 16, CPR = DK / 8, NKC = KVB * CPR / NTHREADS;
;     constexpr int SHM_K = KVB * DK * 2;
;     constexpr int OFF_V = 0, OFF_K = 2 * SHM_V, OFF_WS = OFF_K + 2 * SHM_K, OFF_CB = OFF_WS + NWAVES * 256, OFF_CV = 86016;
;     static_assert(OFF_CB + 512 <= OFF_CV && OFF_CV + NWAVES * 8192 <= LDS_BARW, "attention LDS map");
;     constexpr float C2 = (layer == 0 ? 0.07216878364870322f : 0.08838834764831845f) * 1.4426950408889634f;
;     constexpr int QLD = layer == 0 ? 3072 : 8192, QHS = layer == 0 ? 192 : 128, KLD = layer == 0 ? 4096 : 8192, KC0 = layer == 0 ? 0 : 2048, KHS = layer == 0 ? 256 : 128, VC0 = layer == 0 ? 128 : 4096;
;     const bf16* Qs = layer == 0 ? WSP(bf16, WS_QL) : WSP(bf16, WS_Z); const bf16* Ks = layer == 0 ? WSP(bf16, WS_KVL) : WSP(bf16, WS_Z); const bf16* KRs = WSP(bf16, WS_KR); bf16* Ob = WSP(bf16, WS_O);
;     const float* qkg = INF(layer == 0 ? 8 : 20); const int* positions = (const int*)arg_ptr(1);
;     const float* CBg = WSP(float, WS_C); const bf16* Zg = WSP(bf16, WS_Z);
;     const int wid = __builtin_amdgcn_readfirstlane(tid >> 6), r32 = lane & 31, hi = lane >> 5;
;     auto koff_n = [](int tk, int j) { const int ci = j * 256 + tk, row = ci >> 4, pc = ci & 15, lc = pc ^ (row & 7); return (unsigned)(row * KLD + lc * 8) * 2u; };
;     auto koff_r = [](int tk, int j) { const int ci = j * 256 + tk, row = ci >> 3, pc = ci & 7, lc = pc ^ (row & 7); return (unsigned)(row * 64 + lc * 8) * 2u; };
;     auto voff_f = [](int tk, int j) { const int ci = j * 256 + tk, st = ci >> 5, w = ci & 31, kk = (st >> 2) * 8 + (w >> 2), key = (kk & ~0xC) | ((kk & 4) << 1) | ((kk & 8) >> 1), c = (st & 3) * 32 + (w & 3) * 8;
;         return (unsigned)(key * KLD + c) * 2u; };
;     const int tkp = (tid - 256) & 255; const unsigned kof0 = koff_n(tkp, 0), vof0 = voff_f(tkp, 0), rof0 = koff_r(tkp, 0);
;     const int kbn = r32 * 256 + ((hi * 16) ^ ((r32 & 7) << 4)), kbr0 = 16384 + r32 * 128 + ((hi * 16) ^ ((r32 & 7) << 4));
;     const unsigned ldsb = (unsigned)(uintptr_t)lds;
;     const int vb0 = (int)(unsigned)(uintptr_t)(lds + OFF_V) + v_rd_base(lane);
;     LAS float* wsl = (LAS float*)(lds + OFF_WS) + wid * 64; LAS float* li_l = wsl; LAS float* al_l = wsl + 32;
.Lgbd_3:
.LBB0_525:
	s_or_b64 exec, exec, s[4:5]
	s_mov_b32 s0, 30
	s_waitcnt lgkmcnt(0)
	s_barrier
	s_ashr_i32 s1, s0, 31
	s_lshl_b64 s[0:1], s[0:1], 3
	s_add_u32 s0, s80, s0
	s_addc_u32 s1, s81, s1
	v_mov_b32_e32 v4, v0
	s_load_dwordx2 s[4:5], s[0:1], 0x0
	s_mov_b32 s9, s78
	v_readfirstlane_b32 s0, v4
	s_mov_b32 s28, s79
	s_mov_b32 s8, 8
	s_mov_b32 s6, 1
	s_ashr_i32 s14, s0, 6
	s_mov_b32 s0, 15
	s_ashr_i32 s1, s0, 31
	s_lshl_b64 s[0:1], s[0:1], 3
	s_add_u32 s0, s80, s0
	s_addc_u32 s1, s81, s1
	s_load_dwordx2 s[10:11], s[0:1], 0x0
	s_mov_b32 s0, 16
	s_ashr_i32 s1, s0, 31
	s_lshl_b64 s[0:1], s[0:1], 3
	s_add_u32 s0, s80, s0
	s_addc_u32 s1, s81, s1
	s_load_dwordx2 s[12:13], s[0:1], 0x0
	s_waitcnt lgkmcnt(0)
	s_add_u32 s0, s4, 0x3e00000
	s_addc_u32 s1, s5, 0
	s_add_u32 s2, s4, 0x13e00000
	s_addc_u32 s3, s5, 0
	s_lshl_b32 s7, s28, 2
	s_add_i32 s15, s14, s7
	s_lshl_b32 s7, s14, 14
	s_and_b32 s7, s7, 0xc000
	v_writelane_b32 v252, s9, 9
	s_add_i32 s24, s7, 0
	s_lshl_b32 s22, s9, 2
	s_add_i32 s23, s24, 0x15000
	v_writelane_b32 v252, s79, 10
	s_mov_b32 s29, 0
	s_cmpk_gt_i32 s28, 0x1ff
	s_mov_b32 s33, -1
	v_writelane_b32 v252, s80, 11
	s_nop 1
	v_writelane_b32 v252, s81, 12
	s_cbranch_scc1 .LBB0_583
	s_add_u32 s7, s4, 0x64300000
	v_bfe_u32 v1, v4, 4, 4
	v_and_b32_e32 v3, 15, v4
	v_writelane_b32 v252, s7, 13
	s_addc_u32 s7, s5, 0
	v_bitop3_b32 v3, v1, v3, 15 bitop3:0x6c
	v_lshlrev_b32_e32 v1, 13, v1
	v_writelane_b32 v252, s7, 14
	s_add_u32 s7, s4, 0x31e00000
	v_lshl_or_b32 v1, v3, 4, v1
	v_lshrrev_b32_e32 v3, 5, v4
	v_lshrrev_b32_e32 v7, 1, v4
	v_writelane_b32 v252, s7, 15
	s_addc_u32 s7, s5, 0
	v_and_b32_e32 v3, 4, v3
	v_bfe_u32 v6, v4, 2, 2
	v_and_b32_e32 v7, 8, v7
	v_writelane_b32 v252, s7, 16
	s_add_u32 s7, s4, 0x42000000
	v_or3_b32 v3, v6, v7, v3
	v_and_b32_e32 v6, 0x60, v4
	v_lshlrev_b32_e32 v7, 3, v4
	v_writelane_b32 v252, s7, 17
	s_addc_u32 s7, s5, 0
	s_ashr_i32 s9, s8, 31
	v_and_or_b32 v6, v7, 24, v6
	s_lshl_b64 s[8:9], s[8:9], 3
	v_lshlrev_b32_e32 v6, 1, v6
	s_add_u32 s8, s80, s8
	v_lshl_or_b32 v181, v3, 13, v6
	v_bfe_u32 v3, v4, 3, 5
	v_writelane_b32 v252, s7, 18
	s_addc_u32 s9, s81, s9
	s_ashr_i32 s7, s6, 31
	v_lshrrev_b32_e32 v6, 1, v3
	v_xor_b32_e32 v6, v6, v4
	s_lshl_b64 s[6:7], s[6:7], 3
	v_bfe_u32 v5, v4, 5, 1
	v_lshlrev_b32_e32 v3, 7, v3
	v_lshlrev_b32_e32 v6, 4, v6
	s_movk_i32 s62, 0x70
	s_add_u32 s6, s80, s6
	v_and_b32_e32 v180, 31, v4
	v_and_or_b32 v188, v6, s62, v3
	v_bitop3_b32 v3, v5, v4, 15 bitop3:0x78
	s_addc_u32 s7, s81, s7
	s_load_dwordx2 s[16:17], s[8:9], 0x0
	s_load_dwordx2 s[18:19], s[6:7], 0x0
	v_lshlrev_b32_e32 v3, 4, v3
	v_lshlrev_b32_e32 v6, 7, v180
	s_movk_i32 s6, 0x4000
	v_and_b32_e32 v2, 63, v4
	v_lshl_or_b32 v189, v180, 8, v3
	v_or3_b32 v190, v3, v6, s6
	v_bfe_u32 v226, v4, 1, 3
	v_xor_b32_e32 v226, v226, v5
	v_lshlrev_b32_e32 v226, 4, v226
	v_or3_b32 v190, v226, v6, s6
	v_or_b32_e32 v189, 0x8000, v189
	v_or_b32_e32 v190, 0x8000, v190
	v_xor_b32_e32 v226, 32, v189
	v_xor_b32_e32 v227, 64, v189
	v_xor_b32_e32 v228, 0x60, v189
	v_xor_b32_e32 v232, 0x80, v189
	v_xor_b32_e32 v233, 0xa0, v189
	v_xor_b32_e32 v234, 0xc0, v189
	v_xor_b32_e32 v235, 0xe0, v189
	v_xor_b32_e32 v229, 32, v190
	v_xor_b32_e32 v230, 64, v190
	v_xor_b32_e32 v231, 0x60, v190
	v_lshlrev_b32_e32 v3, 4, v4
	v_lshlrev_b32_e32 v2, 3, v2
	v_and_b32_e32 v3, 0xc0, v3
	v_lshlrev_b32_e32 v6, 1, v4
	v_and_or_b32 v3, v2, 24, v3
	v_and_b32_e32 v6, 32, v6
	v_and_b32_e32 v2, 0x100, v2
	v_or3_b32 v2, v3, v6, v2
	v_add_u32_e32 v191, 0, v2
	v_mov_b32_e32 v3, 0
	v_lshlrev_b32_e32 v2, 4, v5
	v_lshlrev_b32_e32 v8, 3, v5
	v_lshl_add_u64 v[6:7], s[4:5], 0, v[2:3]
	s_mov_b64 s[4:5], 0x5e300000
	v_lshl_add_u64 v[182:183], v[6:7], 0, s[4:5]
	v_and_b32_e32 v2, 32, v4
	v_cvt_f32_ubyte0_e32 v4, v8
	v_or_b32_e32 v7, 1, v8
	s_waitcnt lgkmcnt(0)
; #define LAS __attribute__((address_space(3)))
; __device__ __forceinline__ int v_rd_base(int lane) { return ((lane & 3) << 3) | (((lane >> 2) & 3) << 6) | (((lane >> 4) & 1) << 5) | (((lane >> 5) & 1) << 8); }
; template <int layer>
; __device__ __forceinline__ void attn_phase(LAS unsigned char* lds) {
;     ...
;     const int wid = __builtin_amdgcn_readfirstlane(tid >> 6), r32 = lane & 31, hi = lane >> 5;
;     auto koff_n = [](int tk, int j) { const int ci = j * 256 + tk, row = ci >> 4, pc = ci & 15, lc = pc ^ (row & 7); return (unsigned)(row * KLD + lc * 8) * 2u; };
;     auto koff_r = [](int tk, int j) { const int ci = j * 256 + tk, row = ci >> 3, pc = ci & 7, lc = pc ^ (row & 7); return (unsigned)(row * 64 + lc * 8) * 2u; };
;     auto voff_f = [](int tk, int j) { const int ci = j * 256 + tk, st = ci >> 5, w = ci & 31, kk = (st >> 2) * 8 + (w >> 2), key = (kk & ~0xC) | ((kk & 4) << 1) | ((kk & 8) >> 1), c = (st & 3) * 32 + (w & 3) * 8;
;         return (unsigned)(key * KLD + c) * 2u; };
;     const int tkp = (tid - 256) & 255; const unsigned kof0 = koff_n(tkp, 0), vof0 = voff_f(tkp, 0), rof0 = koff_r(tkp, 0);
;     const int kbn = r32 * 256 + ((hi * 16) ^ ((r32 & 7) << 4)), kbr0 = 16384 + r32 * 128 + ((hi * 16) ^ ((r32 & 7) << 4));
;     const unsigned ldsb = (unsigned)(uintptr_t)lds;
;     const int vb0 = (int)(unsigned)(uintptr_t)(lds + OFF_V) + v_rd_base(lane);
;     LAS float* wsl = (LAS float*)(lds + OFF_WS) + wid * 64; LAS float* li_l = wsl; LAS float* al_l = wsl + 32;
;     ...
;                             for (int e = 0; e < 2; ++e) { const int j = 2 * jj + e; const int i = c * 16 + hi * 8 + j;
;                                 const float freq = exp2f(-(float)i * (13.287712379549449f / 32.0f)); float rev = pos * freq * 0.15915494309189535f; rev -= floorf(rev);
	v_lshl_add_u64 v[184:185], s[16:17], 0, v[2:3]
	v_mul_i32_i24_e32 v2, -4, v5
	v_mul_f32_e32 v5, 0xbed49a78, v4
	s_mov_b32 s6, 0xc2fc0000
	v_cvt_f32_ubyte0_e32 v7, v7
	v_mov_b32_e32 v6, 0x42800000
	v_cmp_gt_f32_e32 vcc, s6, v5
	v_mul_f32_e32 v9, 0xbed49a78, v7
	v_cmp_gt_f32_e64 s[4:5], s6, v9
	v_cndmask_b32_e32 v5, 0, v6, vcc
	v_fmac_f32_e32 v5, 0xbed49a78, v4
	v_cndmask_b32_e64 v9, 0, v6, s[4:5]
	v_exp_f32_e32 v4, v5
	v_fmac_f32_e32 v9, 0xbed49a78, v7
	v_exp_f32_e32 v7, v9
	v_not_b32_e32 v5, 63
	v_cndmask_b32_e32 v9, 0, v5, vcc
	v_ldexp_f32 v192, v4, v9
	v_cndmask_b32_e64 v4, 0, v5, s[4:5]
	v_ldexp_f32 v193, v7, v4
	v_or_b32_e32 v4, 2, v8
	v_cvt_f32_ubyte0_e32 v4, v4
	v_mul_f32_e32 v7, 0xbed49a78, v4
	v_cmp_gt_f32_e32 vcc, s6, v7
	s_lshl_b32 s7, s14, 5
	v_writelane_b32 v252, s18, 19
	v_cndmask_b32_e32 v7, 0, v6, vcc
	v_fmac_f32_e32 v7, 0xbed49a78, v4
	v_exp_f32_e32 v4, v7
	v_or_b32_e32 v7, 3, v8
	v_cvt_f32_ubyte0_e32 v7, v7
	v_mul_f32_e32 v9, 0xbed49a78, v7
	v_cmp_gt_f32_e64 s[4:5], s6, v9
	s_cmp_gt_i32 s14, 3
	v_writelane_b32 v252, s19, 20
	v_cndmask_b32_e64 v9, 0, v6, s[4:5]
	v_fmac_f32_e32 v9, 0xbed49a78, v7
	v_exp_f32_e32 v7, v9
	v_cndmask_b32_e32 v9, 0, v5, vcc
	v_ldexp_f32 v194, v4, v9
	v_cndmask_b32_e64 v4, 0, v5, s[4:5]
	v_ldexp_f32 v195, v7, v4
	v_or_b32_e32 v4, 4, v8
	v_cvt_f32_ubyte0_e32 v4, v4
	v_mul_f32_e32 v7, 0xbed49a78, v4
	v_cmp_gt_f32_e32 vcc, s6, v7
	s_cselect_b64 s[18:19], -1, 0
	s_lshl_b32 s64, s14, 10
	v_cndmask_b32_e32 v7, 0, v6, vcc
	v_fmac_f32_e32 v7, 0xbed49a78, v4
	v_exp_f32_e32 v4, v7
	v_or_b32_e32 v7, 5, v8
	v_cvt_f32_ubyte0_e32 v7, v7
	v_mul_f32_e32 v9, 0xbed49a78, v7
	v_cmp_gt_f32_e64 s[4:5], s6, v9
	s_add_i32 s64, s64, 0
	s_add_i32 s65, s64, 0x7000
	v_cndmask_b32_e64 v9, 0, v6, s[4:5]
	v_fmac_f32_e32 v9, 0xbed49a78, v7
	v_exp_f32_e32 v7, v9
	v_cndmask_b32_e32 v9, 0, v5, vcc
	v_ldexp_f32 v196, v4, v9
	v_cndmask_b32_e64 v4, 0, v5, s[4:5]
	v_ldexp_f32 v197, v7, v4
	v_or_b32_e32 v4, 6, v8
	v_cvt_f32_ubyte0_e32 v4, v4
	v_mul_f32_e32 v7, 0xbed49a78, v4
	v_cmp_gt_f32_e32 vcc, s6, v7
	s_add_i32 s66, s64, 0xb000
	s_add_i32 s67, s64, 0xfffff000
	v_cndmask_b32_e32 v7, 0, v6, vcc
	v_fmac_f32_e32 v7, 0xbed49a78, v4
	v_exp_f32_e32 v4, v7
	v_or_b32_e32 v7, 7, v8
	v_cvt_f32_ubyte0_e32 v7, v7
	v_mul_f32_e32 v9, 0xbed49a78, v7
	v_cmp_gt_f32_e64 s[4:5], s6, v9
	s_add_i32 s68, s64, 0xd000
	s_add_i32 s69, s64, 0x11000
	v_cndmask_b32_e64 v9, 0, v6, s[4:5]
	v_fmac_f32_e32 v9, 0xbed49a78, v7
	v_exp_f32_e32 v7, v9
	v_cndmask_b32_e32 v9, 0, v5, vcc
	v_ldexp_f32 v198, v4, v9
	v_cndmask_b32_e64 v4, 0, v5, s[4:5]
	v_ldexp_f32 v199, v7, v4
	v_or_b32_e32 v4, 16, v8
	v_cvt_f32_ubyte0_e32 v4, v4
	v_mul_f32_e32 v7, 0xbed49a78, v4
	v_cmp_gt_f32_e32 vcc, s6, v7
	s_add_i32 s70, s64, 0x3000
	v_writelane_b32 v252, s14, 21
	v_cndmask_b32_e32 v7, 0, v6, vcc
	v_fmac_f32_e32 v7, 0xbed49a78, v4
	v_exp_f32_e32 v4, v7
	v_or_b32_e32 v7, 17, v8
	v_cvt_f32_ubyte0_e32 v7, v7
	v_mul_f32_e32 v9, 0xbed49a78, v7
	v_cmp_gt_f32_e64 s[4:5], s6, v9
	s_cmp_lt_i32 s14, 4
	s_movk_i32 s61, 0x60
	v_cndmask_b32_e64 v9, 0, v6, s[4:5]
	v_fmac_f32_e32 v9, 0xbed49a78, v7
	v_exp_f32_e32 v7, v9
	v_cndmask_b32_e32 v9, 0, v5, vcc
	v_ldexp_f32 v200, v4, v9
	v_cndmask_b32_e64 v4, 0, v5, s[4:5]
	v_ldexp_f32 v201, v7, v4
	v_or_b32_e32 v4, 18, v8
	v_cvt_f32_ubyte0_e32 v4, v4
	v_mul_f32_e32 v7, 0xbed49a78, v4
	v_cmp_gt_f32_e32 vcc, s6, v7
	s_cselect_b64 s[20:21], -1, 0
	s_add_i32 s71, s24, 0x17000
	v_cndmask_b32_e32 v7, 0, v6, vcc
	v_fmac_f32_e32 v7, 0xbed49a78, v4
	v_exp_f32_e32 v4, v7
	v_or_b32_e32 v7, 19, v8
	v_cvt_f32_ubyte0_e32 v7, v7
	v_mul_f32_e32 v9, 0xbed49a78, v7
	v_cmp_gt_f32_e64 s[4:5], s6, v9
	s_mov_b32 s72, 0x42800000
	v_or_b32_e32 v208, 0x20000, v1
	v_cndmask_b32_e64 v9, 0, v6, s[4:5]
	v_fmac_f32_e32 v9, 0xbed49a78, v7
	v_exp_f32_e32 v7, v9
	v_cndmask_b32_e32 v9, 0, v5, vcc
	v_ldexp_f32 v202, v4, v9
	v_cndmask_b32_e64 v4, 0, v5, s[4:5]
	v_ldexp_f32 v203, v7, v4
	v_or_b32_e32 v4, 20, v8
	v_cvt_f32_ubyte0_e32 v4, v4
	v_mul_f32_e32 v7, 0xbed49a78, v4
	v_cmp_gt_f32_e32 vcc, s6, v7
	s_add_i32 s73, s64, 0x8000
	v_or_b32_e32 v209, 0x40000, v1
	v_cndmask_b32_e32 v7, 0, v6, vcc
	v_fmac_f32_e32 v7, 0xbed49a78, v4
	v_exp_f32_e32 v4, v7
	v_or_b32_e32 v7, 21, v8
	v_cvt_f32_ubyte0_e32 v7, v7
	v_mul_f32_e32 v9, 0xbed49a78, v7
	v_cmp_gt_f32_e64 s[4:5], s6, v9
	s_add_i32 s74, s64, 0x9000
	v_or_b32_e32 v210, 0x60000, v1
	v_cndmask_b32_e64 v9, 0, v6, s[4:5]
	v_fmac_f32_e32 v9, 0xbed49a78, v7
	v_exp_f32_e32 v7, v9
	v_cndmask_b32_e32 v9, 0, v5, vcc
	v_ldexp_f32 v204, v4, v9
	v_cndmask_b32_e64 v4, 0, v5, s[4:5]
	v_ldexp_f32 v205, v7, v4
	v_or_b32_e32 v4, 22, v8
	v_cvt_f32_ubyte0_e32 v4, v4
	v_mul_f32_e32 v7, 0xbed49a78, v4
	v_cmp_gt_f32_e32 vcc, s6, v7
	s_add_i32 s75, s64, 0xa000
	v_or_b32_e32 v211, 0x1000, v188
	v_cndmask_b32_e32 v7, 0, v6, vcc
	v_fmac_f32_e32 v7, 0xbed49a78, v4
	v_exp_f32_e32 v4, v7
	v_or_b32_e32 v7, 23, v8
	v_cvt_f32_ubyte0_e32 v7, v7
	v_mul_f32_e32 v8, 0xbed49a78, v7
	v_cmp_gt_f32_e64 s[4:5], s6, v8
	s_add_i32 s76, s64, 0xc000
	v_or_b32_e32 v212, 0x20000, v181
	v_cndmask_b32_e64 v6, 0, v6, s[4:5]
	v_fmac_f32_e32 v6, 0xbed49a78, v7
	v_exp_f32_e32 v6, v6
	v_cndmask_b32_e32 v7, 0, v5, vcc
	v_ldexp_f32 v206, v4, v7
	v_cndmask_b32_e64 v4, 0, v5, s[4:5]
	v_ldexp_f32 v207, v6, v4
	v_or_b32_e32 v213, 0x40000, v181
	s_add_i32 s77, s64, 0x1000
	v_or_b32_e32 v214, 0x60000, v181
	s_add_i32 s78, s64, 0x2000
	s_add_i32 s79, s64, 0xe000
	s_add_i32 s80, s64, 0xf000
	s_add_i32 s81, s64, 0x10000
	s_add_i32 s82, s64, 0x12000
	s_add_i32 s83, s64, 0x4000
	s_add_i32 s84, s64, 0x5000
	s_add_i32 s85, s64, 0x6000
	s_add_i32 s86, s24, 0x15400
	s_add_i32 s87, s24, 0x15800
	s_add_i32 s88, s24, 0x15c00
	s_add_i32 s89, s24, 0x16000
	s_add_i32 s90, s24, 0x16400
	s_add_i32 s91, s24, 0x16800
	s_add_i32 s92, s24, 0x16c00
	s_add_i32 s93, s24, 0x17400
	s_add_i32 s94, s24, 0x17800
	s_add_i32 s95, s24, 0x17c00
	s_add_i32 s96, s24, 0x18000
	s_add_i32 s97, s24, 0x18400
	s_add_i32 s27, s24, 0x18800
	v_writelane_b32 v252, s24, 22
	s_add_i32 s26, s24, 0x18c00
	v_add3_u32 v215, v2, s7, v180
	v_mov_b32_e32 v216, 0x358637bd
	s_movk_i32 s30, 0x3ff
	s_movk_i32 s31, 0x50
	v_mov_b32_e32 v217, 0x1800
	v_mov_b32_e32 v218, 0x10000
	v_mov_b32_e32 v219, 0xff800000
	v_writelane_b32 v252, s7, 23

; __device__ __forceinline__ unsigned xb_add(unsigned* p, unsigned v) { return __hip_atomic_fetch_add(p, v, __ATOMIC_RELAXED, __HIP_MEMORY_SCOPE_AGENT); }
; __device__ __forceinline__ void xcd_barrier(const XcdBarrier& b) {
;     ...
;     if (threadIdx.x == 0) {
;         unsigned* bar = b.bar;
;         __builtin_amdgcn_s_waitcnt(0);
;         unsigned nloc = b.st[0], nx = b.st[1];
;         if (nloc == 0u) { xcd_barrier_complete(bar, b.x, nloc, nx); b.st[0] = nloc; b.st[1] = nx; }
;         const unsigned old = xb_add(&bar[XB_XSUB(b.x)], 1u);
;         const unsigned gen = old / nloc;
;         if (old + 1u == (gen + 1u) * nloc) {
;             __builtin_amdgcn_fence(__ATOMIC_RELEASE, "agent");
;             asm volatile("s_waitcnt vmcnt(0)" ::: "memory");
;             const unsigned og = xb_add(&bar[XB_TOP], 1u);
;             const unsigned tg = og / nx;
;             if (og + 1u == (tg + 1u) * nx) xb_add(&bar[XB_TOPGEN], 1u);
.LBB0_605:
	s_waitcnt lgkmcnt(0)
	v_readfirstlane_b32 s8, v3
	v_readfirstlane_b32 s9, v1
	v_readlane_b32 s0, v252, 4
	s_lshl_b32 s0, s0, 8
	v_readlane_b32 s2, v252, 2
	v_readlane_b32 s3, v252, 3
	s_add_u32 s6, s2, s0
	s_addc_u32 s7, s3, 0
	s_mul_i32 s10, s8, 5
	s_mul_i32 s11, s9, 5
	v_mov_b32_e32 v4, 0x1000
	v_mov_b32_e32 v5, 1
	global_atomic_add v4, v4, v5, s[6:7] offset:1024 sc0
	v_mov_b32_e32 v1, 0x3400
	s_waitcnt vmcnt(0)
	v_readfirstlane_b32 s0, v4
	s_add_u32 s0, s0, 1
	s_cmp_lg_u32 s0, s10
	buffer_inv sc1
	s_cbranch_scc1 .Lgbw_4
	buffer_wbl2 sc1
	s_waitcnt vmcnt(0)
	global_atomic_add v1, v5, s[2:3]

; #define LAS __attribute__((address_space(3)))
;     __device__ __forceinline__ bool next(int i, SkUnit& u) const { const int L = i * G + c; if (L >= (T / 256) * 4) return false; u.pm = L >> 2; u.ks = L & 3; return true; }
; #define INF(i) ((const float*)arg_ptr(i))
;     __device__ __forceinline__ bool next(int i, DUnit& u) const {
;         long L = (long)i * G + c; const int nwg0 = nM * nN0, nwg1 = nM * nN1;
;         int nN, nwg; if (L < nwg0) { u.p = 0; nN = nN0; nwg = nwg0; } else { L -= nwg0; if (L >= nwg1) return false; u.p = 1; nN = nN1; nwg = nwg1; }
;         int wgid = (int)L; { const int q = nwg / NXCD, r = nwg % NXCD, xcd = wgid % NXCD, off = wgid / NXCD; wgid = (xcd < r ? xcd * (q + 1) : r * (q + 1) + (xcd - r) * q) + off; }
;         const int nig = WGM * nN, gid = wgid / nig, fm = gid * WGM, gsz = (nM - fm) < WGM ? (nM - fm) : WGM;
; template <int layer>
; __device__ __forceinline__ void ph_gemm_wo(LAS unsigned char* lds) {
;     PH_BEGIN;
;     const float* R = INF(0); bf16* H1b = WSP(bf16, WS_H1);
;     const float* gff = INF(layer == 0 ? 10 : 22); bf16* HN = WSP(bf16, WS_HN); float* SSQ = WSP(float, WS_SSQ);
;     fg::DenseSched S{WSP(bf16, WS_O), WSP(bf16, layer == 0 ? WS_W_O0T : WS_W_O1T), 8, nullptr, nullptr, 0, DM, G, bx};
.Lgbd_4:
.LBB0_641:
	s_or_b64 exec, exec, s[4:5]
	s_mov_b32 s0, 30
	s_waitcnt lgkmcnt(0)
	s_barrier
	s_ashr_i32 s1, s0, 31
	s_lshl_b64 s[0:1], s[0:1], 3
	s_add_u32 s12, s80, s0
	s_addc_u32 s13, s81, s1
	v_mov_b32_e32 v1, v0
	s_mov_b32 s0, s78
	s_mov_b32 s1, s79
	s_mov_b32 s2, 0
	s_ashr_i32 s3, s2, 31
	s_lshl_b64 s[2:3], s[2:3], 3
	s_add_u32 s14, s80, s2
	s_mov_b32 s2, 10
	s_addc_u32 s15, s81, s3
	s_ashr_i32 s3, s2, 31
	s_lshl_b64 s[2:3], s[2:3], 3
	s_add_u32 s16, s80, s2
	s_addc_u32 s17, s81, s3
	s_ashr_i32 s2, s1, 31
	v_mov_b32_e32 v1, v0
	s_cmpk_lt_i32 s1, 0x200
	s_cselect_b64 s[4:5], -1, 0
	s_cmpk_gt_i32 s1, 0x1ff
	v_readfirstlane_b32 s20, v1
	s_cbranch_scc1 .LBB0_643
	s_lshr_b32 s3, s2, 29
	s_add_i32 s3, s1, s3
	s_ashr_i32 s6, s3, 3
	s_and_b32 s3, s3, -8
	s_sub_i32 s3, s1, s3
	s_lshr_b32 s7, s3, 31
	s_or_b32 s7, s7, 64
	s_mul_i32 s3, s7, s3
	s_add_i32 s3, s3, s6
	s_ashr_i32 s6, s3, 31
	s_lshr_b32 s6, s6, 26
	s_add_i32 s6, s3, s6
	s_ashr_i32 s7, s6, 6
	s_lshl_b32 s8, s7, 3
	s_sub_i32 s7, 64, s8
	s_min_u32 s9, s7, 8
	s_andn2_b32 s6, s6, 63
	s_sub_i32 s3, s3, s6
	v_cvt_f32_ubyte0_e32 v3, s9
	v_cvt_f32_i32_e32 v2, s3
	v_rcp_iflag_f32_e32 v4, v3
	s_ashr_i32 s6, s3, 30
	s_or_b32 s10, s6, 1
	v_mul_f32_e32 v4, v2, v4
	v_trunc_f32_e32 v4, v4
	v_fma_f32 v2, -v4, v3, v2
	v_cvt_i32_f32_e32 v4, v4
	v_cmp_ge_f32_e64 s[6:7], |v2|, v3
	s_and_b64 s[6:7], s[6:7], exec
	s_cselect_b32 s6, s10, 0
	v_readfirstlane_b32 s7, v4
	s_add_i32 s7, s7, s6
	s_sext_i32_i8 s6, s7
	s_mul_i32 s7, s7, s9
	s_sub_i32 s3, s3, s7
	s_sext_i32_i8 s3, s3
	s_add_i32 s42, s8, s3

; __device__ __forceinline__ unsigned xb_add(unsigned* p, unsigned v) { return __hip_atomic_fetch_add(p, v, __ATOMIC_RELAXED, __HIP_MEMORY_SCOPE_AGENT); }
; __device__ __forceinline__ void xcd_barrier(const XcdBarrier& b) {
;     ...
;     if (threadIdx.x == 0) {
;         unsigned* bar = b.bar;
;         __builtin_amdgcn_s_waitcnt(0);
;         unsigned nloc = b.st[0], nx = b.st[1];
;         if (nloc == 0u) { xcd_barrier_complete(bar, b.x, nloc, nx); b.st[0] = nloc; b.st[1] = nx; }
;         const unsigned old = xb_add(&bar[XB_XSUB(b.x)], 1u);
;         const unsigned gen = old / nloc;
;         if (old + 1u == (gen + 1u) * nloc) {
;             __builtin_amdgcn_fence(__ATOMIC_RELEASE, "agent");
;             asm volatile("s_waitcnt vmcnt(0)" ::: "memory");
;             const unsigned og = xb_add(&bar[XB_TOP], 1u);
;             const unsigned tg = og / nx;
;             if (og + 1u == (tg + 1u) * nx) xb_add(&bar[XB_TOPGEN], 1u);
.LBB0_691:
	s_waitcnt lgkmcnt(0)
	v_readfirstlane_b32 s8, v3
	v_readfirstlane_b32 s9, v1
	v_readlane_b32 s0, v252, 4
	s_lshl_b32 s0, s0, 8
	v_readlane_b32 s2, v252, 2
	v_readlane_b32 s3, v252, 3
	s_add_u32 s6, s2, s0
	s_addc_u32 s7, s3, 0
	s_mul_i32 s10, s8, 6
	s_mul_i32 s11, s9, 6
	v_mov_b32_e32 v4, 0x1000
	v_mov_b32_e32 v5, 1
	global_atomic_add v4, v4, v5, s[6:7] offset:1024 sc0
	v_mov_b32_e32 v1, 0x3400
	s_waitcnt vmcnt(0)
	v_readfirstlane_b32 s0, v4
	s_add_u32 s0, s0, 1
	s_cmp_lg_u32 s0, s10
	buffer_inv sc1
	s_cbranch_scc1 .Lgbw_5
	buffer_wbl2 sc1
	s_waitcnt vmcnt(0)
	global_atomic_add v1, v5, s[2:3]

; __device__ __forceinline__ int otid() { int t = threadIdx.x; asm volatile("" : "+v"(t)); return t; }
; template <bool GATHER, class Unit, class Epi, class Sched>
; __device__ __forceinline__ void gemm_phase(LAS unsigned char* lds, const int K, const Sched& S, const Epi& E) {
;     const int tid = otid(), wid = __builtin_amdgcn_readfirstlane(tid >> 6), lane = tid & 63, wr = wid >> 2, wc = wid & 3, fr = lane & 15, fq = lane >> 4;
;     const int nt = K / BK;
;     int R0, C0, R1, C1; stage_rc(tid * 16, R0, C0); stage_rc(tid * 16 + 8192, R1, C1);
;     const int Rb0 = (R0 & ~31) + 8 * ((R0 & 15) >> 2) + 4 * ((R0 >> 4) & 1) + (R0 & 3), Rb1 = (R1 & ~31) + 8 * ((R1 & 15) >> 2) + 4 * ((R1 >> 4) & 1) + (R1 & 3);
;     const unsigned voffB0 = (unsigned)(Rb0 * K + C0) * 2u, voffB1 = (unsigned)(Rb1 * K + C1) * 2u;
;     const size_t kstep = (size_t)(BK * 2);
;     const size_t hstepB = (size_t)HALF * K * 2;
;     const unsigned ldsw = (unsigned)wid * 1024u;
;     const int aoff = lds_byte(wr * 64 + fr, fq * 8), boff = lds_byte(wc * 32 + fr, fq * 8);
;     ...
;     Unit cur, nxt; int ui = 0;
;     if (!S.next(0, cur)) return;
;     f32x4 acc[2][2][4][2];
; #pragma unroll
;     for (int a = 0; a < 2; ++a)
; #pragma unroll
;         for (int b = 0; b < 2; ++b)
; #pragma unroll
;             for (int m = 0; m < 4; ++m)
; #pragma unroll
;                 for (int n = 0; n < 2; ++n) acc[a][b][m][n] = (f32x4){0.f, 0.f, 0.f, 0.f};
;     bf16x8 At[4][2], B0[2][2], B1[2][2];
;     const char* cA = S.a_base(cur); const char* cB = S.b_base(cur);
;     unsigned vA00 = S.a_voff(cur, R0, C0), vA01 = S.a_voff(cur, R1, C1), vA10 = S.a_voff(cur, HALF + R0, C0), vA11 = S.a_voff(cur, HALF + R1, C1);
;     unsigned vN00 = vA00, vN01 = vA01, vN10 = vA10, vN11 = vA11;
;     bool hi_on = !S.lo_only(cur);
;     FG_STAGE(FG_SB(0, 0), cB, voffB0, voffB1); FG_STAGE(FG_SB(0, 1), cB + hstepB, voffB0, voffB1); FG_STAGE(FG_SA(0, 0), cA, vA00, vA01); FG_STAGE(FG_SA(0, 1), cA, vA10, vA11);
;     if (wr == 1) FG_BAR;
;     FG_WAIT_V(2); FG_BAR;
;     FG_STAGE(FG_SB(1, 0), cB + kstep, voffB0, voffB1); FG_STAGE(FG_SA(1, 0), cA + kstep, vA00, vA01); FG_STAGE(FG_SB(1, 1), cB + hstepB + kstep, voffB0, voffB1);
;     FG_WAIT_V(6); FG_BAR;
;     __device__ __forceinline__ bool next(int i, SkUnit& u) const { const int L = i * G + c; if (L >= (T / 256) * 4) return false; u.pm = L >> 2; u.ks = L & 3; return true; }
.Lgbd_5:
.LBB0_727:
	s_or_b64 exec, exec, s[4:5]
	s_mov_b32 s4, 30
	s_waitcnt lgkmcnt(0)
	v_mov_b32_e32 v1, v0
	s_barrier
	s_mov_b32 s0, s78
	s_mov_b32 s1, s79
	v_mov_b32_e32 v1, v0
	s_cmpk_gt_i32 s1, 0xff
	v_readfirstlane_b32 s14, v1
	s_cbranch_scc1 .LBB0_743
	v_lshlrev_b32_e32 v2, 4, v1
	v_add_u32_e32 v3, 0x2000, v2
	v_ashrrev_i32_e32 v4, 31, v3
	v_lshrrev_b32_e32 v4, 22, v4
	v_add_u32_e32 v4, v3, v4
	v_ashrrev_i32_e32 v10, 10, v4
	v_mul_i32_i24_e32 v4, 0x400, v10
	v_sub_u32_e32 v3, v3, v4
	v_lshrrev_b32_e32 v4, 4, v3
	v_bitop3_b32 v3, v4, v3, 32 bitop3:0x6c
	v_ashrrev_i32_e32 v4, 31, v3
	v_lshrrev_b32_e32 v4, 26, v4
	v_add_u32_e32 v4, v3, v4
	v_lshlrev_b32_e32 v5, 3, v10
	v_ashrrev_i32_e32 v11, 6, v4
	v_and_b32_e32 v5, -16, v5
	s_ashr_i32 s5, s4, 31
	v_add_u32_e32 v5, v11, v5
	s_lshl_b64 s[2:3], s[4:5], 3
	v_and_b32_e32 v6, 3, v11
	s_mov_b32 s5, 0x3fffe0
	v_lshlrev_b32_e32 v7, 1, v5
	v_lshrrev_b32_e32 v8, 2, v5
	v_and_b32_e32 v4, 0xc0, v4
	v_and_or_b32 v6, v5, s5, v6
	v_and_b32_e32 v7, 24, v7
	v_and_b32_e32 v8, 4, v8
	v_sub_u32_e32 v3, v3, v4
	v_mov_b32_e32 v4, 1
	v_or3_b32 v6, v6, v7, v8
	v_lshlrev_b32_e32 v7, 5, v10
	v_ashrrev_i16_sdwa v3, v4, sext(v3) dst_sel:DWORD dst_unused:UNUSED_PAD src0_sel:DWORD src1_sel:BYTE_0
	v_and_b32_e32 v7, 32, v7
	v_bfe_i32 v12, v3, 0, 16
	v_add_lshl_u32 v3, v7, v12, 1
	v_lshl_add_u32 v66, v6, 10, v3
	v_bfe_i32 v6, v1, 27, 1
	v_lshrrev_b32_e32 v6, 22, v6
	v_add_u32_e32 v6, v2, v6
	v_and_b32_e32 v6, 0xfffffc00, v6
	v_sub_u32_e32 v2, v2, v6
	s_add_u32 s2, s80, s2
	v_lshrrev_b32_e32 v6, 4, v2
	s_addc_u32 s3, s81, s3
	v_bitop3_b32 v6, v6, v2, 32 bitop3:0x6c
	v_ashrrev_i32_e32 v2, 31, v2
	s_load_dwordx2 s[12:13], s[2:3], 0x0
	v_lshrrev_b32_e32 v2, 26, v2
	v_add_u32_e32 v2, v6, v2
	v_ashrrev_i32_e32 v13, 6, v2
	v_ashrrev_i32_e32 v2, 31, v1
	v_lshrrev_b32_e32 v2, 26, v2
	v_add_u32_e32 v2, v1, v2
	s_waitcnt lgkmcnt(0)
	s_add_u32 s2, s12, 0x1be00000
	v_ashrrev_i32_e32 v14, 6, v2
	s_addc_u32 s3, s13, 0
	v_lshlrev_b32_e32 v2, 3, v14
	s_add_u32 s22, s12, 0x6c500000
	v_and_b32_e32 v2, -16, v2
	s_addc_u32 s23, s13, 0
	s_ashr_i32 s4, s1, 2
	v_add_u32_e32 v2, v13, v2
	v_and_b32_e32 v7, 3, v13
	s_ashr_i32 s15, s14, 6
	s_and_b32 s27, s1, 3
	v_and_or_b32 v7, v2, s5, v7
	s_ashr_i32 s5, s4, 31
	s_ashr_i32 s16, s14, 8
	s_lshl_b32 s26, s15, 10
	v_lshlrev_b32_e32 v8, 1, v2
	v_lshrrev_b32_e32 v9, 2, v2
	s_lshl_b32 s8, s27, 10
	s_lshl_b64 s[6:7], s[4:5], 20
	v_and_b32_e32 v8, 24, v8
	v_and_b32_e32 v9, 4, v9
	s_add_u32 s5, s2, s6
	v_or3_b32 v7, v7, v8, v9
	v_mul_i32_i24_e32 v9, 64, v13
	s_addc_u32 s7, s3, s7
	v_sub_u32_e32 v6, v6, v9
	s_add_u32 s6, s5, s8
	v_lshlrev_b32_e32 v8, 5, v14
	v_ashrrev_i16_sdwa v4, v4, sext(v6) dst_sel:DWORD dst_unused:UNUSED_PAD src0_sel:DWORD src1_sel:BYTE_0
	s_addc_u32 s7, s7, 0
	s_lshl_b32 s5, s27, 18
	v_and_b32_e32 v8, 32, v8
	v_bfe_i32 v15, v4, 0, 16
	s_add_u32 s8, s22, s5
	v_add_lshl_u32 v4, v8, v15, 1
	s_addc_u32 s9, s23, 0
	s_add_i32 s5, s26, 0
	v_lshl_add_u32 v68, v7, 10, v4
	s_add_i32 m0, s5, 0x10000
	v_lshl_add_u32 v70, v2, 12, v4
	global_load_lds_dwordx4 v68, s[8:9]
	s_add_i32 m0, s5, 0x12000
	s_add_u32 s10, s8, 0x20000
	s_addc_u32 s11, s9, 0
	s_add_i32 s28, s5, 0x14000
	global_load_lds_dwordx4 v66, s[8:9]
	s_mov_b32 m0, s28
	s_add_i32 s29, s5, 0x16000
	global_load_lds_dwordx4 v68, s[10:11]
	s_mov_b32 m0, s29
	s_add_i32 s30, s5, 0x2000
	global_load_lds_dwordx4 v66, s[10:11]
	s_mov_b32 m0, s5
	v_lshl_add_u32 v72, v5, 12, v3
	global_load_lds_dwordx4 v70, s[6:7]
	s_mov_b32 m0, s30
	s_add_i32 s31, s5, 0x4000
	v_add_u32_e32 v74, 0x80000, v70
	global_load_lds_dwordx4 v72, s[6:7]
	s_mov_b32 m0, s31
	s_add_i32 s33, s5, 0x6000
	v_add_u32_e32 v76, 0x80000, v72
	global_load_lds_dwordx4 v74, s[6:7]
	s_mov_b32 m0, s33
	v_mov_b32_e32 v79, 0
	global_load_lds_dwordx4 v76, s[6:7]
	v_mov_b32_e32 v69, v79
	v_mov_b32_e32 v67, v79
	v_mov_b32_e32 v71, v79
	v_mov_b32_e32 v73, v79
	s_cmp_eq_u32 s16, 1
	s_mov_b32 s34, 0
	s_mov_b32 s17, 0x80000
	v_lshl_add_u64 v[8:9], s[8:9], 0, v[68:69]
	v_lshl_add_u64 v[6:7], s[8:9], 0, v[66:67]
	v_lshl_add_u64 v[2:3], s[6:7], 0, v[70:71]
	s_cselect_b64 s[10:11], -1, 0
	s_cmp_lg_u32 s16, 1
	v_lshl_add_u64 v[4:5], s[6:7], 0, v[72:73]
	s_cbranch_scc1 .LBB0_730
	s_barrier

; __device__ __forceinline__ unsigned xb_add(unsigned* p, unsigned v) { return __hip_atomic_fetch_add(p, v, __ATOMIC_RELAXED, __HIP_MEMORY_SCOPE_AGENT); }
; __device__ __forceinline__ void xcd_barrier(const XcdBarrier& b) {
;     ...
;     if (threadIdx.x == 0) {
;         unsigned* bar = b.bar;
;         __builtin_amdgcn_s_waitcnt(0);
;         unsigned nloc = b.st[0], nx = b.st[1];
;         if (nloc == 0u) { xcd_barrier_complete(bar, b.x, nloc, nx); b.st[0] = nloc; b.st[1] = nx; }
;         const unsigned old = xb_add(&bar[XB_XSUB(b.x)], 1u);
;         const unsigned gen = old / nloc;
;         if (old + 1u == (gen + 1u) * nloc) {
;             __builtin_amdgcn_fence(__ATOMIC_RELEASE, "agent");
;             asm volatile("s_waitcnt vmcnt(0)" ::: "memory");
;             const unsigned og = xb_add(&bar[XB_TOP], 1u);
;             const unsigned tg = og / nx;
;             if (og + 1u == (tg + 1u) * nx) xb_add(&bar[XB_TOPGEN], 1u);
.LBB0_759:
	s_waitcnt lgkmcnt(0)
	v_readfirstlane_b32 s8, v3
	v_readfirstlane_b32 s9, v1
	v_readlane_b32 s0, v252, 4
	s_lshl_b32 s0, s0, 8
	v_readlane_b32 s2, v252, 2
	v_readlane_b32 s3, v252, 3
	s_add_u32 s6, s2, s0
	s_addc_u32 s7, s3, 0
	s_mul_i32 s10, s8, 7
	s_mul_i32 s11, s9, 7
	v_mov_b32_e32 v4, 0x1000
	v_mov_b32_e32 v5, 1
	global_atomic_add v4, v4, v5, s[6:7] offset:1024 sc0
	v_mov_b32_e32 v1, 0x3400
	s_waitcnt vmcnt(0)
	v_readfirstlane_b32 s0, v4
	s_add_u32 s0, s0, 1
	s_cmp_lg_u32 s0, s10
	buffer_inv sc1
	s_cbranch_scc1 .Lgbw_6
	buffer_wbl2 sc1
	s_waitcnt vmcnt(0)
	global_atomic_add v1, v5, s[2:3]

; #define LAS __attribute__((address_space(3)))
; __device__ __forceinline__ float rsq(float x) { return __builtin_amdgcn_rsqf(x); }
; #define INF(i) ((const float*)arg_ptr(i))
; template <int layer>
; __device__ __forceinline__ void ph_route(LAS unsigned char* lds) {
;     PH_BEGIN;
;     LAS unsigned* lcnt = (LAS unsigned*)lds; LAS unsigned* lbase = lcnt + 64;
;     const float* PR = WSP(float, WS_PR); int* TOK = WSP(int, WS_TOK); float* GATE = WSP(float, WS_GATE); int* TSLOT = WSP(int, WS_TSLOT); const float* SSQ = WSP(float, WS_SSQ); float* RSL = WSP(float, WS_RSL);
;     unsigned* cnt = WSP(unsigned, WS_CTL) + (layer == 0 ? CW_CNT0 : CW_CNT1);
;     const float* b_rg = INF(layer == 0 ? 12 : 24); const float* b_re = INF(layer == 0 ? 14 : 26);
;     constexpr int TPW = 128;
;     static_assert(T % TPW == 0 && T / TPW <= 248, "whole workgroups of tokens, one trip");
;     if (bx * TPW < T) {
;         if (tid < 64) lcnt[tid] = 0u;
;         __syncthreads();
;         const int t = bx * TPW + tid; int e1o = 0, e2o = 0; float g1o = 0.f, g2o = 0.f, rso = 0.f; unsigned r1 = 0u, r2 = 0u;
;         if (tid < TPW) {
;         const float* pr = PR + (size_t)t * 80;
;         float rstd; { f32x4 q = *(const f32x4*)(SSQ + (size_t)t * 32);
; #pragma unroll
;             for (int i = 1; i < 8; ++i) q += *(const f32x4*)(SSQ + (size_t)t * 32 + 4 * i);
;             rstd = rsq(((q[0] + q[1]) + (q[2] + q[3])) * (1.0f / DM) + EPS); }
;         auto sum4 = [=](int j) { const f32x4 a0 = *(const f32x4*)(pr + j), a1 = *(const f32x4*)(pr + (size_t)T * 80 + j), a2 = *(const f32x4*)(pr + (size_t)2 * T * 80 + j), a3 = *(const f32x4*)(pr + (size_t)3 * T * 80 + j);
;             return (a0 + a1) + (a2 + a3); };
;         float gl[8]; int g = 0; float gm = -3.0e38f;
;         { const f32x4 x0 = sum4(0), x1 = sum4(4);
; #pragma unroll
;           for (int j = 0; j < 8; ++j) { gl[j] = (j < 4 ? x0[j & 3] : x1[j & 3]) * rstd + b_rg[j]; if (gl[j] > gm) { gm = gl[j]; g = j; } } }
.Lgbd_6:
.LBB0_795:
	s_or_b64 exec, exec, s[4:5]
	s_mov_b32 s4, 30
	v_mov_b32_e32 v16, v0
	s_mov_b32 s0, s78
	s_waitcnt lgkmcnt(0)
	s_barrier
	s_mov_b32 s0, s79
	s_mov_b32 s8, 12
	s_mov_b32 s6, 14
	s_cmpk_gt_i32 s0, 0x7f
	s_cbranch_scc1 .LBB0_811
	s_ashr_i32 s5, s4, 31
	s_lshl_b64 s[2:3], s[4:5], 3
	s_add_u32 s2, s80, s2
	s_addc_u32 s3, s81, s3
	s_ashr_i32 s9, s8, 31
	s_load_dwordx2 s[18:19], s[2:3], 0x0
	s_lshl_b64 s[2:3], s[8:9], 3
	s_add_u32 s10, s80, s2
	s_addc_u32 s11, s81, s3
	s_ashr_i32 s7, s6, 31
	s_lshl_b64 s[2:3], s[6:7], 3
	s_add_u32 s12, s80, s2
	s_addc_u32 s13, s81, s3
	v_cmp_gt_i32_e64 s[6:7], 64, v16
	v_lshl_add_u32 v1, v16, 2, 0
	s_and_saveexec_b64 s[4:5], s[6:7]
	v_mov_b32_e32 v2, 0
	ds_write_b32 v1, v2
	s_or_b64 exec, exec, s[4:5]
	v_lshl_add_u32 v14, s0, 7, v16
	s_movk_i32 s0, 0x80
	v_cmp_gt_i32_e64 s[4:5], s0, v16
	v_mov_b32_e32 v6, 0
	v_mov_b32_e32 v4, 0
	v_mov_b32_e32 v2, 0
	v_mov_b32_e32 v7, 0
	v_mov_b32_e32 v15, 0
	v_mov_b32_e32 v3, 0
	v_mov_b32_e32 v8, 0
	s_waitcnt lgkmcnt(0)
	s_barrier
	s_and_saveexec_b64 s[20:21], s[4:5]
	s_cbranch_execz .LBB0_804
	v_ashrrev_i32_e32 v15, 31, v14
	v_lshlrev_b64 v[2:3], 7, v[14:15]
	v_lshl_add_u64 v[2:3], s[18:19], 0, v[2:3]
	s_mov_b64 s[0:1], 0x4e000000
	v_lshl_add_u64 v[4:5], v[2:3], 0, s[0:1]
	s_movk_i32 s0, 0x140
	v_mov_b64_e32 v[6:7], s[18:19]
	v_mad_i64_i32 v[74:75], s[0:1], v14, s0, v[6:7]
	s_mov_b32 s0, 0x6db00000
	s_nop 0
	v_add_co_u32_e64 v6, s[8:9], s0, v74
	s_mov_b32 s0, 0x6e000000
	s_nop 0
	v_addc_co_u32_e64 v7, s[8:9], 0, v75, s[8:9]
	global_load_dwordx4 v[10:13], v[6:7], off
	v_add_co_u32_e64 v6, s[8:9], s0, v74
	s_mov_b32 s0, 0x6e500000
	s_nop 0
	v_addc_co_u32_e64 v7, s[8:9], 0, v75, s[8:9]
	global_load_dwordx4 v[18:21], v[6:7], off
	v_add_co_u32_e64 v6, s[8:9], s0, v74
	s_mov_b32 s0, 0x6ea00000
	s_nop 0
	v_addc_co_u32_e64 v7, s[8:9], 0, v75, s[8:9]
	global_load_dwordx4 v[22:25], v[6:7], off
	v_add_co_u32_e64 v6, s[8:9], s0, v74
	v_add_co_u32_e32 v2, vcc, 0x4e000000, v2
	s_nop 0
	v_addc_co_u32_e64 v7, s[8:9], 0, v75, s[8:9]
	global_load_dwordx4 v[26:29], v[6:7], off
	v_addc_co_u32_e32 v3, vcc, 0, v3, vcc
	global_load_dwordx4 v[30:33], v[2:3], off
	global_load_dwordx4 v[34:37], v[4:5], off offset:16
	global_load_dwordx4 v[38:41], v[4:5], off offset:32
	global_load_dwordx4 v[42:45], v[4:5], off offset:48
	global_load_dwordx4 v[46:49], v[4:5], off offset:64
	global_load_dwordx4 v[50:53], v[4:5], off offset:80
	global_load_dwordx4 v[54:57], v[4:5], off offset:96
	global_load_dwordx4 v[58:61], v[4:5], off offset:112
	s_load_dwordx2 s[0:1], s[10:11], 0x0
	s_load_dwordx2 s[24:25], s[12:13], 0x0
	v_mov_b32_e32 v79, 0
	s_mov_b64 s[2:3], 0x6db00000
	v_lshl_add_u64 v[80:81], v[74:75], 0, s[2:3]
	s_waitcnt lgkmcnt(0)
	global_load_dwordx4 v[6:9], v79, s[0:1]
	s_mov_b64 s[2:3], 0x6e000000
	v_lshl_add_u64 v[82:83], v[74:75], 0, s[2:3]
	s_mov_b64 s[2:3], 0x6e500000
	v_lshl_add_u64 v[84:85], v[74:75], 0, s[2:3]
	s_mov_b64 s[2:3], 0x6ea00000
	global_load_dwordx4 v[62:65], v[80:81], off offset:16
	global_load_dwordx4 v[66:69], v[82:83], off offset:16
	global_load_dwordx4 v[70:73], v[84:85], off offset:16
	v_lshl_add_u64 v[86:87], v[74:75], 0, s[2:3]
	global_load_dwordx4 v[74:77], v[86:87], off offset:16
	global_load_dwordx4 v[2:5], v79, s[0:1] offset:16
	v_mov_b32_e32 v15, 0x358637bd
	s_mov_b32 s0, 0xff61b1e6
	s_waitcnt vmcnt(17)
	v_mov_b32_e32 v88, v10
	s_waitcnt vmcnt(16)
	v_mov_b32_e32 v90, v18
	s_waitcnt vmcnt(15)
	v_mov_b32_e32 v89, v22
	v_mov_b32_e32 v22, v11
	s_waitcnt vmcnt(12)
	v_pk_add_f32 v[30:31], v[30:31], v[34:35]
	s_waitcnt vmcnt(11)
	v_pk_add_f32 v[30:31], v[30:31], v[38:39]
	v_mov_b32_e32 v91, v26
	v_mov_b32_e32 v26, v19
	v_pk_add_f32 v[18:19], v[32:33], v[36:37]
	s_waitcnt vmcnt(10)
	v_pk_add_f32 v[30:31], v[30:31], v[42:43]
	v_pk_add_f32 v[18:19], v[18:19], v[40:41]
	s_waitcnt vmcnt(9)
	v_pk_add_f32 v[30:31], v[30:31], v[46:47]
	v_pk_add_f32 v[18:19], v[18:19], v[44:45]
	s_waitcnt vmcnt(8)
	v_pk_add_f32 v[30:31], v[30:31], v[50:51]
	v_pk_add_f32 v[18:19], v[18:19], v[48:49]
	s_waitcnt vmcnt(7)
	v_pk_add_f32 v[30:31], v[30:31], v[54:55]
	v_pk_add_f32 v[18:19], v[18:19], v[52:53]
	s_waitcnt vmcnt(6)
	v_pk_add_f32 v[30:31], v[30:31], v[58:59]
	v_pk_add_f32 v[18:19], v[18:19], v[56:57]
	v_pk_add_f32 v[10:11], v[88:89], v[90:91]
	v_pk_add_f32 v[18:19], v[18:19], v[60:61]
	v_add_f32_e32 v10, v10, v11
	v_pk_mov_b32 v[32:33], v[30:31], v[18:19] op_sel:[1,0]
	v_mov_b32_e32 v31, v19
	v_pk_add_f32 v[18:19], v[32:33], v[30:31]
	s_nop 0
	v_add_f32_e32 v17, v18, v19
	v_fmac_f32_e32 v15, 0x3a000000, v17
	v_rsq_f32_e32 v15, v15
	v_pk_add_f32 v[18:19], v[22:23], v[26:27]
	s_waitcnt vmcnt(5)
	v_fma_f32 v17, v15, v10, v6
	v_add_f32_e32 v11, v18, v19
	v_fma_f32 v18, v15, v11, v7
	v_max_f32_e32 v6, 0xff61b1e6, v17
	v_cmp_gt_f32_e32 vcc, v18, v6
	v_mov_b32_e32 v7, v24
	v_mov_b32_e32 v10, v20
	v_cndmask_b32_e32 v19, v6, v18, vcc
	v_mov_b32_e32 v6, v12
	v_mov_b32_e32 v11, v28
	v_pk_add_f32 v[6:7], v[6:7], v[10:11]
	v_mov_b32_e32 v24, v13
	v_add_f32_e32 v6, v6, v7
	v_mov_b32_e32 v28, v21
	v_fma_f32 v8, v15, v6, v8
	v_pk_add_f32 v[6:7], v[24:25], v[28:29]
	v_cmp_gt_f32_e64 s[8:9], v8, v19
	v_add_f32_e32 v6, v6, v7
	v_fmac_f32_e32 v9, v15, v6
	v_cndmask_b32_e64 v10, v19, v8, s[8:9]
	v_cmp_gt_f32_e64 s[10:11], v9, v10
	s_waitcnt vmcnt(4)
	v_mov_b32_e32 v6, v62
	s_waitcnt vmcnt(2)
	v_mov_b32_e32 v7, v70
	v_cndmask_b32_e64 v12, v10, v9, s[10:11]
	v_mov_b32_e32 v10, v66
	s_waitcnt vmcnt(1)
	v_mov_b32_e32 v11, v74
	v_pk_add_f32 v[6:7], v[6:7], v[10:11]
	v_mov_b32_e32 v70, v63
	v_add_f32_e32 v6, v6, v7
	v_mov_b32_e32 v74, v67
	s_waitcnt vmcnt(0)
; template <int layer>
; __device__ __forceinline__ void ph_route(LAS unsigned char* lds) {
;     ...
;           for (int j = 0; j < 8; ++j) { gl[j] = (j < 4 ? x0[j & 3] : x1[j & 3]) * rstd + b_rg[j]; if (gl[j] > gm) { gm = gl[j]; g = j; } } }
;         float se = 0.f;
; #pragma unroll
;         for (int j = 0; j < 8; ++j) se += expf(gl[j] - gm);
;         const float pg = 1.0f / se;
;         float el[8]; int i1 = 0; float m1 = -3.0e38f;
;         { const f32x4 x0 = sum4(8 + g * 8), x1 = sum4(12 + g * 8);
; #pragma unroll
;           for (int j = 0; j < 8; ++j) { el[j] = (j < 4 ? x0[j & 3] : x1[j & 3]) * rstd + b_re[g * 8 + j]; if (el[j] > m1) { m1 = el[j]; i1 = j; } } }
;         int i2 = 0; float m2 = -3.0e38f;
; #pragma unroll
;         for (int j = 0; j < 8; ++j) { if (j != i1 && el[j] > m2) { m2 = el[j]; i2 = j; } }
;         const float w2 = expf(m2 - m1), g1 = pg / (1.0f + w2), g2 = pg * w2 / (1.0f + w2);
	v_fma_f32 v7, v15, v6, v2
	v_pk_add_f32 v[10:11], v[70:71], v[74:75]
	v_cmp_gt_f32_e64 s[12:13], v7, v12
	v_add_f32_e32 v6, v10, v11
	v_fma_f32 v6, v15, v6, v3
	v_cndmask_b32_e64 v2, v12, v7, s[12:13]
	v_cmp_gt_f32_e64 s[14:15], v6, v2
	v_mov_b32_e32 v3, v72
	v_mov_b32_e32 v10, v68
	v_cndmask_b32_e64 v12, v2, v6, s[14:15]
	v_mov_b32_e32 v2, v64
	v_mov_b32_e32 v11, v76
	v_pk_add_f32 v[2:3], v[2:3], v[10:11]
	v_mov_b32_e32 v72, v65
	v_add_f32_e32 v2, v2, v3
	v_mov_b32_e32 v76, v69
	v_fma_f32 v4, v15, v2, v4
	v_pk_add_f32 v[2:3], v[72:73], v[76:77]
	v_cmp_gt_f32_e64 s[16:17], v4, v12
	v_add_f32_e32 v2, v2, v3
	v_fmac_f32_e32 v5, v15, v2
	v_cndmask_b32_e64 v2, 0, 8, vcc
	v_cndmask_b32_e64 v2, v2, 16, s[8:9]
	v_cndmask_b32_e64 v2, v2, 24, s[10:11]
	v_cndmask_b32_e64 v2, v2, 32, s[12:13]
	v_cndmask_b32_e64 v19, v12, v4, s[16:17]
	v_cndmask_b32_e64 v2, v2, 40, s[14:15]
	v_cndmask_b32_e64 v2, v2, 48, s[16:17]
	v_cmp_gt_f32_e32 vcc, v5, v19
	v_mov_b32_e32 v3, v79
	s_nop 0
	v_cndmask_b32_e64 v2, v2, 56, vcc
	v_add_u32_e32 v78, 8, v2
	v_lshlrev_b64 v[10:11], 2, v[2:3]
	v_lshlrev_b64 v[12:13], 2, v[78:79]
	v_lshl_add_u64 v[56:57], v[80:81], 0, v[10:11]
	v_lshl_add_u64 v[58:59], v[82:83], 0, v[12:13]
	v_lshl_add_u64 v[60:61], v[84:85], 0, v[12:13]
	v_lshl_add_u64 v[62:63], v[86:87], 0, v[12:13]
	global_load_dwordx4 v[20:23], v[56:57], off offset:32
	global_load_dwordx4 v[24:27], v[58:59], off
	global_load_dwordx4 v[28:31], v[60:61], off
	global_load_dwordx4 v[32:35], v[62:63], off
	v_lshl_add_u64 v[64:65], s[24:25], 0, v[10:11]
	global_load_dwordx4 v[36:39], v[64:65], off
	global_load_dwordx4 v[40:43], v[56:57], off offset:48
	global_load_dwordx4 v[44:47], v[60:61], off offset:16
	global_load_dwordx4 v[48:51], v[58:59], off offset:16
	global_load_dwordx4 v[52:55], v[62:63], off offset:16
	global_load_dwordx4 v[10:13], v[64:65], off offset:16
	s_waitcnt vmcnt(9)
	v_mov_b32_e32 v56, v20
	s_waitcnt vmcnt(8)
	v_mov_b32_e32 v58, v24
	s_waitcnt vmcnt(7)
	v_mov_b32_e32 v57, v28
	s_waitcnt vmcnt(6)
	v_mov_b32_e32 v59, v32
	v_pk_add_f32 v[56:57], v[56:57], v[58:59]
	v_mov_b32_e32 v20, v22
	v_mov_b32_e32 v28, v21
	v_mov_b32_e32 v32, v25
	v_mov_b32_e32 v21, v30
	v_mov_b32_e32 v24, v26
	v_mov_b32_e32 v25, v34
	v_add_f32_e32 v3, v56, v57
	v_pk_add_f32 v[28:29], v[28:29], v[32:33]
	v_pk_add_f32 v[20:21], v[20:21], v[24:25]
	s_waitcnt vmcnt(5)
	v_fma_f32 v24, v15, v3, v36
	v_add_f32_e32 v22, v28, v29
	v_max_f32_e32 v3, v24, v24
	v_fma_f32 v25, v15, v22, v37
	v_max_f32_e32 v3, 0xff61b1e6, v3
	v_cmp_gt_f32_e64 s[10:11], v25, v3
	v_add_f32_e32 v20, v20, v21
	v_mov_b32_e32 v30, v23
	v_mov_b32_e32 v34, v27
	v_cndmask_b32_e64 v3, v3, v25, s[10:11]
	v_fma_f32 v26, v15, v20, v38
	v_pk_add_f32 v[20:21], v[30:31], v[34:35]
	v_cndmask_b32_e64 v22, 0, 1, s[10:11]
	v_cmp_gt_f32_e64 s[10:11], v26, v3
	v_add_f32_e32 v20, v20, v21
	v_fmac_f32_e32 v39, v15, v20
	v_cndmask_b32_e64 v3, v3, v26, s[10:11]
	v_cndmask_b32_e64 v22, v22, 2, s[10:11]
	v_cmp_gt_f32_e64 s[10:11], v39, v3
	s_waitcnt vmcnt(4)
	v_mov_b32_e32 v20, v40
	s_waitcnt vmcnt(3)
	v_mov_b32_e32 v21, v44
	v_cndmask_b32_e64 v27, v22, 3, s[10:11]
	s_waitcnt vmcnt(2)
	v_mov_b32_e32 v22, v48
	s_waitcnt vmcnt(1)
	v_mov_b32_e32 v23, v52
	v_pk_add_f32 v[20:21], v[20:21], v[22:23]
	v_mov_b32_e32 v44, v41
	v_add_f32_e32 v20, v20, v21
	v_mov_b32_e32 v52, v49
	v_cndmask_b32_e64 v3, v3, v39, s[10:11]
	s_waitcnt vmcnt(0)
	v_fma_f32 v22, v15, v20, v10
	v_pk_add_f32 v[20:21], v[44:45], v[52:53]
	v_cmp_gt_f32_e64 s[10:11], v22, v3
	v_add_f32_e32 v20, v20, v21
	v_fma_f32 v23, v15, v20, v11
	v_cndmask_b32_e64 v3, v3, v22, s[10:11]
	v_cndmask_b32_e64 v10, v27, 4, s[10:11]
	v_cmp_gt_f32_e64 s[10:11], v23, v3
	v_mov_b32_e32 v11, v46
	v_mov_b32_e32 v20, v50
	v_cndmask_b32_e64 v27, v10, 5, s[10:11]
	v_mov_b32_e32 v10, v42
	v_mov_b32_e32 v21, v54
	v_pk_add_f32 v[10:11], v[10:11], v[20:21]
	v_mov_b32_e32 v46, v43
	v_add_f32_e32 v10, v10, v11
	v_mov_b32_e32 v54, v51
	v_cndmask_b32_e64 v3, v3, v23, s[10:11]
	v_fma_f32 v20, v15, v10, v12
	v_pk_add_f32 v[10:11], v[46:47], v[54:55]
	v_cmp_ngt_f32_e64 s[10:11], v20, v3
	v_add_f32_e32 v10, v10, v11
	v_fmac_f32_e32 v13, v15, v10
	v_cndmask_b32_e64 v12, v20, v3, s[10:11]
	v_cndmask_b32_e64 v3, 6, v27, s[10:11]
	v_cmp_gt_f32_e64 s[14:15], v13, v12
	v_cmp_nlt_f32_e64 s[8:9], s0, v24
	v_mov_b32_e32 v10, 0xff61b1e6
	v_cndmask_b32_e64 v3, v3, 7, s[14:15]
	v_cmp_eq_u32_e64 s[16:17], 0, v3
	s_or_b64 s[8:9], s[16:17], s[8:9]
	v_cndmask_b32_e64 v10, v24, v10, s[8:9]
	v_cmp_ne_u32_e64 s[8:9], 1, v3
	v_cmp_gt_f32_e64 s[16:17], v25, v10
	s_and_b64 s[8:9], s[8:9], s[16:17]
	v_cndmask_b32_e64 v10, v10, v25, s[8:9]
	v_cndmask_b32_e64 v11, 0, 1, s[8:9]
	v_cmp_ne_u32_e64 s[8:9], 2, v3
	v_cmp_gt_f32_e64 s[16:17], v26, v10
	s_and_b64 s[8:9], s[8:9], s[16:17]
	v_cndmask_b32_e64 v10, v10, v26, s[8:9]
	v_cndmask_b32_e64 v11, v11, 2, s[8:9]
	v_cmp_ne_u32_e64 s[8:9], 3, v3
	v_cmp_gt_f32_e64 s[16:17], v39, v10
	s_and_b64 s[8:9], s[8:9], s[16:17]
	v_cndmask_b32_e64 v10, v10, v39, s[8:9]
	v_cndmask_b32_e64 v11, v11, 3, s[8:9]
	v_cmp_ne_u32_e64 s[8:9], 4, v3
	v_cmp_gt_f32_e64 s[16:17], v22, v10
	s_and_b64 s[8:9], s[8:9], s[16:17]
	v_cndmask_b32_e64 v10, v10, v22, s[8:9]
	v_cndmask_b32_e64 v11, v11, 4, s[8:9]
	v_cmp_ne_u32_e64 s[8:9], 5, v3
	v_cmp_gt_f32_e64 s[16:17], v23, v10
	s_and_b64 s[8:9], s[8:9], s[16:17]
	v_cndmask_b32_e64 v21, v10, v23, s[8:9]
	v_cndmask_b32_e64 v11, v11, 5, s[8:9]
	s_or_b64 s[0:1], s[10:11], s[14:15]
	v_cmp_gt_f32_e64 s[8:9], v20, v21
	s_and_b64 s[8:9], s[0:1], s[8:9]
	v_cmp_ngt_f32_e64 s[12:13], v13, v12
	v_cndmask_b32_e64 v10, v11, 6, s[8:9]
	v_cndmask_b32_e64 v11, v21, v20, s[8:9]
	s_and_saveexec_b64 s[10:11], s[12:13]
	s_cbranch_execz .LBB0_803
	v_cmp_gt_f32_e64 s[8:9], v13, v11
	s_and_saveexec_b64 s[12:13], s[8:9]
	v_mov_b32_e32 v10, 7
	v_mov_b32_e32 v11, v13
	s_or_b64 exec, exec, s[12:13]
	v_mov_b32_e32 v13, v12

; __device__ __forceinline__ unsigned xb_add(unsigned* p, unsigned v) { return __hip_atomic_fetch_add(p, v, __ATOMIC_RELAXED, __HIP_MEMORY_SCOPE_AGENT); }
; __device__ __forceinline__ void xcd_barrier(const XcdBarrier& b) {
;     ...
;     if (threadIdx.x == 0) {
;         unsigned* bar = b.bar;
;         __builtin_amdgcn_s_waitcnt(0);
;         unsigned nloc = b.st[0], nx = b.st[1];
;         if (nloc == 0u) { xcd_barrier_complete(bar, b.x, nloc, nx); b.st[0] = nloc; b.st[1] = nx; }
;         const unsigned old = xb_add(&bar[XB_XSUB(b.x)], 1u);
;         const unsigned gen = old / nloc;
;         if (old + 1u == (gen + 1u) * nloc) {
;             __builtin_amdgcn_fence(__ATOMIC_RELEASE, "agent");
;             asm volatile("s_waitcnt vmcnt(0)" ::: "memory");
;             const unsigned og = xb_add(&bar[XB_TOP], 1u);
;             const unsigned tg = og / nx;
;             if (og + 1u == (tg + 1u) * nx) xb_add(&bar[XB_TOPGEN], 1u);
.LBB0_827:
	s_waitcnt lgkmcnt(0)
	v_readfirstlane_b32 s8, v3
	v_readfirstlane_b32 s9, v1
	v_readlane_b32 s0, v252, 4
	s_lshl_b32 s0, s0, 8
	v_readlane_b32 s2, v252, 2
	v_readlane_b32 s3, v252, 3
	s_add_u32 s6, s2, s0
	s_addc_u32 s7, s3, 0
	s_mul_i32 s10, s8, 8
	s_mul_i32 s11, s9, 8
	v_mov_b32_e32 v4, 0x1000
	v_mov_b32_e32 v5, 1
	global_atomic_add v4, v4, v5, s[6:7] offset:1024 sc0
	v_mov_b32_e32 v1, 0x3400
	s_waitcnt vmcnt(0)
	v_readfirstlane_b32 s0, v4
	s_add_u32 s0, s0, 1
	s_cmp_lg_u32 s0, s10
	buffer_inv sc1
	s_cbranch_scc1 .Lgbw_7
	buffer_wbl2 sc1
	s_waitcnt vmcnt(0)
	global_atomic_add v1, v5, s[2:3]

; #define LAS __attribute__((address_space(3)))
; __device__ __forceinline__ int otid() { int t = threadIdx.x; asm volatile("" : "+v"(t)); return t; }
; __device__ __forceinline__ void moe_prefix(LAS unsigned char* lds, const unsigned* cnt) {
;     LAS int* s_ts = (LAS int*)(lds + LDS_TS); LAS int* s_cn = (LAS int*)(lds + LDS_CN);
;     LAS unsigned char* s_te = lds + LDS_TE;
;     LAS int* s_xs = (LAS int*)(lds + LDS_XS);
;     const int tz_ = otid();
;     if (tz_ < 64) { const int e = tz_; const int c = (int)cnt[e], nt = (c + 255) >> 8;
;         int incl = nt;
; #pragma unroll
;         for (int o = 1; o < 64; o <<= 1) { const int up = __shfl_up(incl, o); if (e >= o) incl += up; }
;         const int excl = incl - nt;
;         s_ts[e] = excl; s_cn[e] = c;
;         for (int i = 0; i < nt; ++i) s_te[excl + i] = (unsigned char)e;
; template <int layer>
; __device__ __forceinline__ void ph_gateup(LAS unsigned char* lds) {
;     PH_BEGIN;
;     moe_prefix(lds, WSP(unsigned, WS_CTL) + (layer == 0 ? CW_CNT0 : CW_CNT1));
.Lgbd_7:
.LBB0_863:
	s_or_b64 exec, exec, s[4:5]
	s_mov_b32 s0, 30
	s_waitcnt lgkmcnt(0)
	s_barrier
	s_ashr_i32 s1, s0, 31
	s_lshl_b64 s[0:1], s[0:1], 3
	s_add_u32 s0, s80, s0
	s_addc_u32 s1, s81, s1
	s_load_dwordx2 s[12:13], s[0:1], 0x0
	v_mov_b32_e32 v1, v0
	s_mov_b32 s36, s78
	s_mov_b32 s1, s79
	v_mov_b32_e32 v6, v0
	s_nop 0
	v_cmp_gt_i32_e32 vcc, 64, v6
	s_and_saveexec_b64 s[4:5], vcc
	s_cbranch_execz .LBB0_893
	v_ashrrev_i32_e32 v7, 31, v6
	s_waitcnt lgkmcnt(0)
	v_lshl_add_u64 v[2:3], v[6:7], 2, s[12:13]
	v_add_co_u32_e32 v2, vcc, 0x1000, v2
	v_lshl_add_u32 v4, v6, 2, 0
	s_nop 0
	v_addc_co_u32_e32 v3, vcc, 0, v3, vcc
	global_load_dword v2, v[2:3], off
	v_mbcnt_hi_u32_b32 v3, -1, v236
	v_and_b32_e32 v7, 64, v3
	v_add_u32_e32 v1, -1, v3
	v_cmp_lt_i32_e32 vcc, v1, v7
	v_add_u32_e32 v5, -2, v3
	v_add_u32_e32 v8, -4, v3
	v_cndmask_b32_e32 v1, v1, v3, vcc
	v_lshlrev_b32_e32 v10, 2, v1
	v_cmp_lt_i32_e32 vcc, v5, v7
	v_add_u32_e32 v9, -8, v3
	v_add_u32_e32 v13, -16, v3
	v_cndmask_b32_e32 v5, v5, v3, vcc
	v_cmp_lt_i32_e32 vcc, 0, v6
	v_lshlrev_b32_e32 v5, 2, v5
	v_subrev_u32_e32 v14, 32, v3
	v_add_u32_e32 v16, 0x26c40, v4
	v_add_u32_e32 v4, 0x26d50, v4
	s_waitcnt vmcnt(0)
	v_add_u32_e32 v1, 0xff, v2
	v_ashrrev_i32_e32 v1, 8, v1
	ds_bpermute_b32 v10, v10, v1
	ds_write_b32 v4, v2
	s_waitcnt lgkmcnt(1)
	v_cndmask_b32_e32 v10, 0, v10, vcc
	v_add_u32_e32 v12, v10, v1
	ds_bpermute_b32 v5, v5, v12
	v_cmp_lt_i32_e32 vcc, v8, v7
	s_nop 1
	v_cndmask_b32_e32 v8, v8, v3, vcc
	v_cmp_lt_i32_e32 vcc, 1, v6
	v_lshlrev_b32_e32 v8, 2, v8
	s_waitcnt lgkmcnt(0)
	v_cndmask_b32_e32 v11, 0, v5, vcc
	v_add_u32_e32 v5, v11, v12
	ds_bpermute_b32 v8, v8, v5
	v_cmp_lt_i32_e32 vcc, v9, v7
	s_nop 1
	v_cndmask_b32_e32 v9, v9, v3, vcc
	v_cmp_lt_i32_e32 vcc, 3, v6
	v_lshlrev_b32_e32 v9, 2, v9
	s_waitcnt lgkmcnt(0)
	v_cndmask_b32_e32 v12, 0, v8, vcc
	v_add_u32_e32 v5, v12, v5
	ds_bpermute_b32 v8, v9, v5
	v_cmp_lt_i32_e32 vcc, v13, v7
	s_nop 1
	v_cndmask_b32_e32 v9, v13, v3, vcc
	v_cmp_lt_i32_e32 vcc, 7, v6
	v_lshlrev_b32_e32 v9, 2, v9
	s_waitcnt lgkmcnt(0)
	v_cndmask_b32_e32 v13, 0, v8, vcc
	v_add_u32_e32 v5, v13, v5
	ds_bpermute_b32 v8, v9, v5
	v_cmp_lt_i32_e32 vcc, v14, v7
	s_nop 1
	v_cndmask_b32_e32 v3, v14, v3, vcc
	v_cmp_lt_i32_e32 vcc, 15, v6
	v_lshlrev_b32_e32 v3, 2, v3
	s_waitcnt lgkmcnt(0)
	v_cndmask_b32_e32 v14, 0, v8, vcc
	v_add_u32_e32 v5, v14, v5
	ds_bpermute_b32 v3, v3, v5
	v_cmp_lt_i32_e32 vcc, 31, v6
	v_sub_u32_e32 v2, v5, v1
	s_waitcnt lgkmcnt(0)
	v_cndmask_b32_e32 v15, 0, v3, vcc
	v_add_u32_e32 v2, v2, v15
	v_cmp_lt_i32_e32 vcc, 0, v1
	ds_write_b32 v16, v2
	s_and_saveexec_b64 s[6:7], vcc
	s_cbranch_execz .LBB0_877
	v_cmp_lt_u32_e32 vcc, 7, v1
	s_mov_b64 s[10:11], -1
	v_mov_b32_e32 v2, 0
	s_and_saveexec_b64 s[8:9], vcc
	s_cbranch_execz .LBB0_874
	s_mov_b32 s0, 0x4040404
	v_add_u32_e32 v2, -8, v1
	v_perm_b32 v8, v6, v6, s0
	v_lshrrev_b32_e32 v3, 3, v2
	v_mov_b32_e32 v9, v8
	v_add_u32_e32 v16, 1, v3
	v_cmp_lt_u32_e32 vcc, 55, v2
	v_mov_b32_e32 v19, 0
	s_and_saveexec_b64 s[10:11], vcc
	s_cbranch_execz .LBB0_870
	v_add3_u32 v2, v10, v15, v14
	v_add3_u32 v2, v2, v13, v12
	v_and_b32_e32 v17, 0x3ffffff8, v16
	s_mov_b32 s0, 0
	v_add3_u32 v18, v2, v11, 0
	s_mov_b64 s[14:15], 0
	v_mov_b32_e32 v2, v8
	v_mov_b32_e32 v3, v8
	v_mov_b32_e32 v4, v8
	v_mov_b32_e32 v5, v8

; __device__ __forceinline__ unsigned xb_add(unsigned* p, unsigned v) { return __hip_atomic_fetch_add(p, v, __ATOMIC_RELAXED, __HIP_MEMORY_SCOPE_AGENT); }
; __device__ __forceinline__ void xcd_barrier(const XcdBarrier& b) {
;     ...
;     if (threadIdx.x == 0) {
;         unsigned* bar = b.bar;
;         __builtin_amdgcn_s_waitcnt(0);
;         unsigned nloc = b.st[0], nx = b.st[1];
;         if (nloc == 0u) { xcd_barrier_complete(bar, b.x, nloc, nx); b.st[0] = nloc; b.st[1] = nx; }
;         const unsigned old = xb_add(&bar[XB_XSUB(b.x)], 1u);
;         const unsigned gen = old / nloc;
;         if (old + 1u == (gen + 1u) * nloc) {
;             __builtin_amdgcn_fence(__ATOMIC_RELEASE, "agent");
;             asm volatile("s_waitcnt vmcnt(0)" ::: "memory");
;             const unsigned og = xb_add(&bar[XB_TOP], 1u);
;             const unsigned tg = og / nx;
;             if (og + 1u == (tg + 1u) * nx) xb_add(&bar[XB_TOPGEN], 1u);
.LBB0_961:
	s_waitcnt lgkmcnt(0)
	v_readfirstlane_b32 s8, v3
	v_readfirstlane_b32 s9, v1
	v_readlane_b32 s0, v252, 4
	s_lshl_b32 s0, s0, 8
	v_readlane_b32 s2, v252, 2
	v_readlane_b32 s3, v252, 3
	s_add_u32 s6, s2, s0
	s_addc_u32 s7, s3, 0
	s_mul_i32 s10, s8, 9
	s_mul_i32 s11, s9, 9
	v_mov_b32_e32 v4, 0x1000
	v_mov_b32_e32 v5, 1
	global_atomic_add v4, v4, v5, s[6:7] offset:1024 sc0
	v_mov_b32_e32 v1, 0x3400
	s_waitcnt vmcnt(0)
	v_readfirstlane_b32 s0, v4
	s_add_u32 s0, s0, 1
	s_cmp_lg_u32 s0, s10
	buffer_inv sc1
	s_cbranch_scc1 .Lgbw_8
	buffer_wbl2 sc1
	s_waitcnt vmcnt(0)
	global_atomic_add v1, v5, s[2:3]

; #define LAS __attribute__((address_space(3)))
; __device__ __forceinline__ int otid() { int t = threadIdx.x; asm volatile("" : "+v"(t)); return t; }
; __device__ __forceinline__ void moe_prefix(LAS unsigned char* lds, const unsigned* cnt) {
;     LAS int* s_ts = (LAS int*)(lds + LDS_TS); LAS int* s_cn = (LAS int*)(lds + LDS_CN);
;     LAS unsigned char* s_te = lds + LDS_TE;
;     LAS int* s_xs = (LAS int*)(lds + LDS_XS);
;     const int tz_ = otid();
;     if (tz_ < 64) { const int e = tz_; const int c = (int)cnt[e], nt = (c + 255) >> 8;
;         int incl = nt;
; #pragma unroll
;         for (int o = 1; o < 64; o <<= 1) { const int up = __shfl_up(incl, o); if (e >= o) incl += up; }
;         const int excl = incl - nt;
;         s_ts[e] = excl; s_cn[e] = c;
;         for (int i = 0; i < nt; ++i) s_te[excl + i] = (unsigned char)e;
; template <int layer>
; __device__ __forceinline__ void ph_down(LAS unsigned char* lds) {
;     PH_BEGIN;
;     moe_prefix(lds, WSP(unsigned, WS_CTL) + (layer == 0 ? CW_CNT0 : CW_CNT1));
.Lgbd_8:
.LBB0_997:
	s_or_b64 exec, exec, s[4:5]
	s_mov_b32 s0, 30
	s_waitcnt lgkmcnt(0)
	s_barrier
	s_ashr_i32 s1, s0, 31
	s_lshl_b64 s[0:1], s[0:1], 3
	s_add_u32 s0, s80, s0
	s_addc_u32 s1, s81, s1
	s_load_dwordx2 s[4:5], s[0:1], 0x0
	v_mov_b32_e32 v1, v0
	s_mov_b32 s16, s78
	s_mov_b32 s1, s79
	v_mov_b32_e32 v6, v0
	s_nop 0
	v_cmp_gt_i32_e32 vcc, 64, v6
	s_and_saveexec_b64 s[6:7], vcc
	s_cbranch_execz .LBB0_1027
	v_ashrrev_i32_e32 v7, 31, v6
	s_waitcnt lgkmcnt(0)
	v_lshl_add_u64 v[2:3], v[6:7], 2, s[4:5]
	v_add_co_u32_e32 v2, vcc, 0x1000, v2
	v_lshl_add_u32 v4, v6, 2, 0
	s_nop 0
	v_addc_co_u32_e32 v3, vcc, 0, v3, vcc
	global_load_dword v2, v[2:3], off
	v_mbcnt_hi_u32_b32 v3, -1, v236
	v_and_b32_e32 v7, 64, v3
	v_add_u32_e32 v1, -1, v3
	v_cmp_lt_i32_e32 vcc, v1, v7
	v_add_u32_e32 v5, -2, v3
	v_add_u32_e32 v8, -4, v3
	v_cndmask_b32_e32 v1, v1, v3, vcc
	v_lshlrev_b32_e32 v10, 2, v1
	v_cmp_lt_i32_e32 vcc, v5, v7
	v_add_u32_e32 v9, -8, v3
	v_add_u32_e32 v13, -16, v3
	v_cndmask_b32_e32 v5, v5, v3, vcc
	v_cmp_lt_i32_e32 vcc, 0, v6
	v_lshlrev_b32_e32 v5, 2, v5
	v_subrev_u32_e32 v14, 32, v3
	v_add_u32_e32 v16, 0x26c40, v4
	v_add_u32_e32 v4, 0x26d50, v4
	s_waitcnt vmcnt(0)
	v_add_u32_e32 v1, 0xff, v2
	v_ashrrev_i32_e32 v1, 8, v1
	ds_bpermute_b32 v10, v10, v1
	ds_write_b32 v4, v2
	s_waitcnt lgkmcnt(1)
	v_cndmask_b32_e32 v10, 0, v10, vcc
	v_add_u32_e32 v12, v10, v1
	ds_bpermute_b32 v5, v5, v12
	v_cmp_lt_i32_e32 vcc, v8, v7
	s_nop 1
	v_cndmask_b32_e32 v8, v8, v3, vcc
	v_cmp_lt_i32_e32 vcc, 1, v6
	v_lshlrev_b32_e32 v8, 2, v8
	s_waitcnt lgkmcnt(0)
	v_cndmask_b32_e32 v11, 0, v5, vcc
	v_add_u32_e32 v5, v11, v12
	ds_bpermute_b32 v8, v8, v5
	v_cmp_lt_i32_e32 vcc, v9, v7
	s_nop 1
	v_cndmask_b32_e32 v9, v9, v3, vcc
	v_cmp_lt_i32_e32 vcc, 3, v6
	v_lshlrev_b32_e32 v9, 2, v9
	s_waitcnt lgkmcnt(0)
	v_cndmask_b32_e32 v12, 0, v8, vcc
	v_add_u32_e32 v5, v12, v5
	ds_bpermute_b32 v8, v9, v5
	v_cmp_lt_i32_e32 vcc, v13, v7
	s_nop 1
	v_cndmask_b32_e32 v9, v13, v3, vcc
	v_cmp_lt_i32_e32 vcc, 7, v6
	v_lshlrev_b32_e32 v9, 2, v9
	s_waitcnt lgkmcnt(0)
	v_cndmask_b32_e32 v13, 0, v8, vcc
	v_add_u32_e32 v5, v13, v5
	ds_bpermute_b32 v8, v9, v5
	v_cmp_lt_i32_e32 vcc, v14, v7
	s_nop 1
	v_cndmask_b32_e32 v3, v14, v3, vcc
	v_cmp_lt_i32_e32 vcc, 15, v6
	v_lshlrev_b32_e32 v3, 2, v3
	s_waitcnt lgkmcnt(0)
	v_cndmask_b32_e32 v14, 0, v8, vcc
	v_add_u32_e32 v5, v14, v5
	ds_bpermute_b32 v3, v3, v5
	v_cmp_lt_i32_e32 vcc, 31, v6
	v_sub_u32_e32 v2, v5, v1
	s_waitcnt lgkmcnt(0)
	v_cndmask_b32_e32 v15, 0, v3, vcc
	v_add_u32_e32 v2, v2, v15
	v_cmp_lt_i32_e32 vcc, 0, v1
	ds_write_b32 v16, v2
	s_and_saveexec_b64 s[8:9], vcc
	s_cbranch_execz .LBB0_1011
	v_cmp_lt_u32_e32 vcc, 7, v1
	s_mov_b64 s[12:13], -1
	v_mov_b32_e32 v2, 0
	s_and_saveexec_b64 s[10:11], vcc
	s_cbranch_execz .LBB0_1008
	s_mov_b32 s0, 0x4040404
	v_add_u32_e32 v2, -8, v1
	v_perm_b32 v8, v6, v6, s0
	v_lshrrev_b32_e32 v3, 3, v2
	v_mov_b32_e32 v9, v8
	v_add_u32_e32 v16, 1, v3
	v_cmp_lt_u32_e32 vcc, 55, v2
	v_mov_b32_e32 v19, 0
	s_and_saveexec_b64 s[12:13], vcc
	s_cbranch_execz .LBB0_1004
	v_add3_u32 v2, v10, v15, v14
	v_add3_u32 v2, v2, v13, v12
	v_and_b32_e32 v17, 0x3ffffff8, v16
	s_mov_b32 s0, 0
	v_add3_u32 v18, v2, v11, 0
	s_mov_b64 s[14:15], 0
	v_mov_b32_e32 v2, v8
	v_mov_b32_e32 v3, v8
	v_mov_b32_e32 v4, v8
	v_mov_b32_e32 v5, v8

; __device__ __forceinline__ unsigned xb_add(unsigned* p, unsigned v) { return __hip_atomic_fetch_add(p, v, __ATOMIC_RELAXED, __HIP_MEMORY_SCOPE_AGENT); }
; __device__ __forceinline__ void xcd_barrier(const XcdBarrier& b) {
;     ...
;     if (threadIdx.x == 0) {
;         unsigned* bar = b.bar;
;         __builtin_amdgcn_s_waitcnt(0);
;         unsigned nloc = b.st[0], nx = b.st[1];
;         if (nloc == 0u) { xcd_barrier_complete(bar, b.x, nloc, nx); b.st[0] = nloc; b.st[1] = nx; }
;         const unsigned old = xb_add(&bar[XB_XSUB(b.x)], 1u);
;         const unsigned gen = old / nloc;
;         if (old + 1u == (gen + 1u) * nloc) {
;             __builtin_amdgcn_fence(__ATOMIC_RELEASE, "agent");
;             asm volatile("s_waitcnt vmcnt(0)" ::: "memory");
;             const unsigned og = xb_add(&bar[XB_TOP], 1u);
;             const unsigned tg = og / nx;
;             if (og + 1u == (tg + 1u) * nx) xb_add(&bar[XB_TOPGEN], 1u);
.LBB0_1105:
	s_waitcnt lgkmcnt(0)
	v_readfirstlane_b32 s8, v3
	v_readfirstlane_b32 s9, v1
	v_readlane_b32 s0, v252, 4
	s_lshl_b32 s0, s0, 8
	v_readlane_b32 s2, v252, 2
	v_readlane_b32 s3, v252, 3
	s_add_u32 s6, s2, s0
	s_addc_u32 s7, s3, 0
	s_mul_i32 s10, s8, 10
	s_mul_i32 s11, s9, 10
	v_mov_b32_e32 v4, 0x1000
	v_mov_b32_e32 v5, 1
	global_atomic_add v4, v4, v5, s[6:7] offset:1024 sc0
	v_mov_b32_e32 v1, 0x3400
	s_waitcnt vmcnt(0)
	v_readfirstlane_b32 s0, v4
	s_add_u32 s0, s0, 1
	s_cmp_lg_u32 s0, s10
	buffer_inv sc1
	s_cbranch_scc1 .Lgbw_9
	buffer_wbl2 sc1
	s_waitcnt vmcnt(0)
	global_atomic_add v1, v5, s[2:3]

; #define LAS __attribute__((address_space(3)))
; __device__ __forceinline__ int otid() { int t = threadIdx.x; asm volatile("" : "+v"(t)); return t; }
; __device__ __forceinline__ void moe_prefix(LAS unsigned char* lds, const unsigned* cnt) {
;     LAS int* s_ts = (LAS int*)(lds + LDS_TS); LAS int* s_cn = (LAS int*)(lds + LDS_CN);
;     LAS unsigned char* s_te = lds + LDS_TE;
;     LAS int* s_xs = (LAS int*)(lds + LDS_XS);
;     const int tz_ = otid();
;     if (tz_ < 64) { const int e = tz_; const int c = (int)cnt[e], nt = (c + 255) >> 8;
;         int incl = nt;
; #pragma unroll
;         for (int o = 1; o < 64; o <<= 1) { const int up = __shfl_up(incl, o); if (e >= o) incl += up; }
;         const int excl = incl - nt;
;         s_ts[e] = excl; s_cn[e] = c;
;         for (int i = 0; i < nt; ++i) s_te[excl + i] = (unsigned char)e;
; template <int MODE>
; __device__ __forceinline__ void norm_rows(LAS unsigned char* lds, float* in, const float* gain, const unsigned* cnt) {
;     PH_BEGIN;
;     bf16* HN = WSP(bf16, WS_HN); const bf16* YS = WSP(bf16, WS_YS); const int* TSLOT = WSP(int, WS_TSLOT); bf16* H1b = WSP(bf16, WS_H1);
;     if (MODE != 0) moe_prefix(lds, cnt);
.Lgbd_9:
.LBB0_1141:
	s_or_b64 exec, exec, s[4:5]
	s_mov_b32 s0, 29
	s_waitcnt lgkmcnt(0)
	s_barrier
	s_mov_b32 s0, 17
	s_ashr_i32 s1, s0, 31
	s_lshl_b64 s[0:1], s[0:1], 3
	s_add_u32 s0, s80, s0
	s_addc_u32 s1, s81, s1
	s_load_dwordx2 s[8:9], s[0:1], 0x0
	s_mov_b32 s0, 30
	s_mov_b32 s10, 30
	s_ashr_i32 s1, s0, 31
	s_lshl_b64 s[0:1], s[0:1], 3
	s_add_u32 s0, s80, s0
	s_addc_u32 s1, s81, s1
	s_load_dwordx2 s[4:5], s[0:1], 0x0
	v_mov_b32_e32 v1, v0
	s_mov_b32 s2, s78
	s_mov_b32 s3, s79
	v_mov_b32_e32 v6, v0
	s_nop 0
	v_cmp_gt_i32_e32 vcc, 64, v6
	s_and_saveexec_b64 s[6:7], vcc
	s_cbranch_execz .LBB0_1171
	s_ashr_i32 s11, s10, 31
	s_lshl_b64 s[0:1], s[10:11], 3
	s_add_u32 s0, s80, s0
	s_addc_u32 s1, s81, s1
	s_load_dwordx2 s[0:1], s[0:1], 0x0
	v_ashrrev_i32_e32 v7, 31, v6
	v_lshl_add_u32 v4, v6, 2, 0
	v_add_u32_e32 v17, 0x26c40, v4
	v_add_u32_e32 v4, 0x26d50, v4
	s_waitcnt lgkmcnt(0)
	v_lshl_add_u64 v[2:3], v[6:7], 2, s[0:1]
	v_add_co_u32_e32 v2, vcc, 0x1000, v2
	s_nop 1
	v_addc_co_u32_e32 v3, vcc, 0, v3, vcc
	global_load_dword v2, v[2:3], off
	v_mbcnt_hi_u32_b32 v3, -1, v236
	v_and_b32_e32 v10, 64, v3
	v_add_u32_e32 v5, -1, v3
	v_cmp_lt_i32_e32 vcc, v5, v10
	v_add_u32_e32 v8, -2, v3
	v_add_u32_e32 v9, -4, v3
	v_cndmask_b32_e32 v5, v5, v3, vcc
	v_lshlrev_b32_e32 v5, 2, v5
	v_cmp_lt_i32_e32 vcc, v8, v10
	v_add_u32_e32 v13, -8, v3
	v_add_u32_e32 v14, -16, v3
	v_cndmask_b32_e32 v8, v8, v3, vcc
	v_cmp_lt_i32_e32 vcc, 0, v6
	v_lshlrev_b32_e32 v8, 2, v8
	v_subrev_u32_e32 v15, 32, v3
	s_waitcnt vmcnt(0)
	v_add_u32_e32 v7, 0xff, v2
	v_ashrrev_i32_e32 v7, 8, v7
	ds_bpermute_b32 v5, v5, v7
	ds_write_b32 v4, v2
	s_waitcnt lgkmcnt(1)
	v_cndmask_b32_e32 v11, 0, v5, vcc
	v_add_u32_e32 v5, v11, v7
	ds_bpermute_b32 v8, v8, v5
	v_cmp_lt_i32_e32 vcc, v9, v10
	s_nop 1
	v_cndmask_b32_e32 v9, v9, v3, vcc
	v_cmp_lt_i32_e32 vcc, 1, v6
	v_lshlrev_b32_e32 v9, 2, v9
	s_waitcnt lgkmcnt(0)
	v_cndmask_b32_e32 v12, 0, v8, vcc
	v_add_u32_e32 v5, v12, v5
	ds_bpermute_b32 v8, v9, v5
	v_cmp_lt_i32_e32 vcc, v13, v10
	s_nop 1
	v_cndmask_b32_e32 v9, v13, v3, vcc
	v_cmp_lt_i32_e32 vcc, 3, v6
	v_lshlrev_b32_e32 v9, 2, v9
	s_waitcnt lgkmcnt(0)
	v_cndmask_b32_e32 v13, 0, v8, vcc
	v_add_u32_e32 v5, v13, v5
	ds_bpermute_b32 v8, v9, v5
	v_cmp_lt_i32_e32 vcc, v14, v10
	s_nop 1
	v_cndmask_b32_e32 v9, v14, v3, vcc
	v_cmp_lt_i32_e32 vcc, 7, v6
	v_lshlrev_b32_e32 v9, 2, v9
	s_waitcnt lgkmcnt(0)
	v_cndmask_b32_e32 v14, 0, v8, vcc
	v_add_u32_e32 v5, v14, v5
	ds_bpermute_b32 v8, v9, v5
	v_cmp_lt_i32_e32 vcc, v15, v10
	s_nop 1
	v_cndmask_b32_e32 v3, v15, v3, vcc
	v_cmp_lt_i32_e32 vcc, 15, v6
	v_lshlrev_b32_e32 v3, 2, v3
	s_waitcnt lgkmcnt(0)
	v_cndmask_b32_e32 v15, 0, v8, vcc
	v_add_u32_e32 v5, v15, v5
	ds_bpermute_b32 v3, v3, v5
	v_cmp_lt_i32_e32 vcc, 31, v6
	v_sub_u32_e32 v2, v5, v7
	s_waitcnt lgkmcnt(0)
	v_cndmask_b32_e32 v16, 0, v3, vcc
	v_add_u32_e32 v2, v2, v16
	v_cmp_lt_i32_e32 vcc, 0, v7
	ds_write_b32 v17, v2
	s_and_saveexec_b64 s[10:11], vcc
	s_cbranch_execz .LBB0_1155
	v_cmp_lt_u32_e32 vcc, 7, v7
	s_mov_b64 s[14:15], -1
	v_mov_b32_e32 v2, 0
	s_and_saveexec_b64 s[12:13], vcc
	s_cbranch_execz .LBB0_1152
	s_mov_b32 s0, 0x4040404
	v_add_u32_e32 v2, -8, v7
	v_perm_b32 v8, v6, v6, s0
	v_lshrrev_b32_e32 v3, 3, v2
	v_mov_b32_e32 v9, v8
	v_add_u32_e32 v17, 1, v3
	v_cmp_lt_u32_e32 vcc, 55, v2
	v_mov_b32_e32 v20, 0
	s_and_saveexec_b64 s[14:15], vcc
	s_cbranch_execz .LBB0_1148
	v_add3_u32 v2, v11, v16, v15
	v_add3_u32 v2, v2, v14, v13
	v_and_b32_e32 v18, 0x3ffffff8, v17
	s_mov_b32 s0, 0
	v_add3_u32 v19, v2, v12, 0
	s_mov_b64 s[16:17], 0
	v_mov_b32_e32 v2, v8
	v_mov_b32_e32 v3, v8
	v_mov_b32_e32 v4, v8
	v_mov_b32_e32 v5, v8

; __device__ __forceinline__ unsigned xb_add(unsigned* p, unsigned v) { return __hip_atomic_fetch_add(p, v, __ATOMIC_RELAXED, __HIP_MEMORY_SCOPE_AGENT); }
; __device__ __forceinline__ void xcd_barrier(const XcdBarrier& b) {
;     ...
;     if (threadIdx.x == 0) {
;         unsigned* bar = b.bar;
;         __builtin_amdgcn_s_waitcnt(0);
;         unsigned nloc = b.st[0], nx = b.st[1];
;         if (nloc == 0u) { xcd_barrier_complete(bar, b.x, nloc, nx); b.st[0] = nloc; b.st[1] = nx; }
;         const unsigned old = xb_add(&bar[XB_XSUB(b.x)], 1u);
;         const unsigned gen = old / nloc;
;         if (old + 1u == (gen + 1u) * nloc) {
;             __builtin_amdgcn_fence(__ATOMIC_RELEASE, "agent");
;             asm volatile("s_waitcnt vmcnt(0)" ::: "memory");
;             const unsigned og = xb_add(&bar[XB_TOP], 1u);
;             const unsigned tg = og / nx;
;             if (og + 1u == (tg + 1u) * nx) xb_add(&bar[XB_TOPGEN], 1u);
.LBB0_1192:
	s_waitcnt lgkmcnt(0)
	v_readfirstlane_b32 s8, v3
	v_readfirstlane_b32 s9, v1
	v_readlane_b32 s0, v252, 4
	s_lshl_b32 s0, s0, 8
	v_readlane_b32 s2, v252, 2
	v_readlane_b32 s3, v252, 3
	s_add_u32 s6, s2, s0
	s_addc_u32 s7, s3, 0
	s_mul_i32 s10, s8, 11
	s_mul_i32 s11, s9, 11
	v_mov_b32_e32 v4, 0x1000
	v_mov_b32_e32 v5, 1
	global_atomic_add v4, v4, v5, s[6:7] offset:1024 sc0
	v_mov_b32_e32 v1, 0x3400
	s_waitcnt vmcnt(0)
	v_readfirstlane_b32 s0, v4
	s_add_u32 s0, s0, 1
	s_cmp_lg_u32 s0, s10
	buffer_inv sc1
	s_cbranch_scc1 .Lgbw_10
	buffer_wbl2 sc1
	s_waitcnt vmcnt(0)
	global_atomic_add v1, v5, s[2:3]

;     __device__ __forceinline__ bool next(int i, SkUnit& u) const { const int L = i * G + c; if (L >= (T / 256) * 4) return false; u.pm = L >> 2; u.ks = L & 3; return true; }
; #define INF(i) ((const float*)arg_ptr(i))
;     __device__ __forceinline__ bool next(int i, DUnit& u) const {
;         long L = (long)i * G + c; const int nwg0 = nM * nN0, nwg1 = nM * nN1;
;         int nN, nwg; if (L < nwg0) { u.p = 0; nN = nN0; nwg = nwg0; } else { L -= nwg0; if (L >= nwg1) return false; u.p = 1; nN = nN1; nwg = nwg1; }
;         int wgid = (int)L; { const int q = nwg / NXCD, r = nwg % NXCD, xcd = wgid % NXCD, off = wgid / NXCD; wgid = (xcd < r ? xcd * (q + 1) : r * (q + 1) + (xcd - r) * q) + off; }
;         const int nig = WGM * nN, gid = wgid / nig, fm = gid * WGM, gsz = (nM - fm) < WGM ? (nM - fm) : WGM;
; template <int layer>
; __device__ __forceinline__ void ph_gemm_z(LAS unsigned char* lds) {
;     ...
;         fg::DenseSched S{HN, WSP(bf16, WS_W_IN1T), 32, nullptr, nullptr, 0, DM, G, bx};
;         const float* gk = INF(20) + 128;
;         auto E = [=](const f32x4 (&acc)[2][2][4][2], const fg::DUnit& u, int wr, int wc, int fr, int fq) {
.Lgbd_10:
.LBB0_1228:
	s_or_b64 exec, exec, s[4:5]
	s_mov_b32 s0, 30
	s_waitcnt lgkmcnt(0)
	s_barrier
	s_ashr_i32 s1, s0, 31
	s_lshl_b64 s[0:1], s[0:1], 3
	s_add_u32 s0, s80, s0
	s_addc_u32 s1, s81, s1
	s_load_dwordx2 s[6:7], s[0:1], 0x0
	v_mov_b32_e32 v1, v0
	s_mov_b32 s0, s78
	s_mov_b32 s1, s79
	s_mov_b32 s2, 20
	s_ashr_i32 s3, s2, 31
	s_lshl_b64 s[2:3], s[2:3], 3
	s_add_u32 s4, s80, s2
	s_addc_u32 s5, s81, s3
	s_ashr_i32 s22, s1, 31
	v_mov_b32_e32 v1, v0
	s_cmpk_lt_i32 s1, 0x800
	s_cselect_b64 s[8:9], -1, 0
	s_cmpk_gt_i32 s1, 0x7ff
	v_readfirstlane_b32 s14, v1
	s_cbranch_scc1 .LBB0_1230
	s_lshr_b32 s2, s22, 29
	s_add_i32 s2, s1, s2
	s_ashr_i32 s3, s2, 3
	s_and_b32 s2, s2, -8
	s_sub_i32 s2, s1, s2
	s_lshr_b32 s10, s2, 31
	s_bitset1_b32 s10, 8
	s_mul_i32 s2, s10, s2
	s_add_i32 s2, s2, s3
	s_ashr_i32 s3, s2, 31
	s_lshr_b32 s3, s3, 24
	s_add_i32 s3, s2, s3
	s_ashr_i32 s10, s3, 8
	s_lshl_b32 s10, s10, 3
	s_sub_i32 s11, 64, s10
	s_min_u32 s11, s11, 8
	s_and_b32 s3, s3, 0xffffff00
	s_sub_i32 s12, s2, s3
	v_cvt_f32_ubyte0_e32 v3, s11
	v_cvt_f32_i32_e32 v2, s12
	v_rcp_iflag_f32_e32 v4, v3
	s_ashr_i32 s2, s12, 30
	s_or_b32 s13, s2, 1
	v_mul_f32_e32 v4, v2, v4
	v_trunc_f32_e32 v4, v4
	v_fma_f32 v2, -v4, v3, v2
	v_cvt_i32_f32_e32 v4, v4
	v_cmp_ge_f32_e64 s[2:3], |v2|, v3
	s_and_b64 s[2:3], s[2:3], exec
	s_cselect_b32 s2, s13, 0
	v_readfirstlane_b32 s3, v4
	s_add_i32 s2, s3, s2
	s_sext_i32_i16 s44, s2
	s_mul_i32 s2, s2, s11
	s_sub_i32 s2, s12, s2
	s_sext_i32_i16 s2, s2
	s_add_i32 s42, s10, s2

; __device__ __forceinline__ unsigned xb_add(unsigned* p, unsigned v) { return __hip_atomic_fetch_add(p, v, __ATOMIC_RELAXED, __HIP_MEMORY_SCOPE_AGENT); }
; __device__ __forceinline__ void xcd_barrier(const XcdBarrier& b) {
;     ...
;     if (threadIdx.x == 0) {
;         unsigned* bar = b.bar;
;         __builtin_amdgcn_s_waitcnt(0);
;         unsigned nloc = b.st[0], nx = b.st[1];
;         if (nloc == 0u) { xcd_barrier_complete(bar, b.x, nloc, nx); b.st[0] = nloc; b.st[1] = nx; }
;         const unsigned old = xb_add(&bar[XB_XSUB(b.x)], 1u);
;         const unsigned gen = old / nloc;
;         if (old + 1u == (gen + 1u) * nloc) {
;             __builtin_amdgcn_fence(__ATOMIC_RELEASE, "agent");
;             asm volatile("s_waitcnt vmcnt(0)" ::: "memory");
;             const unsigned og = xb_add(&bar[XB_TOP], 1u);
;             const unsigned tg = og / nx;
;             if (og + 1u == (tg + 1u) * nx) xb_add(&bar[XB_TOPGEN], 1u);
.LBB0_1314:
	s_waitcnt lgkmcnt(0)
	v_readfirstlane_b32 s8, v3
	v_readfirstlane_b32 s9, v1
	v_readlane_b32 s0, v252, 4
	s_lshl_b32 s0, s0, 8
	v_readlane_b32 s2, v252, 2
	v_readlane_b32 s3, v252, 3
	s_add_u32 s6, s2, s0
	s_addc_u32 s7, s3, 0
	s_mul_i32 s10, s8, 12
	s_mul_i32 s11, s9, 12
	v_mov_b32_e32 v4, 0x1000
	v_mov_b32_e32 v5, 1
	global_atomic_add v4, v4, v5, s[6:7] offset:1024 sc0
	v_mov_b32_e32 v1, 0x3400
	s_waitcnt vmcnt(0)
	v_readfirstlane_b32 s0, v4
	s_add_u32 s0, s0, 1
	s_cmp_lg_u32 s0, s10
	buffer_inv sc1
	s_cbranch_scc1 .Lgbw_11
	buffer_wbl2 sc1
	s_waitcnt vmcnt(0)
	global_atomic_add v1, v5, s[2:3]

; #define LAS __attribute__((address_space(3)))
; #define INF(i) ((const float*)arg_ptr(i))
; __device__ __forceinline__ void ph_fox_prep(LAS unsigned char* lds) {
;     PH_BEGIN;
;     const float* PF = WSP(float, WS_PF); float* CB = WSP(float, WS_C); const float* fb = INF(19);
;     LAS float* wtot = (LAS float*)lds;
;     for (int bh = bx; bh < NB * NH; bh += G) {
;         const int b = bh >> 4, h = bh & 15; const float bias = fb[h];
;         const float* pf = PF + (size_t)h * T + (size_t)b * SEQ + tid * 8;
;         f32x4 pq[4][2];
; #pragma unroll
;         for (int ks = 0; ks < 4; ++ks) { pq[ks][0] = *(const f32x4*)(pf + (size_t)ks * 16 * T); pq[ks][1] = *(const f32x4*)(pf + (size_t)ks * 16 * T + 4); }
;         float v[8]; float run = 0.f;
; #pragma unroll
;         for (int i = 0; i < 8; ++i) {
;             const float xx = ((pq[0][i >> 2][i & 3] + pq[1][i >> 2][i & 3]) + (pq[2][i >> 2][i & 3] + pq[3][i >> 2][i & 3])) + bias;
;             run += fminf(xx, 0.f) - log1pf(expf(-fabsf(xx))); v[i] = run; }
;         float incl = run;
; #pragma unroll
;         for (int o = 1; o < 64; o <<= 1) { const float up = __shfl_up(incl, o); if (lane >= o) incl += up; }
.Lgbd_11:
.LBB0_1350:
	s_or_b64 exec, exec, s[4:5]
	s_mov_b32 s6, 30
	s_waitcnt lgkmcnt(0)
	v_mov_b32_e32 v1, v0
	s_mov_b32 s0, s78
	s_mov_b32 s34, s79
	s_barrier
	s_mov_b32 s4, 19
	s_cmp_gt_i32 s34, 63
	s_cbranch_scc1 .LBB0_1365
	s_ashr_i32 s7, s6, 31
	s_lshl_b64 s[2:3], s[6:7], 3
	s_add_u32 s2, s80, s2
	s_addc_u32 s3, s81, s3
	s_load_dwordx2 s[6:7], s[2:3], 0x0
	v_lshlrev_b32_e32 v34, 3, v1
	v_ashrrev_i32_e32 v35, 31, v34
	v_mbcnt_hi_u32_b32 v6, -1, v236
	v_and_b32_e32 v7, 64, v6
	s_waitcnt lgkmcnt(0)
	s_add_u32 s1, s6, 0x6d700000
	s_addc_u32 s2, s7, 0
	v_lshl_add_u64 v[2:3], v[34:35], 2, s[6:7]
	s_mov_b64 s[6:7], 0x5e200000
	v_lshl_add_u64 v[36:37], v[2:3], 0, s[6:7]
	v_add_u32_e32 v2, -1, v6
	v_cmp_lt_i32_e64 s[6:7], v2, v7
	s_ashr_i32 s5, s4, 31
	s_lshl_b64 s[4:5], s[4:5], 3
	v_cndmask_b32_e64 v2, v2, v6, s[6:7]
	v_lshlrev_b32_e32 v38, 2, v2
	v_add_u32_e32 v2, -2, v6
	v_cmp_lt_i32_e64 s[8:9], v2, v7
	s_add_u32 s4, s80, s4
	s_addc_u32 s5, s81, s5
	v_cndmask_b32_e64 v2, v2, v6, s[8:9]
	v_lshlrev_b32_e32 v39, 2, v2
	v_add_u32_e32 v2, -4, v6
	v_cmp_lt_i32_e64 s[10:11], v2, v7
	s_load_dwordx2 s[36:37], s[4:5], 0x0
	v_ashrrev_i32_e32 v4, 6, v1
	v_cndmask_b32_e64 v2, v2, v6, s[10:11]
	v_lshlrev_b32_e32 v40, 2, v2
	v_add_u32_e32 v2, -8, v6
	v_cmp_lt_i32_e64 s[12:13], v2, v7
	v_and_b32_e32 v5, 63, v1
	v_and_b32_e32 v44, 7, v4
	v_cndmask_b32_e64 v2, v2, v6, s[12:13]
	v_lshlrev_b32_e32 v41, 2, v2
	v_add_u32_e32 v2, -16, v6
	v_cmp_lt_i32_e64 s[14:15], v2, v7
	v_cmp_eq_u32_e32 vcc, 63, v5
	v_lshl_add_u32 v1, v4, 2, 0
	v_cndmask_b32_e64 v2, v2, v6, s[14:15]
	v_lshlrev_b32_e32 v42, 2, v2
	v_subrev_u32_e32 v2, 32, v6
	v_cmp_lt_i32_e64 s[16:17], v2, v7
	v_cmp_lt_i32_e64 s[4:5], 0, v4
	v_cmp_eq_u32_e64 s[6:7], 0, v5
	v_cndmask_b32_e64 v2, v2, v6, s[16:17]
	v_cmp_gt_u32_e64 s[8:9], 2, v5
	v_cmp_gt_u32_e64 s[10:11], 4, v5
	v_cmp_gt_u32_e64 s[12:13], 8, v5
	v_cmp_gt_u32_e64 s[14:15], 16, v5
	v_lshlrev_b32_e32 v43, 2, v2
	v_cmp_gt_u32_e64 s[16:17], 32, v5
	v_cmp_lt_u32_e64 s[18:19], 7, v4
	v_and_b32_e32 v45, 0x7ffffff8, v4
	v_cmp_ne_u32_e64 s[20:21], 0, v44
	s_mov_b64 s[38:39], 0x100000
	s_mov_b32 s3, 0x100000
	s_mov_b64 s[40:41], 0x200000
	s_mov_b32 s22, 0x200000
	s_mov_b64 s[42:43], 0x300000
	s_mov_b32 s23, 0x300000
	s_mov_b32 s44, 0xbfb8aa3b
	s_mov_b32 s26, 0xb2a5705f
	s_mov_b32 s27, 0x42ce8ed0
	s_mov_b32 s28, 0xc2b17218
	s_mov_b32 s29, 0x7f800000
	v_mov_b32_e32 v46, 0x7f800000
	s_mov_b32 s30, 0x3f2aaaab
	v_mov_b32_e32 v47, 0x3ecc95a3
	s_mov_b32 s31, 0x3f317218
	s_mov_b32 s33, 0x33800000
	s_branch .LBB0_1354

; __device__ __forceinline__ unsigned xb_add(unsigned* p, unsigned v) { return __hip_atomic_fetch_add(p, v, __ATOMIC_RELAXED, __HIP_MEMORY_SCOPE_AGENT); }
; __device__ __forceinline__ void xcd_barrier(const XcdBarrier& b) {
;     ...
;     if (threadIdx.x == 0) {
;         unsigned* bar = b.bar;
;         __builtin_amdgcn_s_waitcnt(0);
;         unsigned nloc = b.st[0], nx = b.st[1];
;         if (nloc == 0u) { xcd_barrier_complete(bar, b.x, nloc, nx); b.st[0] = nloc; b.st[1] = nx; }
;         const unsigned old = xb_add(&bar[XB_XSUB(b.x)], 1u);
;         const unsigned gen = old / nloc;
;         if (old + 1u == (gen + 1u) * nloc) {
;             __builtin_amdgcn_fence(__ATOMIC_RELEASE, "agent");
;             asm volatile("s_waitcnt vmcnt(0)" ::: "memory");
;             const unsigned og = xb_add(&bar[XB_TOP], 1u);
;             const unsigned tg = og / nx;
;             if (og + 1u == (tg + 1u) * nx) xb_add(&bar[XB_TOPGEN], 1u);
.LBB0_1381:
	s_waitcnt lgkmcnt(0)
	v_readfirstlane_b32 s8, v3
	v_readfirstlane_b32 s9, v1
	v_readlane_b32 s0, v252, 4
	s_lshl_b32 s0, s0, 8
	v_readlane_b32 s2, v252, 2
	v_readlane_b32 s3, v252, 3
	s_add_u32 s6, s2, s0
	s_addc_u32 s7, s3, 0
	s_mul_i32 s10, s8, 13
	s_mul_i32 s11, s9, 13
	v_mov_b32_e32 v4, 0x1000
	v_mov_b32_e32 v5, 1
	global_atomic_add v4, v4, v5, s[6:7] offset:1024 sc0
	v_mov_b32_e32 v1, 0x3400
	s_waitcnt vmcnt(0)
	v_readfirstlane_b32 s0, v4
	s_add_u32 s0, s0, 1
	s_cmp_lg_u32 s0, s10
	buffer_inv sc1
	s_cbranch_scc1 .Lgbw_12
	buffer_wbl2 sc1
	s_waitcnt vmcnt(0)
	global_atomic_add v1, v5, s[2:3]

; template <int layer>
; __device__ __forceinline__ void attn_phase(LAS unsigned char* lds) {
;     PH_BEGIN;
;     constexpr int DK = layer == 0 ? 192 : 128, NQ = DK / 16, CPR = DK / 8, NKC = KVB * CPR / NTHREADS;
;     constexpr int SHM_K = KVB * DK * 2;
;     constexpr int OFF_V = 0, OFF_K = 2 * SHM_V, OFF_WS = OFF_K + 2 * SHM_K, OFF_CB = OFF_WS + NWAVES * 256, OFF_CV = 86016;
;     static_assert(OFF_CB + 512 <= OFF_CV && OFF_CV + NWAVES * 8192 <= LDS_BARW, "attention LDS map");
;     constexpr float C2 = (layer == 0 ? 0.07216878364870322f : 0.08838834764831845f) * 1.4426950408889634f;
;     constexpr int QLD = layer == 0 ? 3072 : 8192, QHS = layer == 0 ? 192 : 128, KLD = layer == 0 ? 4096 : 8192, KC0 = layer == 0 ? 0 : 2048, KHS = layer == 0 ? 256 : 128, VC0 = layer == 0 ? 128 : 4096;
;     const bf16* Qs = layer == 0 ? WSP(bf16, WS_QL) : WSP(bf16, WS_Z); const bf16* Ks = layer == 0 ? WSP(bf16, WS_KVL) : WSP(bf16, WS_Z); const bf16* KRs = WSP(bf16, WS_KR); bf16* Ob = WSP(bf16, WS_O);
;     const float* qkg = INF(layer == 0 ? 8 : 20); const int* positions = (const int*)arg_ptr(1);
;     const float* CBg = WSP(float, WS_C); const bf16* Zg = WSP(bf16, WS_Z);
;     const int wid = __builtin_amdgcn_readfirstlane(tid >> 6), r32 = lane & 31, hi = lane >> 5;
;     auto koff_n = [](int tk, int j) { const int ci = j * 256 + tk, row = ci >> 4, pc = ci & 15, lc = pc ^ (row & 7); return (unsigned)(row * KLD + lc * 8) * 2u; };
;     auto koff_r = [](int tk, int j) { const int ci = j * 256 + tk, row = ci >> 3, pc = ci & 7, lc = pc ^ (row & 7); return (unsigned)(row * 64 + lc * 8) * 2u; };
;     auto voff_f = [](int tk, int j) { const int ci = j * 256 + tk, st = ci >> 5, w = ci & 31, kk = (st >> 2) * 8 + (w >> 2), key = (kk & ~0xC) | ((kk & 4) << 1) | ((kk & 8) >> 1), c = (st & 3) * 32 + (w & 3) * 8;
;         return (unsigned)(key * KLD + c) * 2u; };
;     const int tkp = (tid - 256) & 255; const unsigned kof0 = koff_n(tkp, 0), vof0 = voff_f(tkp, 0), rof0 = koff_r(tkp, 0);
;     const int kbn = r32 * 256 + ((hi * 16) ^ ((r32 & 7) << 4)), kbr0 = 16384 + r32 * 128 + ((hi * 16) ^ ((r32 & 7) << 4));
;     const unsigned ldsb = (unsigned)(uintptr_t)lds;
;     const int vb0 = (int)(unsigned)(uintptr_t)(lds + OFF_V) + v_rd_base(lane);
;     LAS float* wsl = (LAS float*)(lds + OFF_WS) + wid * 64; LAS float* li_l = wsl; LAS float* al_l = wsl + 32;
.Lgbd_12:
.LBB0_1417:
	s_or_b64 exec, exec, s[4:5]
	s_mov_b32 s0, 30
	s_waitcnt lgkmcnt(0)
	s_barrier
	s_ashr_i32 s1, s0, 31
	s_lshl_b64 s[0:1], s[0:1], 3
	s_add_u32 s0, s80, s0
	s_addc_u32 s1, s81, s1
	s_load_dwordx2 s[4:5], s[0:1], 0x0
	v_mov_b32_e32 v4, v0
	s_mov_b32 s2, s78
	s_mov_b32 s9, s79
	s_mov_b32 s6, 20
	s_mov_b32 s0, 1
	s_mov_b32 s17, 0
	v_readfirstlane_b32 s0, v4
	s_ashr_i32 s3, s0, 6
	s_mov_b32 s0, 27
	s_ashr_i32 s1, s0, 31
	s_lshl_b64 s[0:1], s[0:1], 3
	s_add_u32 s0, s80, s0
	s_addc_u32 s1, s81, s1
	s_load_dwordx2 s[12:13], s[0:1], 0x0
	s_mov_b32 s0, 28
	s_ashr_i32 s1, s0, 31
	s_lshl_b64 s[0:1], s[0:1], 3
	s_add_u32 s0, s80, s0
	s_addc_u32 s1, s81, s1
	s_waitcnt lgkmcnt(0)
	s_add_u32 s60, s4, 0x3e00000
	s_addc_u32 s61, s5, 0
	s_add_u32 s62, s4, 0x13e00000
	s_load_dwordx2 s[14:15], s[0:1], 0x0
	s_addc_u32 s63, s5, 0
	s_lshl_b32 s0, s9, 2
	s_add_i32 s73, s3, s0
	s_lshl_b32 s0, s3, 14
	s_and_b32 s0, s0, 0xc000
	s_add_i32 s10, s0, 0
	s_lshl_b32 s64, s2, 2
	s_add_i32 s65, s10, 0x15000
	s_cmpk_gt_i32 s9, 0x1ff
	s_mov_b32 s70, -1
	v_writelane_b32 v252, s2, 9
	s_cbranch_scc1 .LBB0_1477
	s_add_u32 s18, s4, 0x1fe00000
	s_addc_u32 s19, s5, 0
	v_lshrrev_b32_e32 v1, 4, v4
	v_and_b32_e32 v2, 15, v4
	s_add_u32 s0, s4, 0x42000000
	v_bitop3_b32 v1, v1, v2, 15 bitop3:0x6c
	v_lshlrev_b32_e32 v2, 10, v4
	v_writelane_b32 v252, s0, 13
	s_addc_u32 s0, s5, 0
	s_ashr_i32 s7, s6, 31
	v_and_b32_e32 v2, 0x3c000, v2
	v_writelane_b32 v252, s0, 14
	s_lshl_b64 s[0:1], s[6:7], 3
	v_lshl_or_b32 v1, v1, 4, v2
	v_lshrrev_b32_e32 v2, 5, v4
	v_lshrrev_b32_e32 v5, 1, v4
	s_add_u32 s0, s80, s0
	v_and_b32_e32 v2, 4, v2
	v_bfe_u32 v3, v4, 2, 2
	v_and_b32_e32 v5, 8, v5
	s_addc_u32 s1, s81, s1
	v_or3_b32 v2, v3, v5, v2
	v_and_b32_e32 v3, 0x60, v4
	v_lshlrev_b32_e32 v5, 3, v4
	s_add_u32 s2, s4, 0x5e200000
	v_and_or_b32 v3, v5, 24, v3
	v_writelane_b32 v252, s2, 15
	s_addc_u32 s2, s5, 0
	v_bfe_u32 v7, v4, 5, 1
	v_lshlrev_b32_e32 v3, 1, v3
	s_lshl_b32 s6, s3, 5
	v_and_b32_e32 v132, 31, v4
	v_lshl_or_b32 v133, v2, 14, v3
	v_bitop3_b32 v2, v7, v4, 15 bitop3:0x78
	s_cmp_gt_i32 s3, 3
	v_writelane_b32 v252, s2, 16
	v_lshlrev_b32_e32 v2, 4, v2
	v_lshlrev_b32_e32 v3, 7, v132
	s_movk_i32 s2, 0x4000
	s_cselect_b64 s[20:21], -1, 0
	s_lshl_b32 s76, s3, 10
	v_and_b32_e32 v6, 63, v4
	s_load_dwordx2 s[0:1], s[0:1], 0x0
	v_or3_b32 v173, v2, v3, s2
	v_lshlrev_b32_e32 v3, 4, v4
	s_add_i32 s76, s76, 0
	v_lshl_or_b32 v172, v132, 8, v2
	v_xor_b32_e32 v206, 32, v172
	v_xor_b32_e32 v207, 64, v172
	v_xor_b32_e32 v237, 0x60, v172
	v_xor_b32_e32 v244, 0x80, v172
	v_xor_b32_e32 v245, 0xa0, v172
	v_xor_b32_e32 v246, 0xc0, v172
	v_xor_b32_e32 v247, 0xe0, v172
	v_lshlrev_b32_e32 v2, 3, v6
	v_and_b32_e32 v3, 0xc0, v3
	v_lshlrev_b32_e32 v5, 1, v4
	s_add_i32 s77, s76, 0x7000
	s_add_i32 s78, s76, 0xfffff000
	v_and_or_b32 v3, v2, 24, v3
	v_and_b32_e32 v5, 32, v5
	v_and_b32_e32 v2, 0x100, v2
	s_cmp_eq_u32 s3, 4
	v_or3_b32 v2, v3, v5, v2
	v_mov_b32_e32 v3, 0
	v_writelane_b32 v252, s18, 26
	s_cselect_b64 s[4:5], -1, 0
	s_add_i32 s79, s76, 0xb000
	s_add_i32 s80, s76, 0x3000
	v_writelane_b32 v252, s19, 27
	v_and_b32_e32 v4, 32, v4
	v_mov_b32_e32 v5, v3
	s_cmp_lt_i32 s3, 4
	v_add_u32_e32 v174, 0, v2
	v_lshlrev_b32_e32 v2, 4, v7
	s_waitcnt lgkmcnt(0)
	v_lshl_add_u64 v[136:137], s[0:1], 0, v[4:5]
	v_writelane_b32 v252, s3, 18
	s_cselect_b64 s[24:25], -1, 0
	s_add_i32 s81, 0, 0x10800
	v_mul_i32_i24_e32 v4, -4, v7
	s_add_i32 s83, 0, 0x10900
	s_movk_i32 s74, 0x60
	v_lshl_add_u64 v[134:135], s[18:19], 0, v[2:3]
	v_lshlrev_b32_e32 v175, 2, v6
	v_add_u32_e32 v176, s81, v2
	s_add_i32 s82, s10, 0x17000
	v_add_u32_e32 v177, s83, v2
	v_or_b32_e32 v178, 0x40000, v1
	s_add_i32 s84, s76, 0x8000
	v_or_b32_e32 v179, 0x80000, v1
	s_add_i32 s85, s76, 0x9000
	v_or_b32_e32 v180, 0xc0000, v1
	s_add_i32 s86, s76, 0xa000
	v_or_b32_e32 v181, 0x40000, v133
	v_or_b32_e32 v182, 0x80000, v133
	s_add_i32 s87, s76, 0x1000
	v_or_b32_e32 v183, 0xc0000, v133
	s_add_i32 s88, s76, 0x2000
	s_add_i32 s89, s76, 0xc000
	s_add_i32 s90, s76, 0xd000
	s_add_i32 s91, s76, 0xe000
	s_add_i32 s92, s76, 0x4000
	s_add_i32 s93, s76, 0x5000
	s_add_i32 s94, s76, 0x6000
	s_add_i32 s95, s10, 0x15400
	s_add_i32 s96, s10, 0x15800
	s_add_i32 s97, s10, 0x15c00
	s_add_i32 s30, s10, 0x16000
	s_add_i32 s31, s10, 0x16400
	s_add_i32 s22, s10, 0x16800
	s_add_i32 s23, s10, 0x16c00
	s_add_i32 s28, s10, 0x17400
	s_add_i32 s29, s10, 0x17800
	s_add_i32 s33, s10, 0x17c00
	s_add_i32 s3, s10, 0x18000
	s_add_i32 s2, s10, 0x18400
	s_add_i32 s67, s10, 0x18800
	v_writelane_b32 v252, s10, 17
	s_add_i32 s66, s10, 0x18c00
	v_add3_u32 v184, v4, s6, v132
	v_mov_b32_e32 v185, 0x358637bd
	v_cndmask_b32_e64 v186, 0, 1, s[20:21]
	s_movk_i32 s1, 0x3ff
	s_movk_i32 s0, 0x70
	s_movk_i32 s26, 0x50
	s_mov_b32 s27, 0x42800000
	v_cndmask_b32_e64 v187, 0, 1, s[4:5]
	v_mov_b32_e32 v188, 0x10000
	v_mov_b32_e32 v189, 0xff800000
	v_writelane_b32 v252, s6, 23
	s_branch .LBB0_1420

; __device__ __forceinline__ unsigned xb_add(unsigned* p, unsigned v) { return __hip_atomic_fetch_add(p, v, __ATOMIC_RELAXED, __HIP_MEMORY_SCOPE_AGENT); }
; __device__ __forceinline__ void xcd_barrier(const XcdBarrier& b) {
;     ...
;     if (threadIdx.x == 0) {
;         unsigned* bar = b.bar;
;         __builtin_amdgcn_s_waitcnt(0);
;         unsigned nloc = b.st[0], nx = b.st[1];
;         if (nloc == 0u) { xcd_barrier_complete(bar, b.x, nloc, nx); b.st[0] = nloc; b.st[1] = nx; }
;         const unsigned old = xb_add(&bar[XB_XSUB(b.x)], 1u);
;         const unsigned gen = old / nloc;
;         if (old + 1u == (gen + 1u) * nloc) {
;             __builtin_amdgcn_fence(__ATOMIC_RELEASE, "agent");
;             asm volatile("s_waitcnt vmcnt(0)" ::: "memory");
;             const unsigned og = xb_add(&bar[XB_TOP], 1u);
;             const unsigned tg = og / nx;
;             if (og + 1u == (tg + 1u) * nx) xb_add(&bar[XB_TOPGEN], 1u);
.LBB0_1499:
	s_waitcnt lgkmcnt(0)
	v_readfirstlane_b32 s8, v3
	v_readfirstlane_b32 s9, v1
	v_readlane_b32 s0, v252, 4
	s_lshl_b32 s0, s0, 8
	v_readlane_b32 s2, v252, 2
	v_readlane_b32 s3, v252, 3
	s_add_u32 s6, s2, s0
	s_addc_u32 s7, s3, 0
	s_mul_i32 s10, s8, 14
	s_mul_i32 s11, s9, 14
	v_mov_b32_e32 v4, 0x1000
	v_mov_b32_e32 v5, 1
	global_atomic_add v4, v4, v5, s[6:7] offset:1024 sc0
	v_mov_b32_e32 v1, 0x3400
	s_waitcnt vmcnt(0)
	v_readfirstlane_b32 s0, v4
	s_add_u32 s0, s0, 1
	s_cmp_lg_u32 s0, s10
	buffer_inv sc1
	s_cbranch_scc1 .Lgbw_13
	buffer_wbl2 sc1
	s_waitcnt vmcnt(0)
	global_atomic_add v1, v5, s[2:3]

; #define LAS __attribute__((address_space(3)))
;     __device__ __forceinline__ bool next(int i, SkUnit& u) const { const int L = i * G + c; if (L >= (T / 256) * 4) return false; u.pm = L >> 2; u.ks = L & 3; return true; }
; #define INF(i) ((const float*)arg_ptr(i))
;     __device__ __forceinline__ bool next(int i, DUnit& u) const {
;         long L = (long)i * G + c; const int nwg0 = nM * nN0, nwg1 = nM * nN1;
;         int nN, nwg; if (L < nwg0) { u.p = 0; nN = nN0; nwg = nwg0; } else { L -= nwg0; if (L >= nwg1) return false; u.p = 1; nN = nN1; nwg = nwg1; }
;         int wgid = (int)L; { const int q = nwg / NXCD, r = nwg % NXCD, xcd = wgid % NXCD, off = wgid / NXCD; wgid = (xcd < r ? xcd * (q + 1) : r * (q + 1) + (xcd - r) * q) + off; }
;         const int nig = WGM * nN, gid = wgid / nig, fm = gid * WGM, gsz = (nM - fm) < WGM ? (nM - fm) : WGM;
; template <int layer>
; __device__ __forceinline__ void ph_gemm_wo(LAS unsigned char* lds) {
;     PH_BEGIN;
;     const float* R = INF(0); bf16* H1b = WSP(bf16, WS_H1);
;     const float* gff = INF(layer == 0 ? 10 : 22); bf16* HN = WSP(bf16, WS_HN); float* SSQ = WSP(float, WS_SSQ);
;     fg::DenseSched S{WSP(bf16, WS_O), WSP(bf16, layer == 0 ? WS_W_O0T : WS_W_O1T), 8, nullptr, nullptr, 0, DM, G, bx};
.Lgbd_13:
.LBB0_1535:
	s_or_b64 exec, exec, s[4:5]
	s_mov_b32 s0, 30
	s_waitcnt lgkmcnt(0)
	s_barrier
	s_ashr_i32 s1, s0, 31
	s_lshl_b64 s[0:1], s[0:1], 3
	s_add_u32 s10, s80, s0
	s_addc_u32 s11, s81, s1
	v_mov_b32_e32 v1, v0
	s_mov_b32 s0, s78
	s_mov_b32 s1, s79
	s_mov_b32 s2, 0
	s_mov_b32 s2, 22
	s_ashr_i32 s3, s2, 31
	s_lshl_b64 s[2:3], s[2:3], 3
	s_add_u32 s12, s80, s2
	s_addc_u32 s13, s81, s3
	s_ashr_i32 s2, s1, 31
	v_mov_b32_e32 v1, v0
	s_cmpk_lt_i32 s1, 0x200
	s_cselect_b64 s[4:5], -1, 0
	s_cmpk_gt_i32 s1, 0x1ff
	v_readfirstlane_b32 s18, v1
	s_cbranch_scc1 .LBB0_1537
	s_lshr_b32 s3, s2, 29
	s_add_i32 s3, s1, s3
	s_ashr_i32 s6, s3, 3
	s_and_b32 s3, s3, -8
	s_sub_i32 s3, s1, s3
	s_lshr_b32 s7, s3, 31
	s_or_b32 s7, s7, 64
	s_mul_i32 s3, s7, s3
	s_add_i32 s3, s3, s6
	s_ashr_i32 s6, s3, 31
	s_lshr_b32 s6, s6, 26
	s_add_i32 s6, s3, s6
	s_ashr_i32 s7, s6, 6
	s_lshl_b32 s8, s7, 3
	s_sub_i32 s7, 64, s8
	s_min_u32 s9, s7, 8
	s_andn2_b32 s6, s6, 63
	s_sub_i32 s3, s3, s6
	v_cvt_f32_ubyte0_e32 v3, s9
	v_cvt_f32_i32_e32 v2, s3
	v_rcp_iflag_f32_e32 v4, v3
	s_ashr_i32 s6, s3, 30
	s_or_b32 s14, s6, 1
	v_mul_f32_e32 v4, v2, v4
	v_trunc_f32_e32 v4, v4
	v_fma_f32 v2, -v4, v3, v2
	v_cvt_i32_f32_e32 v4, v4
	v_cmp_ge_f32_e64 s[6:7], |v2|, v3
	s_and_b64 s[6:7], s[6:7], exec
	s_cselect_b32 s6, s14, 0
	v_readfirstlane_b32 s7, v4
	s_add_i32 s7, s7, s6
	s_sext_i32_i8 s6, s7
	s_mul_i32 s7, s7, s9
	s_sub_i32 s3, s3, s7
	s_sext_i32_i8 s3, s3
	s_add_i32 s40, s8, s3

; __device__ __forceinline__ unsigned xb_add(unsigned* p, unsigned v) { return __hip_atomic_fetch_add(p, v, __ATOMIC_RELAXED, __HIP_MEMORY_SCOPE_AGENT); }
; __device__ __forceinline__ void xcd_barrier(const XcdBarrier& b) {
;     ...
;     if (threadIdx.x == 0) {
;         unsigned* bar = b.bar;
;         __builtin_amdgcn_s_waitcnt(0);
;         unsigned nloc = b.st[0], nx = b.st[1];
;         if (nloc == 0u) { xcd_barrier_complete(bar, b.x, nloc, nx); b.st[0] = nloc; b.st[1] = nx; }
;         const unsigned old = xb_add(&bar[XB_XSUB(b.x)], 1u);
;         const unsigned gen = old / nloc;
;         if (old + 1u == (gen + 1u) * nloc) {
;             __builtin_amdgcn_fence(__ATOMIC_RELEASE, "agent");
;             asm volatile("s_waitcnt vmcnt(0)" ::: "memory");
;             const unsigned og = xb_add(&bar[XB_TOP], 1u);
;             const unsigned tg = og / nx;
;             if (og + 1u == (tg + 1u) * nx) xb_add(&bar[XB_TOPGEN], 1u);
.LBB0_1585:
	s_waitcnt lgkmcnt(0)
	v_readfirstlane_b32 s8, v3
	v_readfirstlane_b32 s9, v1
	v_readlane_b32 s0, v252, 4
	s_lshl_b32 s0, s0, 8
	v_readlane_b32 s2, v252, 2
	v_readlane_b32 s3, v252, 3
	s_add_u32 s6, s2, s0
	s_addc_u32 s7, s3, 0
	s_mul_i32 s10, s8, 15
	s_mul_i32 s11, s9, 15
	v_mov_b32_e32 v4, 0x1000
	v_mov_b32_e32 v5, 1
	global_atomic_add v4, v4, v5, s[6:7] offset:1024 sc0
	v_mov_b32_e32 v1, 0x3400
	s_waitcnt vmcnt(0)
	v_readfirstlane_b32 s0, v4
	s_add_u32 s0, s0, 1
	s_cmp_lg_u32 s0, s10
	buffer_inv sc1
	s_cbranch_scc1 .Lgbw_14
	buffer_wbl2 sc1
	s_waitcnt vmcnt(0)
	global_atomic_add v1, v5, s[2:3]

; __device__ __forceinline__ int otid() { int t = threadIdx.x; asm volatile("" : "+v"(t)); return t; }
; template <bool GATHER, class Unit, class Epi, class Sched>
; __device__ __forceinline__ void gemm_phase(LAS unsigned char* lds, const int K, const Sched& S, const Epi& E) {
;     const int tid = otid(), wid = __builtin_amdgcn_readfirstlane(tid >> 6), lane = tid & 63, wr = wid >> 2, wc = wid & 3, fr = lane & 15, fq = lane >> 4;
;     const int nt = K / BK;
;     int R0, C0, R1, C1; stage_rc(tid * 16, R0, C0); stage_rc(tid * 16 + 8192, R1, C1);
;     const int Rb0 = (R0 & ~31) + 8 * ((R0 & 15) >> 2) + 4 * ((R0 >> 4) & 1) + (R0 & 3), Rb1 = (R1 & ~31) + 8 * ((R1 & 15) >> 2) + 4 * ((R1 >> 4) & 1) + (R1 & 3);
;     const unsigned voffB0 = (unsigned)(Rb0 * K + C0) * 2u, voffB1 = (unsigned)(Rb1 * K + C1) * 2u;
;     const size_t kstep = (size_t)(BK * 2);
;     const size_t hstepB = (size_t)HALF * K * 2;
;     const unsigned ldsw = (unsigned)wid * 1024u;
;     const int aoff = lds_byte(wr * 64 + fr, fq * 8), boff = lds_byte(wc * 32 + fr, fq * 8);
;     ...
;     Unit cur, nxt; int ui = 0;
;     if (!S.next(0, cur)) return;
;     f32x4 acc[2][2][4][2];
; #pragma unroll
;     for (int a = 0; a < 2; ++a)
; #pragma unroll
;         for (int b = 0; b < 2; ++b)
; #pragma unroll
;             for (int m = 0; m < 4; ++m)
; #pragma unroll
;                 for (int n = 0; n < 2; ++n) acc[a][b][m][n] = (f32x4){0.f, 0.f, 0.f, 0.f};
;     bf16x8 At[4][2], B0[2][2], B1[2][2];
;     const char* cA = S.a_base(cur); const char* cB = S.b_base(cur);
;     unsigned vA00 = S.a_voff(cur, R0, C0), vA01 = S.a_voff(cur, R1, C1), vA10 = S.a_voff(cur, HALF + R0, C0), vA11 = S.a_voff(cur, HALF + R1, C1);
;     unsigned vN00 = vA00, vN01 = vA01, vN10 = vA10, vN11 = vA11;
;     bool hi_on = !S.lo_only(cur);
;     FG_STAGE(FG_SB(0, 0), cB, voffB0, voffB1); FG_STAGE(FG_SB(0, 1), cB + hstepB, voffB0, voffB1); FG_STAGE(FG_SA(0, 0), cA, vA00, vA01); FG_STAGE(FG_SA(0, 1), cA, vA10, vA11);
;     if (wr == 1) FG_BAR;
;     FG_WAIT_V(2); FG_BAR;
;     FG_STAGE(FG_SB(1, 0), cB + kstep, voffB0, voffB1); FG_STAGE(FG_SA(1, 0), cA + kstep, vA00, vA01); FG_STAGE(FG_SB(1, 1), cB + hstepB + kstep, voffB0, voffB1);
;     FG_WAIT_V(6); FG_BAR;
;     __device__ __forceinline__ bool next(int i, SkUnit& u) const { const int L = i * G + c; if (L >= (T / 256) * 4) return false; u.pm = L >> 2; u.ks = L & 3; return true; }
.Lgbd_14:
.LBB0_1621:
	s_or_b64 exec, exec, s[4:5]
	s_mov_b32 s4, 30
	s_waitcnt lgkmcnt(0)
	v_mov_b32_e32 v1, v0
	s_barrier
	s_mov_b32 s0, s78
	s_mov_b32 s1, s79
	v_mov_b32_e32 v1, v0
	s_cmpk_gt_i32 s1, 0xff
	v_readfirstlane_b32 s14, v1
	s_cbranch_scc1 .LBB0_1637
	v_lshlrev_b32_e32 v2, 4, v1
	v_add_u32_e32 v3, 0x2000, v2
	v_ashrrev_i32_e32 v4, 31, v3
	v_lshrrev_b32_e32 v4, 22, v4
	v_add_u32_e32 v4, v3, v4
	v_ashrrev_i32_e32 v10, 10, v4
	v_mul_i32_i24_e32 v4, 0x400, v10
	v_sub_u32_e32 v3, v3, v4
	v_lshrrev_b32_e32 v4, 4, v3
	v_bitop3_b32 v3, v4, v3, 32 bitop3:0x6c
	v_ashrrev_i32_e32 v4, 31, v3
	v_lshrrev_b32_e32 v4, 26, v4
	v_add_u32_e32 v4, v3, v4
	v_lshlrev_b32_e32 v5, 3, v10
	v_ashrrev_i32_e32 v11, 6, v4
	v_and_b32_e32 v5, -16, v5
	s_ashr_i32 s5, s4, 31
	v_add_u32_e32 v5, v11, v5
	s_lshl_b64 s[2:3], s[4:5], 3
	v_and_b32_e32 v6, 3, v11
	s_mov_b32 s5, 0x3fffe0
	v_lshlrev_b32_e32 v7, 1, v5
	v_lshrrev_b32_e32 v8, 2, v5
	v_and_b32_e32 v4, 0xc0, v4
	v_and_or_b32 v6, v5, s5, v6
	v_and_b32_e32 v7, 24, v7
	v_and_b32_e32 v8, 4, v8
	v_sub_u32_e32 v3, v3, v4
	v_mov_b32_e32 v4, 1
	v_or3_b32 v6, v6, v7, v8
	v_lshlrev_b32_e32 v7, 5, v10
	v_ashrrev_i16_sdwa v3, v4, sext(v3) dst_sel:DWORD dst_unused:UNUSED_PAD src0_sel:DWORD src1_sel:BYTE_0
	v_and_b32_e32 v7, 32, v7
	v_bfe_i32 v12, v3, 0, 16
	v_add_lshl_u32 v3, v7, v12, 1
	v_lshl_add_u32 v66, v6, 10, v3
	v_bfe_i32 v6, v1, 27, 1
	v_lshrrev_b32_e32 v6, 22, v6
	v_add_u32_e32 v6, v2, v6
	v_and_b32_e32 v6, 0xfffffc00, v6
	v_sub_u32_e32 v2, v2, v6
	s_add_u32 s2, s80, s2
	v_lshrrev_b32_e32 v6, 4, v2
	s_addc_u32 s3, s81, s3
	v_bitop3_b32 v6, v6, v2, 32 bitop3:0x6c
	v_ashrrev_i32_e32 v2, 31, v2
	s_load_dwordx2 s[12:13], s[2:3], 0x0
	v_lshrrev_b32_e32 v2, 26, v2
	v_add_u32_e32 v2, v6, v2
	v_ashrrev_i32_e32 v13, 6, v2
	v_ashrrev_i32_e32 v2, 31, v1
	v_lshrrev_b32_e32 v2, 26, v2
	v_add_u32_e32 v2, v1, v2
	s_waitcnt lgkmcnt(0)
	s_add_u32 s2, s12, 0x1be00000
	v_ashrrev_i32_e32 v14, 6, v2
	s_addc_u32 s3, s13, 0
	v_lshlrev_b32_e32 v2, 3, v14
	s_add_u32 s22, s12, 0x6c600000
	v_and_b32_e32 v2, -16, v2
	s_addc_u32 s23, s13, 0
	s_ashr_i32 s4, s1, 2
	v_add_u32_e32 v2, v13, v2
	v_and_b32_e32 v7, 3, v13
	s_ashr_i32 s15, s14, 6
	s_and_b32 s27, s1, 3
	v_and_or_b32 v7, v2, s5, v7
	s_ashr_i32 s5, s4, 31
	s_ashr_i32 s16, s14, 8
	s_lshl_b32 s26, s15, 10
	v_lshlrev_b32_e32 v8, 1, v2
	v_lshrrev_b32_e32 v9, 2, v2
	s_lshl_b32 s8, s27, 10
	s_lshl_b64 s[6:7], s[4:5], 20
	v_and_b32_e32 v8, 24, v8
	v_and_b32_e32 v9, 4, v9
	s_add_u32 s5, s2, s6
	v_or3_b32 v7, v7, v8, v9
	v_mul_i32_i24_e32 v9, 64, v13
	s_addc_u32 s7, s3, s7
	v_sub_u32_e32 v6, v6, v9
	s_add_u32 s6, s5, s8
	v_lshlrev_b32_e32 v8, 5, v14
	v_ashrrev_i16_sdwa v4, v4, sext(v6) dst_sel:DWORD dst_unused:UNUSED_PAD src0_sel:DWORD src1_sel:BYTE_0
	s_addc_u32 s7, s7, 0
	s_lshl_b32 s5, s27, 18
	v_and_b32_e32 v8, 32, v8
	v_bfe_i32 v15, v4, 0, 16
	s_add_u32 s8, s22, s5
	v_add_lshl_u32 v4, v8, v15, 1
	s_addc_u32 s9, s23, 0
	s_add_i32 s5, s26, 0
	v_lshl_add_u32 v68, v7, 10, v4
	s_add_i32 m0, s5, 0x10000
	v_lshl_add_u32 v70, v2, 12, v4
	global_load_lds_dwordx4 v68, s[8:9]
	s_add_i32 m0, s5, 0x12000
	s_add_u32 s10, s8, 0x20000
	s_addc_u32 s11, s9, 0
	s_add_i32 s28, s5, 0x14000
	global_load_lds_dwordx4 v66, s[8:9]
	s_mov_b32 m0, s28
	s_add_i32 s29, s5, 0x16000
	global_load_lds_dwordx4 v68, s[10:11]
	s_mov_b32 m0, s29
	s_add_i32 s30, s5, 0x2000
	global_load_lds_dwordx4 v66, s[10:11]
	s_mov_b32 m0, s5
	v_lshl_add_u32 v72, v5, 12, v3
	global_load_lds_dwordx4 v70, s[6:7]
	s_mov_b32 m0, s30
	s_add_i32 s31, s5, 0x4000
	v_add_u32_e32 v74, 0x80000, v70
	global_load_lds_dwordx4 v72, s[6:7]
	s_mov_b32 m0, s31
	s_add_i32 s33, s5, 0x6000
	v_add_u32_e32 v76, 0x80000, v72
	global_load_lds_dwordx4 v74, s[6:7]
	s_mov_b32 m0, s33
	v_mov_b32_e32 v79, 0
	global_load_lds_dwordx4 v76, s[6:7]
	v_mov_b32_e32 v69, v79
	v_mov_b32_e32 v67, v79
	v_mov_b32_e32 v71, v79
	v_mov_b32_e32 v73, v79
	s_cmp_eq_u32 s16, 1
	s_mov_b32 s34, 0
	s_mov_b32 s17, 0x80000
	v_lshl_add_u64 v[8:9], s[8:9], 0, v[68:69]
	v_lshl_add_u64 v[6:7], s[8:9], 0, v[66:67]
	v_lshl_add_u64 v[2:3], s[6:7], 0, v[70:71]
	s_cselect_b64 s[10:11], -1, 0
	s_cmp_lg_u32 s16, 1
	v_lshl_add_u64 v[4:5], s[6:7], 0, v[72:73]
	s_cbranch_scc1 .LBB0_1624
	s_barrier

; __device__ __forceinline__ unsigned xb_add(unsigned* p, unsigned v) { return __hip_atomic_fetch_add(p, v, __ATOMIC_RELAXED, __HIP_MEMORY_SCOPE_AGENT); }
; __device__ __forceinline__ void xcd_barrier(const XcdBarrier& b) {
;     ...
;     if (threadIdx.x == 0) {
;         unsigned* bar = b.bar;
;         __builtin_amdgcn_s_waitcnt(0);
;         unsigned nloc = b.st[0], nx = b.st[1];
;         if (nloc == 0u) { xcd_barrier_complete(bar, b.x, nloc, nx); b.st[0] = nloc; b.st[1] = nx; }
;         const unsigned old = xb_add(&bar[XB_XSUB(b.x)], 1u);
;         const unsigned gen = old / nloc;
;         if (old + 1u == (gen + 1u) * nloc) {
;             __builtin_amdgcn_fence(__ATOMIC_RELEASE, "agent");
;             asm volatile("s_waitcnt vmcnt(0)" ::: "memory");
;             const unsigned og = xb_add(&bar[XB_TOP], 1u);
;             const unsigned tg = og / nx;
;             if (og + 1u == (tg + 1u) * nx) xb_add(&bar[XB_TOPGEN], 1u);
.LBB0_1653:
	s_waitcnt lgkmcnt(0)
	v_readfirstlane_b32 s8, v3
	v_readfirstlane_b32 s9, v1
	v_readlane_b32 s0, v252, 4
	s_lshl_b32 s0, s0, 8
	v_readlane_b32 s2, v252, 2
	v_readlane_b32 s3, v252, 3
	s_add_u32 s6, s2, s0
	s_addc_u32 s7, s3, 0
	s_mul_i32 s10, s8, 16
	s_mul_i32 s11, s9, 16
	v_mov_b32_e32 v4, 0x1000
	v_mov_b32_e32 v5, 1
	global_atomic_add v4, v4, v5, s[6:7] offset:1024 sc0
	v_mov_b32_e32 v1, 0x3400
	s_waitcnt vmcnt(0)
	v_readfirstlane_b32 s0, v4
	s_add_u32 s0, s0, 1
	s_cmp_lg_u32 s0, s10
	buffer_inv sc1
	s_cbranch_scc1 .Lgbw_15
	buffer_wbl2 sc1
	s_waitcnt vmcnt(0)
	global_atomic_add v1, v5, s[2:3]

; #define LAS __attribute__((address_space(3)))
; __device__ __forceinline__ float rsq(float x) { return __builtin_amdgcn_rsqf(x); }
; #define INF(i) ((const float*)arg_ptr(i))
; template <int layer>
; __device__ __forceinline__ void ph_route(LAS unsigned char* lds) {
;     PH_BEGIN;
;     LAS unsigned* lcnt = (LAS unsigned*)lds; LAS unsigned* lbase = lcnt + 64;
;     const float* PR = WSP(float, WS_PR); int* TOK = WSP(int, WS_TOK); float* GATE = WSP(float, WS_GATE); int* TSLOT = WSP(int, WS_TSLOT); const float* SSQ = WSP(float, WS_SSQ); float* RSL = WSP(float, WS_RSL);
;     unsigned* cnt = WSP(unsigned, WS_CTL) + (layer == 0 ? CW_CNT0 : CW_CNT1);
;     const float* b_rg = INF(layer == 0 ? 12 : 24); const float* b_re = INF(layer == 0 ? 14 : 26);
;     constexpr int TPW = 128;
;     static_assert(T % TPW == 0 && T / TPW <= 248, "whole workgroups of tokens, one trip");
;     if (bx * TPW < T) {
;         if (tid < 64) lcnt[tid] = 0u;
;         __syncthreads();
;         const int t = bx * TPW + tid; int e1o = 0, e2o = 0; float g1o = 0.f, g2o = 0.f, rso = 0.f; unsigned r1 = 0u, r2 = 0u;
;         if (tid < TPW) {
;         const float* pr = PR + (size_t)t * 80;
;         float rstd; { f32x4 q = *(const f32x4*)(SSQ + (size_t)t * 32);
; #pragma unroll
;             for (int i = 1; i < 8; ++i) q += *(const f32x4*)(SSQ + (size_t)t * 32 + 4 * i);
;             rstd = rsq(((q[0] + q[1]) + (q[2] + q[3])) * (1.0f / DM) + EPS); }
;         auto sum4 = [=](int j) { const f32x4 a0 = *(const f32x4*)(pr + j), a1 = *(const f32x4*)(pr + (size_t)T * 80 + j), a2 = *(const f32x4*)(pr + (size_t)2 * T * 80 + j), a3 = *(const f32x4*)(pr + (size_t)3 * T * 80 + j);
;             return (a0 + a1) + (a2 + a3); };
;         float gl[8]; int g = 0; float gm = -3.0e38f;
;         { const f32x4 x0 = sum4(0), x1 = sum4(4);
; #pragma unroll
;           for (int j = 0; j < 8; ++j) { gl[j] = (j < 4 ? x0[j & 3] : x1[j & 3]) * rstd + b_rg[j]; if (gl[j] > gm) { gm = gl[j]; g = j; } } }
.Lgbd_15:
.LBB0_1689:
	s_or_b64 exec, exec, s[4:5]
	s_mov_b32 s4, 30
	v_mov_b32_e32 v16, v0
	s_mov_b32 s0, s78
	s_waitcnt lgkmcnt(0)
	s_barrier
	s_mov_b32 s0, s79
	s_mov_b32 s8, 24
	s_mov_b32 s6, 26
	s_cmpk_gt_i32 s0, 0x7f
	s_cbranch_scc1 .LBB0_1705
	s_ashr_i32 s5, s4, 31
	s_lshl_b64 s[2:3], s[4:5], 3
	s_add_u32 s2, s80, s2
	s_addc_u32 s3, s81, s3
	s_ashr_i32 s9, s8, 31
	s_load_dwordx2 s[18:19], s[2:3], 0x0
	s_lshl_b64 s[2:3], s[8:9], 3
	s_add_u32 s10, s80, s2
	s_addc_u32 s11, s81, s3
	s_ashr_i32 s7, s6, 31
	s_lshl_b64 s[2:3], s[6:7], 3
	s_add_u32 s12, s80, s2
	s_addc_u32 s13, s81, s3
	v_cmp_gt_i32_e64 s[6:7], 64, v16
	v_lshl_add_u32 v1, v16, 2, 0
	s_and_saveexec_b64 s[4:5], s[6:7]
	v_mov_b32_e32 v2, 0
	ds_write_b32 v1, v2
	s_or_b64 exec, exec, s[4:5]
	v_lshl_add_u32 v14, s0, 7, v16
	s_movk_i32 s0, 0x80
	v_cmp_gt_i32_e64 s[4:5], s0, v16
	v_mov_b32_e32 v6, 0
	v_mov_b32_e32 v4, 0
	v_mov_b32_e32 v2, 0
	v_mov_b32_e32 v7, 0
	v_mov_b32_e32 v15, 0
	v_mov_b32_e32 v3, 0
	v_mov_b32_e32 v8, 0
	s_waitcnt lgkmcnt(0)
	s_barrier
	s_and_saveexec_b64 s[20:21], s[4:5]
	s_cbranch_execz .LBB0_1698
	v_ashrrev_i32_e32 v15, 31, v14
	v_lshlrev_b64 v[2:3], 7, v[14:15]
	v_lshl_add_u64 v[2:3], s[18:19], 0, v[2:3]
	s_mov_b64 s[0:1], 0x4e000000
	v_lshl_add_u64 v[4:5], v[2:3], 0, s[0:1]
	s_movk_i32 s0, 0x140
	v_mov_b64_e32 v[6:7], s[18:19]
	v_mad_i64_i32 v[74:75], s[0:1], v14, s0, v[6:7]
	s_mov_b32 s0, 0x6db00000
	s_nop 0
	v_add_co_u32_e64 v6, s[8:9], s0, v74
	s_mov_b32 s0, 0x6e000000
	s_nop 0
	v_addc_co_u32_e64 v7, s[8:9], 0, v75, s[8:9]
	global_load_dwordx4 v[10:13], v[6:7], off
	v_add_co_u32_e64 v6, s[8:9], s0, v74
	s_mov_b32 s0, 0x6e500000
	s_nop 0
	v_addc_co_u32_e64 v7, s[8:9], 0, v75, s[8:9]
	global_load_dwordx4 v[18:21], v[6:7], off
	v_add_co_u32_e64 v6, s[8:9], s0, v74
	s_mov_b32 s0, 0x6ea00000
	s_nop 0
	v_addc_co_u32_e64 v7, s[8:9], 0, v75, s[8:9]
	global_load_dwordx4 v[22:25], v[6:7], off
	v_add_co_u32_e64 v6, s[8:9], s0, v74
	v_add_co_u32_e32 v2, vcc, 0x4e000000, v2
	s_nop 0
	v_addc_co_u32_e64 v7, s[8:9], 0, v75, s[8:9]
	global_load_dwordx4 v[26:29], v[6:7], off
	v_addc_co_u32_e32 v3, vcc, 0, v3, vcc
	global_load_dwordx4 v[30:33], v[2:3], off
	global_load_dwordx4 v[34:37], v[4:5], off offset:16
	global_load_dwordx4 v[38:41], v[4:5], off offset:32
	global_load_dwordx4 v[42:45], v[4:5], off offset:48
	global_load_dwordx4 v[46:49], v[4:5], off offset:64
	global_load_dwordx4 v[50:53], v[4:5], off offset:80
	global_load_dwordx4 v[54:57], v[4:5], off offset:96
	global_load_dwordx4 v[58:61], v[4:5], off offset:112
	s_load_dwordx2 s[0:1], s[10:11], 0x0
	s_load_dwordx2 s[24:25], s[12:13], 0x0
	v_mov_b32_e32 v79, 0
	s_mov_b64 s[2:3], 0x6db00000
	v_lshl_add_u64 v[80:81], v[74:75], 0, s[2:3]
	s_waitcnt lgkmcnt(0)
	global_load_dwordx4 v[6:9], v79, s[0:1]
	s_mov_b64 s[2:3], 0x6e000000
	v_lshl_add_u64 v[82:83], v[74:75], 0, s[2:3]
	s_mov_b64 s[2:3], 0x6e500000
	v_lshl_add_u64 v[84:85], v[74:75], 0, s[2:3]
	s_mov_b64 s[2:3], 0x6ea00000
	global_load_dwordx4 v[62:65], v[80:81], off offset:16
	global_load_dwordx4 v[66:69], v[82:83], off offset:16
	global_load_dwordx4 v[70:73], v[84:85], off offset:16
	v_lshl_add_u64 v[86:87], v[74:75], 0, s[2:3]
	global_load_dwordx4 v[74:77], v[86:87], off offset:16
	global_load_dwordx4 v[2:5], v79, s[0:1] offset:16
	v_mov_b32_e32 v15, 0x358637bd
	s_mov_b32 s0, 0xff61b1e6
	s_waitcnt vmcnt(17)
	v_mov_b32_e32 v88, v10
	s_waitcnt vmcnt(16)
	v_mov_b32_e32 v90, v18
	s_waitcnt vmcnt(15)
	v_mov_b32_e32 v89, v22
	v_mov_b32_e32 v22, v11
	s_waitcnt vmcnt(12)
	v_pk_add_f32 v[30:31], v[30:31], v[34:35]
	s_waitcnt vmcnt(11)
	v_pk_add_f32 v[30:31], v[30:31], v[38:39]
	v_mov_b32_e32 v91, v26
	v_mov_b32_e32 v26, v19
	v_pk_add_f32 v[18:19], v[32:33], v[36:37]
	s_waitcnt vmcnt(10)
	v_pk_add_f32 v[30:31], v[30:31], v[42:43]
	v_pk_add_f32 v[18:19], v[18:19], v[40:41]
	s_waitcnt vmcnt(9)
	v_pk_add_f32 v[30:31], v[30:31], v[46:47]
	v_pk_add_f32 v[18:19], v[18:19], v[44:45]
	s_waitcnt vmcnt(8)
	v_pk_add_f32 v[30:31], v[30:31], v[50:51]
	v_pk_add_f32 v[18:19], v[18:19], v[48:49]
	s_waitcnt vmcnt(7)
	v_pk_add_f32 v[30:31], v[30:31], v[54:55]
	v_pk_add_f32 v[18:19], v[18:19], v[52:53]
	s_waitcnt vmcnt(6)
	v_pk_add_f32 v[30:31], v[30:31], v[58:59]
	v_pk_add_f32 v[18:19], v[18:19], v[56:57]
	v_pk_add_f32 v[10:11], v[88:89], v[90:91]
	v_pk_add_f32 v[18:19], v[18:19], v[60:61]
	v_add_f32_e32 v10, v10, v11
	v_pk_mov_b32 v[32:33], v[30:31], v[18:19] op_sel:[1,0]
	v_mov_b32_e32 v31, v19
	v_pk_add_f32 v[18:19], v[32:33], v[30:31]
	s_nop 0
	v_add_f32_e32 v17, v18, v19
	v_fmac_f32_e32 v15, 0x3a000000, v17
	v_rsq_f32_e32 v15, v15
	v_pk_add_f32 v[18:19], v[22:23], v[26:27]
	s_waitcnt vmcnt(5)
	v_fma_f32 v17, v15, v10, v6
	v_add_f32_e32 v11, v18, v19
	v_fma_f32 v18, v15, v11, v7
	v_max_f32_e32 v6, 0xff61b1e6, v17
	v_cmp_gt_f32_e32 vcc, v18, v6
	v_mov_b32_e32 v7, v24
	v_mov_b32_e32 v10, v20
	v_cndmask_b32_e32 v19, v6, v18, vcc
	v_mov_b32_e32 v6, v12
	v_mov_b32_e32 v11, v28
	v_pk_add_f32 v[6:7], v[6:7], v[10:11]
	v_mov_b32_e32 v24, v13
	v_add_f32_e32 v6, v6, v7
	v_mov_b32_e32 v28, v21
	v_fma_f32 v8, v15, v6, v8
	v_pk_add_f32 v[6:7], v[24:25], v[28:29]
	v_cmp_gt_f32_e64 s[8:9], v8, v19
	v_add_f32_e32 v6, v6, v7
	v_fmac_f32_e32 v9, v15, v6
	v_cndmask_b32_e64 v10, v19, v8, s[8:9]
	v_cmp_gt_f32_e64 s[10:11], v9, v10
	s_waitcnt vmcnt(4)
	v_mov_b32_e32 v6, v62
	s_waitcnt vmcnt(2)
	v_mov_b32_e32 v7, v70
	v_cndmask_b32_e64 v12, v10, v9, s[10:11]
	v_mov_b32_e32 v10, v66
	s_waitcnt vmcnt(1)
	v_mov_b32_e32 v11, v74
	v_pk_add_f32 v[6:7], v[6:7], v[10:11]
	v_mov_b32_e32 v70, v63
	v_add_f32_e32 v6, v6, v7
	v_mov_b32_e32 v74, v67
	s_waitcnt vmcnt(0)
; template <int layer>
; __device__ __forceinline__ void ph_route(LAS unsigned char* lds) {
;     ...
;           for (int j = 0; j < 8; ++j) { gl[j] = (j < 4 ? x0[j & 3] : x1[j & 3]) * rstd + b_rg[j]; if (gl[j] > gm) { gm = gl[j]; g = j; } } }
;         float se = 0.f;
; #pragma unroll
;         for (int j = 0; j < 8; ++j) se += expf(gl[j] - gm);
;         const float pg = 1.0f / se;
;         float el[8]; int i1 = 0; float m1 = -3.0e38f;
;         { const f32x4 x0 = sum4(8 + g * 8), x1 = sum4(12 + g * 8);
; #pragma unroll
;           for (int j = 0; j < 8; ++j) { el[j] = (j < 4 ? x0[j & 3] : x1[j & 3]) * rstd + b_re[g * 8 + j]; if (el[j] > m1) { m1 = el[j]; i1 = j; } } }
;         int i2 = 0; float m2 = -3.0e38f;
; #pragma unroll
;         for (int j = 0; j < 8; ++j) { if (j != i1 && el[j] > m2) { m2 = el[j]; i2 = j; } }
;         const float w2 = expf(m2 - m1), g1 = pg / (1.0f + w2), g2 = pg * w2 / (1.0f + w2);
	v_fma_f32 v7, v15, v6, v2
	v_pk_add_f32 v[10:11], v[70:71], v[74:75]
	v_cmp_gt_f32_e64 s[12:13], v7, v12
	v_add_f32_e32 v6, v10, v11
	v_fma_f32 v6, v15, v6, v3
	v_cndmask_b32_e64 v2, v12, v7, s[12:13]
	v_cmp_gt_f32_e64 s[14:15], v6, v2
	v_mov_b32_e32 v3, v72
	v_mov_b32_e32 v10, v68
	v_cndmask_b32_e64 v12, v2, v6, s[14:15]
	v_mov_b32_e32 v2, v64
	v_mov_b32_e32 v11, v76
	v_pk_add_f32 v[2:3], v[2:3], v[10:11]
	v_mov_b32_e32 v72, v65
	v_add_f32_e32 v2, v2, v3
	v_mov_b32_e32 v76, v69
	v_fma_f32 v4, v15, v2, v4
	v_pk_add_f32 v[2:3], v[72:73], v[76:77]
	v_cmp_gt_f32_e64 s[16:17], v4, v12
	v_add_f32_e32 v2, v2, v3
	v_fmac_f32_e32 v5, v15, v2
	v_cndmask_b32_e64 v2, 0, 8, vcc
	v_cndmask_b32_e64 v2, v2, 16, s[8:9]
	v_cndmask_b32_e64 v2, v2, 24, s[10:11]
	v_cndmask_b32_e64 v2, v2, 32, s[12:13]
	v_cndmask_b32_e64 v19, v12, v4, s[16:17]
	v_cndmask_b32_e64 v2, v2, 40, s[14:15]
	v_cndmask_b32_e64 v2, v2, 48, s[16:17]
	v_cmp_gt_f32_e32 vcc, v5, v19
	v_mov_b32_e32 v3, v79
	s_nop 0
	v_cndmask_b32_e64 v2, v2, 56, vcc
	v_add_u32_e32 v78, 8, v2
	v_lshlrev_b64 v[10:11], 2, v[2:3]
	v_lshlrev_b64 v[12:13], 2, v[78:79]
	v_lshl_add_u64 v[56:57], v[80:81], 0, v[10:11]
	v_lshl_add_u64 v[58:59], v[82:83], 0, v[12:13]
	v_lshl_add_u64 v[60:61], v[84:85], 0, v[12:13]
	v_lshl_add_u64 v[62:63], v[86:87], 0, v[12:13]
	global_load_dwordx4 v[20:23], v[56:57], off offset:32
	global_load_dwordx4 v[24:27], v[58:59], off
	global_load_dwordx4 v[28:31], v[60:61], off
	global_load_dwordx4 v[32:35], v[62:63], off
	v_lshl_add_u64 v[64:65], s[24:25], 0, v[10:11]
	global_load_dwordx4 v[36:39], v[64:65], off
	global_load_dwordx4 v[40:43], v[56:57], off offset:48
	global_load_dwordx4 v[44:47], v[60:61], off offset:16
	global_load_dwordx4 v[48:51], v[58:59], off offset:16
	global_load_dwordx4 v[52:55], v[62:63], off offset:16
	global_load_dwordx4 v[10:13], v[64:65], off offset:16
	s_waitcnt vmcnt(9)
	v_mov_b32_e32 v56, v20
	s_waitcnt vmcnt(8)
	v_mov_b32_e32 v58, v24
	s_waitcnt vmcnt(7)
	v_mov_b32_e32 v57, v28
	s_waitcnt vmcnt(6)
	v_mov_b32_e32 v59, v32
	v_pk_add_f32 v[56:57], v[56:57], v[58:59]
	v_mov_b32_e32 v20, v22
	v_mov_b32_e32 v28, v21
	v_mov_b32_e32 v32, v25
	v_mov_b32_e32 v21, v30
	v_mov_b32_e32 v24, v26
	v_mov_b32_e32 v25, v34
	v_add_f32_e32 v3, v56, v57
	v_pk_add_f32 v[28:29], v[28:29], v[32:33]
	v_pk_add_f32 v[20:21], v[20:21], v[24:25]
	s_waitcnt vmcnt(5)
	v_fma_f32 v24, v15, v3, v36
	v_add_f32_e32 v22, v28, v29
	v_max_f32_e32 v3, v24, v24
	v_fma_f32 v25, v15, v22, v37
	v_max_f32_e32 v3, 0xff61b1e6, v3
	v_cmp_gt_f32_e64 s[10:11], v25, v3
	v_add_f32_e32 v20, v20, v21
	v_mov_b32_e32 v30, v23
	v_mov_b32_e32 v34, v27
	v_cndmask_b32_e64 v3, v3, v25, s[10:11]
	v_fma_f32 v26, v15, v20, v38
	v_pk_add_f32 v[20:21], v[30:31], v[34:35]
	v_cndmask_b32_e64 v22, 0, 1, s[10:11]
	v_cmp_gt_f32_e64 s[10:11], v26, v3
	v_add_f32_e32 v20, v20, v21
	v_fmac_f32_e32 v39, v15, v20
	v_cndmask_b32_e64 v3, v3, v26, s[10:11]
	v_cndmask_b32_e64 v22, v22, 2, s[10:11]
	v_cmp_gt_f32_e64 s[10:11], v39, v3
	s_waitcnt vmcnt(4)
	v_mov_b32_e32 v20, v40
	s_waitcnt vmcnt(3)
	v_mov_b32_e32 v21, v44
	v_cndmask_b32_e64 v27, v22, 3, s[10:11]
	s_waitcnt vmcnt(2)
	v_mov_b32_e32 v22, v48
	s_waitcnt vmcnt(1)
	v_mov_b32_e32 v23, v52
	v_pk_add_f32 v[20:21], v[20:21], v[22:23]
	v_mov_b32_e32 v44, v41
	v_add_f32_e32 v20, v20, v21
	v_mov_b32_e32 v52, v49
	v_cndmask_b32_e64 v3, v3, v39, s[10:11]
	s_waitcnt vmcnt(0)
	v_fma_f32 v22, v15, v20, v10
	v_pk_add_f32 v[20:21], v[44:45], v[52:53]
	v_cmp_gt_f32_e64 s[10:11], v22, v3
	v_add_f32_e32 v20, v20, v21
	v_fma_f32 v23, v15, v20, v11
	v_cndmask_b32_e64 v3, v3, v22, s[10:11]
	v_cndmask_b32_e64 v10, v27, 4, s[10:11]
	v_cmp_gt_f32_e64 s[10:11], v23, v3
	v_mov_b32_e32 v11, v46
	v_mov_b32_e32 v20, v50
	v_cndmask_b32_e64 v27, v10, 5, s[10:11]
	v_mov_b32_e32 v10, v42
	v_mov_b32_e32 v21, v54
	v_pk_add_f32 v[10:11], v[10:11], v[20:21]
	v_mov_b32_e32 v46, v43
	v_add_f32_e32 v10, v10, v11
	v_mov_b32_e32 v54, v51
	v_cndmask_b32_e64 v3, v3, v23, s[10:11]
	v_fma_f32 v20, v15, v10, v12
	v_pk_add_f32 v[10:11], v[46:47], v[54:55]
	v_cmp_ngt_f32_e64 s[10:11], v20, v3
	v_add_f32_e32 v10, v10, v11
	v_fmac_f32_e32 v13, v15, v10
	v_cndmask_b32_e64 v12, v20, v3, s[10:11]
	v_cndmask_b32_e64 v3, 6, v27, s[10:11]
	v_cmp_gt_f32_e64 s[14:15], v13, v12
	v_cmp_nlt_f32_e64 s[8:9], s0, v24
	v_mov_b32_e32 v10, 0xff61b1e6
	v_cndmask_b32_e64 v3, v3, 7, s[14:15]
	v_cmp_eq_u32_e64 s[16:17], 0, v3
	s_or_b64 s[8:9], s[16:17], s[8:9]
	v_cndmask_b32_e64 v10, v24, v10, s[8:9]
	v_cmp_ne_u32_e64 s[8:9], 1, v3
	v_cmp_gt_f32_e64 s[16:17], v25, v10
	s_and_b64 s[8:9], s[8:9], s[16:17]
	v_cndmask_b32_e64 v10, v10, v25, s[8:9]
	v_cndmask_b32_e64 v11, 0, 1, s[8:9]
	v_cmp_ne_u32_e64 s[8:9], 2, v3
	v_cmp_gt_f32_e64 s[16:17], v26, v10
	s_and_b64 s[8:9], s[8:9], s[16:17]
	v_cndmask_b32_e64 v10, v10, v26, s[8:9]
	v_cndmask_b32_e64 v11, v11, 2, s[8:9]
	v_cmp_ne_u32_e64 s[8:9], 3, v3
	v_cmp_gt_f32_e64 s[16:17], v39, v10
	s_and_b64 s[8:9], s[8:9], s[16:17]
	v_cndmask_b32_e64 v10, v10, v39, s[8:9]
	v_cndmask_b32_e64 v11, v11, 3, s[8:9]
	v_cmp_ne_u32_e64 s[8:9], 4, v3
	v_cmp_gt_f32_e64 s[16:17], v22, v10
	s_and_b64 s[8:9], s[8:9], s[16:17]
	v_cndmask_b32_e64 v10, v10, v22, s[8:9]
	v_cndmask_b32_e64 v11, v11, 4, s[8:9]
	v_cmp_ne_u32_e64 s[8:9], 5, v3
	v_cmp_gt_f32_e64 s[16:17], v23, v10
	s_and_b64 s[8:9], s[8:9], s[16:17]
	v_cndmask_b32_e64 v21, v10, v23, s[8:9]
	v_cndmask_b32_e64 v11, v11, 5, s[8:9]
	s_or_b64 s[0:1], s[10:11], s[14:15]
	v_cmp_gt_f32_e64 s[8:9], v20, v21
	s_and_b64 s[8:9], s[0:1], s[8:9]
	v_cmp_ngt_f32_e64 s[12:13], v13, v12
	v_cndmask_b32_e64 v10, v11, 6, s[8:9]
	v_cndmask_b32_e64 v11, v21, v20, s[8:9]
	s_and_saveexec_b64 s[10:11], s[12:13]
	s_cbranch_execz .LBB0_1697
	v_cmp_gt_f32_e64 s[8:9], v13, v11
	s_and_saveexec_b64 s[12:13], s[8:9]
	v_mov_b32_e32 v10, 7
	v_mov_b32_e32 v11, v13
	s_or_b64 exec, exec, s[12:13]
	v_mov_b32_e32 v13, v12

; __device__ __forceinline__ unsigned xb_add(unsigned* p, unsigned v) { return __hip_atomic_fetch_add(p, v, __ATOMIC_RELAXED, __HIP_MEMORY_SCOPE_AGENT); }
; __device__ __forceinline__ void xcd_barrier(const XcdBarrier& b) {
;     ...
;     if (threadIdx.x == 0) {
;         unsigned* bar = b.bar;
;         __builtin_amdgcn_s_waitcnt(0);
;         unsigned nloc = b.st[0], nx = b.st[1];
;         if (nloc == 0u) { xcd_barrier_complete(bar, b.x, nloc, nx); b.st[0] = nloc; b.st[1] = nx; }
;         const unsigned old = xb_add(&bar[XB_XSUB(b.x)], 1u);
;         const unsigned gen = old / nloc;
;         if (old + 1u == (gen + 1u) * nloc) {
;             __builtin_amdgcn_fence(__ATOMIC_RELEASE, "agent");
;             asm volatile("s_waitcnt vmcnt(0)" ::: "memory");
;             const unsigned og = xb_add(&bar[XB_TOP], 1u);
;             const unsigned tg = og / nx;
;             if (og + 1u == (tg + 1u) * nx) xb_add(&bar[XB_TOPGEN], 1u);
.LBB0_1721:
	s_waitcnt lgkmcnt(0)
	v_readfirstlane_b32 s8, v3
	v_readfirstlane_b32 s9, v1
	v_readlane_b32 s0, v252, 4
	s_lshl_b32 s0, s0, 8
	v_readlane_b32 s2, v252, 2
	v_readlane_b32 s3, v252, 3
	s_add_u32 s6, s2, s0
	s_addc_u32 s7, s3, 0
	s_mul_i32 s10, s8, 17
	s_mul_i32 s11, s9, 17
	v_mov_b32_e32 v4, 0x1000
	v_mov_b32_e32 v5, 1
	global_atomic_add v4, v4, v5, s[6:7] offset:1024 sc0
	v_mov_b32_e32 v1, 0x3400
	s_waitcnt vmcnt(0)
	v_readfirstlane_b32 s0, v4
	s_add_u32 s0, s0, 1
	s_cmp_lg_u32 s0, s10
	buffer_inv sc1
	s_cbranch_scc1 .Lgbw_16
	buffer_wbl2 sc1
	s_waitcnt vmcnt(0)
	global_atomic_add v1, v5, s[2:3]

; #define LAS __attribute__((address_space(3)))
; __device__ __forceinline__ int otid() { int t = threadIdx.x; asm volatile("" : "+v"(t)); return t; }
; __device__ __forceinline__ void moe_prefix(LAS unsigned char* lds, const unsigned* cnt) {
;     LAS int* s_ts = (LAS int*)(lds + LDS_TS); LAS int* s_cn = (LAS int*)(lds + LDS_CN);
;     LAS unsigned char* s_te = lds + LDS_TE;
;     LAS int* s_xs = (LAS int*)(lds + LDS_XS);
;     const int tz_ = otid();
;     if (tz_ < 64) { const int e = tz_; const int c = (int)cnt[e], nt = (c + 255) >> 8;
;         int incl = nt;
; #pragma unroll
;         for (int o = 1; o < 64; o <<= 1) { const int up = __shfl_up(incl, o); if (e >= o) incl += up; }
;         const int excl = incl - nt;
;         s_ts[e] = excl; s_cn[e] = c;
;         for (int i = 0; i < nt; ++i) s_te[excl + i] = (unsigned char)e;
; template <int layer>
; __device__ __forceinline__ void ph_gateup(LAS unsigned char* lds) {
;     PH_BEGIN;
;     moe_prefix(lds, WSP(unsigned, WS_CTL) + (layer == 0 ? CW_CNT0 : CW_CNT1));
.Lgbd_16:
.LBB0_1757:
	s_or_b64 exec, exec, s[4:5]
	s_mov_b32 s0, 30
	s_waitcnt lgkmcnt(0)
	s_barrier
	s_ashr_i32 s1, s0, 31
	s_lshl_b64 s[0:1], s[0:1], 3
	s_add_u32 s0, s80, s0
	s_addc_u32 s1, s81, s1
	s_load_dwordx2 s[12:13], s[0:1], 0x0
	v_mov_b32_e32 v1, v0
	s_mov_b32 s36, s78
	s_mov_b32 s1, s79
	v_mov_b32_e32 v6, v0
	s_nop 0
	v_cmp_gt_i32_e32 vcc, 64, v6
	s_and_saveexec_b64 s[4:5], vcc
	s_cbranch_execz .LBB0_1787
	v_ashrrev_i32_e32 v7, 31, v6
	s_waitcnt lgkmcnt(0)
	v_lshl_add_u64 v[2:3], v[6:7], 2, s[12:13]
	v_add_co_u32_e32 v2, vcc, 0x2000, v2
	v_lshl_add_u32 v4, v6, 2, 0
	s_nop 0
	v_addc_co_u32_e32 v3, vcc, 0, v3, vcc
	global_load_dword v2, v[2:3], off
	v_mbcnt_hi_u32_b32 v3, -1, v236
	v_and_b32_e32 v7, 64, v3
	v_add_u32_e32 v1, -1, v3
	v_cmp_lt_i32_e32 vcc, v1, v7
	v_add_u32_e32 v5, -2, v3
	v_add_u32_e32 v8, -4, v3
	v_cndmask_b32_e32 v1, v1, v3, vcc
	v_lshlrev_b32_e32 v10, 2, v1
	v_cmp_lt_i32_e32 vcc, v5, v7
	v_add_u32_e32 v9, -8, v3
	v_add_u32_e32 v13, -16, v3
	v_cndmask_b32_e32 v5, v5, v3, vcc
	v_cmp_lt_i32_e32 vcc, 0, v6
	v_lshlrev_b32_e32 v5, 2, v5
	v_subrev_u32_e32 v14, 32, v3
	v_add_u32_e32 v16, 0x26c40, v4
	v_add_u32_e32 v4, 0x26d50, v4
	s_waitcnt vmcnt(0)
	v_add_u32_e32 v1, 0xff, v2
	v_ashrrev_i32_e32 v1, 8, v1
	ds_bpermute_b32 v10, v10, v1
	ds_write_b32 v4, v2
	s_waitcnt lgkmcnt(1)
	v_cndmask_b32_e32 v10, 0, v10, vcc
	v_add_u32_e32 v12, v10, v1
	ds_bpermute_b32 v5, v5, v12
	v_cmp_lt_i32_e32 vcc, v8, v7
	s_nop 1
	v_cndmask_b32_e32 v8, v8, v3, vcc
	v_cmp_lt_i32_e32 vcc, 1, v6
	v_lshlrev_b32_e32 v8, 2, v8
	s_waitcnt lgkmcnt(0)
	v_cndmask_b32_e32 v11, 0, v5, vcc
	v_add_u32_e32 v5, v11, v12
	ds_bpermute_b32 v8, v8, v5
	v_cmp_lt_i32_e32 vcc, v9, v7
	s_nop 1
	v_cndmask_b32_e32 v9, v9, v3, vcc
	v_cmp_lt_i32_e32 vcc, 3, v6
	v_lshlrev_b32_e32 v9, 2, v9
	s_waitcnt lgkmcnt(0)
	v_cndmask_b32_e32 v12, 0, v8, vcc
	v_add_u32_e32 v5, v12, v5
	ds_bpermute_b32 v8, v9, v5
	v_cmp_lt_i32_e32 vcc, v13, v7
	s_nop 1
	v_cndmask_b32_e32 v9, v13, v3, vcc
	v_cmp_lt_i32_e32 vcc, 7, v6
	v_lshlrev_b32_e32 v9, 2, v9
	s_waitcnt lgkmcnt(0)
	v_cndmask_b32_e32 v13, 0, v8, vcc
	v_add_u32_e32 v5, v13, v5
	ds_bpermute_b32 v8, v9, v5
	v_cmp_lt_i32_e32 vcc, v14, v7
	s_nop 1
	v_cndmask_b32_e32 v3, v14, v3, vcc
	v_cmp_lt_i32_e32 vcc, 15, v6
	v_lshlrev_b32_e32 v3, 2, v3
	s_waitcnt lgkmcnt(0)
	v_cndmask_b32_e32 v14, 0, v8, vcc
	v_add_u32_e32 v5, v14, v5
	ds_bpermute_b32 v3, v3, v5
	v_cmp_lt_i32_e32 vcc, 31, v6
	v_sub_u32_e32 v2, v5, v1
	s_waitcnt lgkmcnt(0)
	v_cndmask_b32_e32 v15, 0, v3, vcc
	v_add_u32_e32 v2, v2, v15
	v_cmp_lt_i32_e32 vcc, 0, v1
	ds_write_b32 v16, v2
	s_and_saveexec_b64 s[6:7], vcc
	s_cbranch_execz .LBB0_1771
	v_cmp_lt_u32_e32 vcc, 7, v1
	s_mov_b64 s[10:11], -1
	v_mov_b32_e32 v2, 0
	s_and_saveexec_b64 s[8:9], vcc
	s_cbranch_execz .LBB0_1768
	s_mov_b32 s0, 0x4040404
	v_add_u32_e32 v2, -8, v1
	v_perm_b32 v8, v6, v6, s0
	v_lshrrev_b32_e32 v3, 3, v2
	v_mov_b32_e32 v9, v8
	v_add_u32_e32 v16, 1, v3
	v_cmp_lt_u32_e32 vcc, 55, v2
	v_mov_b32_e32 v19, 0
	s_and_saveexec_b64 s[10:11], vcc
	s_cbranch_execz .LBB0_1764
	v_add3_u32 v2, v10, v15, v14
	v_add3_u32 v2, v2, v13, v12
	v_and_b32_e32 v17, 0x3ffffff8, v16
	s_mov_b32 s0, 0
	v_add3_u32 v18, v2, v11, 0
	s_mov_b64 s[14:15], 0
	v_mov_b32_e32 v2, v8
	v_mov_b32_e32 v3, v8
	v_mov_b32_e32 v4, v8
	v_mov_b32_e32 v5, v8

; __device__ __forceinline__ unsigned xb_add(unsigned* p, unsigned v) { return __hip_atomic_fetch_add(p, v, __ATOMIC_RELAXED, __HIP_MEMORY_SCOPE_AGENT); }
; __device__ __forceinline__ void xcd_barrier(const XcdBarrier& b) {
;     ...
;     if (threadIdx.x == 0) {
;         unsigned* bar = b.bar;
;         __builtin_amdgcn_s_waitcnt(0);
;         unsigned nloc = b.st[0], nx = b.st[1];
;         if (nloc == 0u) { xcd_barrier_complete(bar, b.x, nloc, nx); b.st[0] = nloc; b.st[1] = nx; }
;         const unsigned old = xb_add(&bar[XB_XSUB(b.x)], 1u);
;         const unsigned gen = old / nloc;
;         if (old + 1u == (gen + 1u) * nloc) {
;             __builtin_amdgcn_fence(__ATOMIC_RELEASE, "agent");
;             asm volatile("s_waitcnt vmcnt(0)" ::: "memory");
;             const unsigned og = xb_add(&bar[XB_TOP], 1u);
;             const unsigned tg = og / nx;
;             if (og + 1u == (tg + 1u) * nx) xb_add(&bar[XB_TOPGEN], 1u);
.LBB0_1855:
	s_waitcnt lgkmcnt(0)
	v_readfirstlane_b32 s8, v3
	v_readfirstlane_b32 s9, v1
	v_readlane_b32 s0, v252, 4
	s_lshl_b32 s0, s0, 8
	v_readlane_b32 s2, v252, 2
	v_readlane_b32 s3, v252, 3
	s_add_u32 s6, s2, s0
	s_addc_u32 s7, s3, 0
	s_mul_i32 s10, s8, 18
	s_mul_i32 s11, s9, 18
	v_mov_b32_e32 v4, 0x1000
	v_mov_b32_e32 v5, 1
	global_atomic_add v4, v4, v5, s[6:7] offset:1024 sc0
	v_mov_b32_e32 v1, 0x3400
	s_waitcnt vmcnt(0)
	v_readfirstlane_b32 s0, v4
	s_add_u32 s0, s0, 1
	s_cmp_lg_u32 s0, s10
	buffer_inv sc1
	s_cbranch_scc1 .Lgbw_17
	buffer_wbl2 sc1
	s_waitcnt vmcnt(0)
	global_atomic_add v1, v5, s[2:3]

; #define LAS __attribute__((address_space(3)))
; __device__ __forceinline__ int otid() { int t = threadIdx.x; asm volatile("" : "+v"(t)); return t; }
; __device__ __forceinline__ void moe_prefix(LAS unsigned char* lds, const unsigned* cnt) {
;     LAS int* s_ts = (LAS int*)(lds + LDS_TS); LAS int* s_cn = (LAS int*)(lds + LDS_CN);
;     LAS unsigned char* s_te = lds + LDS_TE;
;     LAS int* s_xs = (LAS int*)(lds + LDS_XS);
;     const int tz_ = otid();
;     if (tz_ < 64) { const int e = tz_; const int c = (int)cnt[e], nt = (c + 255) >> 8;
;         int incl = nt;
; #pragma unroll
;         for (int o = 1; o < 64; o <<= 1) { const int up = __shfl_up(incl, o); if (e >= o) incl += up; }
;         const int excl = incl - nt;
;         s_ts[e] = excl; s_cn[e] = c;
;         for (int i = 0; i < nt; ++i) s_te[excl + i] = (unsigned char)e;
; template <int layer>
; __device__ __forceinline__ void ph_down(LAS unsigned char* lds) {
;     PH_BEGIN;
;     moe_prefix(lds, WSP(unsigned, WS_CTL) + (layer == 0 ? CW_CNT0 : CW_CNT1));
.Lgbd_17:
.LBB0_1891:
	s_or_b64 exec, exec, s[4:5]
	s_mov_b32 s0, 30
	s_waitcnt lgkmcnt(0)
	s_barrier
	s_ashr_i32 s1, s0, 31
	s_lshl_b64 s[0:1], s[0:1], 3
	s_add_u32 s0, s80, s0
	s_addc_u32 s1, s81, s1
	s_load_dwordx2 s[4:5], s[0:1], 0x0
	v_mov_b32_e32 v1, v0
	s_mov_b32 s16, s78
	s_mov_b32 s1, s79
	v_mov_b32_e32 v6, v0
	s_nop 0
	v_cmp_gt_i32_e32 vcc, 64, v6
	s_and_saveexec_b64 s[6:7], vcc
	s_cbranch_execz .LBB0_1921
	v_ashrrev_i32_e32 v7, 31, v6
	s_waitcnt lgkmcnt(0)
	v_lshl_add_u64 v[2:3], v[6:7], 2, s[4:5]
	v_add_co_u32_e32 v2, vcc, 0x2000, v2
	v_lshl_add_u32 v4, v6, 2, 0
	s_nop 0
	v_addc_co_u32_e32 v3, vcc, 0, v3, vcc
	global_load_dword v2, v[2:3], off
	v_mbcnt_hi_u32_b32 v3, -1, v236
	v_and_b32_e32 v7, 64, v3
	v_add_u32_e32 v1, -1, v3
	v_cmp_lt_i32_e32 vcc, v1, v7
	v_add_u32_e32 v5, -2, v3
	v_add_u32_e32 v8, -4, v3
	v_cndmask_b32_e32 v1, v1, v3, vcc
	v_lshlrev_b32_e32 v10, 2, v1
	v_cmp_lt_i32_e32 vcc, v5, v7
	v_add_u32_e32 v9, -8, v3
	v_add_u32_e32 v13, -16, v3
	v_cndmask_b32_e32 v5, v5, v3, vcc
	v_cmp_lt_i32_e32 vcc, 0, v6
	v_lshlrev_b32_e32 v5, 2, v5
	v_subrev_u32_e32 v14, 32, v3
	v_add_u32_e32 v16, 0x26c40, v4
	v_add_u32_e32 v4, 0x26d50, v4
	s_waitcnt vmcnt(0)
	v_add_u32_e32 v1, 0xff, v2
	v_ashrrev_i32_e32 v1, 8, v1
	ds_bpermute_b32 v10, v10, v1
	ds_write_b32 v4, v2
	s_waitcnt lgkmcnt(1)
	v_cndmask_b32_e32 v10, 0, v10, vcc
	v_add_u32_e32 v12, v10, v1
	ds_bpermute_b32 v5, v5, v12
	v_cmp_lt_i32_e32 vcc, v8, v7
	s_nop 1
	v_cndmask_b32_e32 v8, v8, v3, vcc
	v_cmp_lt_i32_e32 vcc, 1, v6
	v_lshlrev_b32_e32 v8, 2, v8
	s_waitcnt lgkmcnt(0)
	v_cndmask_b32_e32 v11, 0, v5, vcc
	v_add_u32_e32 v5, v11, v12
	ds_bpermute_b32 v8, v8, v5
	v_cmp_lt_i32_e32 vcc, v9, v7
	s_nop 1
	v_cndmask_b32_e32 v9, v9, v3, vcc
	v_cmp_lt_i32_e32 vcc, 3, v6
	v_lshlrev_b32_e32 v9, 2, v9
	s_waitcnt lgkmcnt(0)
	v_cndmask_b32_e32 v12, 0, v8, vcc
	v_add_u32_e32 v5, v12, v5
	ds_bpermute_b32 v8, v9, v5
	v_cmp_lt_i32_e32 vcc, v13, v7
	s_nop 1
	v_cndmask_b32_e32 v9, v13, v3, vcc
	v_cmp_lt_i32_e32 vcc, 7, v6
	v_lshlrev_b32_e32 v9, 2, v9
	s_waitcnt lgkmcnt(0)
	v_cndmask_b32_e32 v13, 0, v8, vcc
	v_add_u32_e32 v5, v13, v5
	ds_bpermute_b32 v8, v9, v5
	v_cmp_lt_i32_e32 vcc, v14, v7
	s_nop 1
	v_cndmask_b32_e32 v3, v14, v3, vcc
	v_cmp_lt_i32_e32 vcc, 15, v6
	v_lshlrev_b32_e32 v3, 2, v3
	s_waitcnt lgkmcnt(0)
	v_cndmask_b32_e32 v14, 0, v8, vcc
	v_add_u32_e32 v5, v14, v5
	ds_bpermute_b32 v3, v3, v5
	v_cmp_lt_i32_e32 vcc, 31, v6
	v_sub_u32_e32 v2, v5, v1
	s_waitcnt lgkmcnt(0)
	v_cndmask_b32_e32 v15, 0, v3, vcc
	v_add_u32_e32 v2, v2, v15
	v_cmp_lt_i32_e32 vcc, 0, v1
	ds_write_b32 v16, v2
	s_and_saveexec_b64 s[8:9], vcc
	s_cbranch_execz .LBB0_1905
	v_cmp_lt_u32_e32 vcc, 7, v1
	s_mov_b64 s[12:13], -1
	v_mov_b32_e32 v2, 0
	s_and_saveexec_b64 s[10:11], vcc
	s_cbranch_execz .LBB0_1902
	s_mov_b32 s0, 0x4040404
	v_add_u32_e32 v2, -8, v1
	v_perm_b32 v8, v6, v6, s0
	v_lshrrev_b32_e32 v3, 3, v2
	v_mov_b32_e32 v9, v8
	v_add_u32_e32 v16, 1, v3
	v_cmp_lt_u32_e32 vcc, 55, v2
	v_mov_b32_e32 v19, 0
	s_and_saveexec_b64 s[12:13], vcc
	s_cbranch_execz .LBB0_1898
	v_add3_u32 v2, v10, v15, v14
	v_add3_u32 v2, v2, v13, v12
	v_and_b32_e32 v17, 0x3ffffff8, v16
	s_mov_b32 s0, 0
	v_add3_u32 v18, v2, v11, 0
	s_mov_b64 s[14:15], 0
	v_mov_b32_e32 v2, v8
	v_mov_b32_e32 v3, v8
	v_mov_b32_e32 v4, v8
	v_mov_b32_e32 v5, v8

; __device__ __forceinline__ unsigned xb_add(unsigned* p, unsigned v) { return __hip_atomic_fetch_add(p, v, __ATOMIC_RELAXED, __HIP_MEMORY_SCOPE_AGENT); }
; __device__ __forceinline__ void xcd_barrier(const XcdBarrier& b) {
;     ...
;     if (threadIdx.x == 0) {
;         unsigned* bar = b.bar;
;         __builtin_amdgcn_s_waitcnt(0);
;         unsigned nloc = b.st[0], nx = b.st[1];
;         if (nloc == 0u) { xcd_barrier_complete(bar, b.x, nloc, nx); b.st[0] = nloc; b.st[1] = nx; }
;         const unsigned old = xb_add(&bar[XB_XSUB(b.x)], 1u);
;         const unsigned gen = old / nloc;
;         if (old + 1u == (gen + 1u) * nloc) {
;             __builtin_amdgcn_fence(__ATOMIC_RELEASE, "agent");
;             asm volatile("s_waitcnt vmcnt(0)" ::: "memory");
;             const unsigned og = xb_add(&bar[XB_TOP], 1u);
;             const unsigned tg = og / nx;
;             if (og + 1u == (tg + 1u) * nx) xb_add(&bar[XB_TOPGEN], 1u);
.LBB0_1999:
	s_waitcnt lgkmcnt(0)
	v_readfirstlane_b32 s8, v3
	v_readfirstlane_b32 s9, v1
	v_readlane_b32 s0, v252, 4
	s_lshl_b32 s0, s0, 8
	v_readlane_b32 s2, v252, 2
	v_readlane_b32 s3, v252, 3
	s_add_u32 s6, s2, s0
	s_addc_u32 s7, s3, 0
	s_mul_i32 s10, s8, 19
	s_mul_i32 s11, s9, 19
	v_mov_b32_e32 v4, 0x1000
	v_mov_b32_e32 v5, 1
	global_atomic_add v4, v4, v5, s[6:7] offset:1024 sc0
	v_mov_b32_e32 v1, 0x3400
	s_waitcnt vmcnt(0)
	v_readfirstlane_b32 s0, v4
	s_add_u32 s0, s0, 1
	s_cmp_lg_u32 s0, s10
	buffer_inv sc1
	s_cbranch_scc1 .Lgbw_18
	buffer_wbl2 sc1
	s_waitcnt vmcnt(0)
	global_atomic_add v1, v5, s[2:3]

; #define LAS __attribute__((address_space(3)))
; __device__ __forceinline__ int otid() { int t = threadIdx.x; asm volatile("" : "+v"(t)); return t; }
; __device__ __forceinline__ void moe_prefix(LAS unsigned char* lds, const unsigned* cnt) {
;     LAS int* s_ts = (LAS int*)(lds + LDS_TS); LAS int* s_cn = (LAS int*)(lds + LDS_CN);
;     LAS unsigned char* s_te = lds + LDS_TE;
;     LAS int* s_xs = (LAS int*)(lds + LDS_XS);
;     const int tz_ = otid();
;     if (tz_ < 64) { const int e = tz_; const int c = (int)cnt[e], nt = (c + 255) >> 8;
;         int incl = nt;
; #pragma unroll
;         for (int o = 1; o < 64; o <<= 1) { const int up = __shfl_up(incl, o); if (e >= o) incl += up; }
;         const int excl = incl - nt;
;         s_ts[e] = excl; s_cn[e] = c;
;         for (int i = 0; i < nt; ++i) s_te[excl + i] = (unsigned char)e;
; template <int MODE>
; __device__ __forceinline__ void norm_rows(LAS unsigned char* lds, float* in, const float* gain, const unsigned* cnt) {
;     PH_BEGIN;
;     bf16* HN = WSP(bf16, WS_HN); const bf16* YS = WSP(bf16, WS_YS); const int* TSLOT = WSP(int, WS_TSLOT); bf16* H1b = WSP(bf16, WS_H1);
;     if (MODE != 0) moe_prefix(lds, cnt);
.Lgbd_18:
.LBB0_2035:
	s_or_b64 exec, exec, s[4:5]
	s_mov_b32 s0, 29
	s_waitcnt lgkmcnt(0)
	s_barrier
	s_ashr_i32 s1, s0, 31
	s_lshl_b64 s[0:1], s[0:1], 3
	s_add_u32 s0, s80, s0
	s_addc_u32 s1, s81, s1
	s_load_dwordx2 s[8:9], s[0:1], 0x0
	s_mov_b32 s0, 30
	s_mov_b32 s10, 30
	s_ashr_i32 s1, s0, 31
	s_lshl_b64 s[0:1], s[0:1], 3
	s_add_u32 s0, s80, s0
	s_addc_u32 s1, s81, s1
	s_load_dwordx2 s[6:7], s[0:1], 0x0
	v_mov_b32_e32 v8, v0
	s_mov_b32 s16, s79
	s_nop 0
	v_cmp_gt_i32_e32 vcc, 64, v0
	s_and_saveexec_b64 s[4:5], vcc
	s_cbranch_execz .LBB0_2065
	s_ashr_i32 s11, s10, 31
	s_lshl_b64 s[0:1], s[10:11], 3
	s_add_u32 s0, s80, s0
	s_addc_u32 s1, s81, s1
	s_load_dwordx2 s[0:1], s[0:1], 0x0
	v_ashrrev_i32_e32 v1, 31, v0
	v_lshl_add_u32 v4, v0, 2, 0
	v_add_u32_e32 v16, 0x26c40, v4
	v_add_u32_e32 v4, 0x26d50, v4
	s_waitcnt lgkmcnt(0)
	v_lshl_add_u64 v[2:3], v[0:1], 2, s[0:1]
	v_add_co_u32_e32 v2, vcc, 0x2000, v2
	s_nop 1
	v_addc_co_u32_e32 v3, vcc, 0, v3, vcc
	global_load_dword v2, v[2:3], off
	v_mbcnt_hi_u32_b32 v3, -1, v236
	v_and_b32_e32 v9, 64, v3
	v_add_u32_e32 v1, -1, v3
	v_cmp_lt_i32_e32 vcc, v1, v9
	v_add_u32_e32 v5, -2, v3
	v_add_u32_e32 v6, -4, v3
	v_cndmask_b32_e32 v1, v1, v3, vcc
	v_lshlrev_b32_e32 v10, 2, v1
	v_cmp_lt_i32_e32 vcc, v5, v9
	v_add_u32_e32 v7, -8, v3
	v_add_u32_e32 v13, -16, v3
	v_cndmask_b32_e32 v5, v5, v3, vcc
	v_cmp_lt_i32_e32 vcc, 0, v0
	v_lshlrev_b32_e32 v5, 2, v5
	v_subrev_u32_e32 v14, 32, v3
	s_waitcnt vmcnt(0)
	v_add_u32_e32 v1, 0xff, v2
	v_ashrrev_i32_e32 v1, 8, v1
	ds_bpermute_b32 v10, v10, v1
	ds_write_b32 v4, v2
	s_waitcnt lgkmcnt(1)
	v_cndmask_b32_e32 v10, 0, v10, vcc
	v_add_u32_e32 v12, v10, v1
	ds_bpermute_b32 v5, v5, v12
	v_cmp_lt_i32_e32 vcc, v6, v9
	s_nop 1
	v_cndmask_b32_e32 v6, v6, v3, vcc
	v_cmp_lt_i32_e32 vcc, 1, v0
	v_lshlrev_b32_e32 v6, 2, v6
	s_waitcnt lgkmcnt(0)
	v_cndmask_b32_e32 v11, 0, v5, vcc
	v_add_u32_e32 v5, v11, v12
	ds_bpermute_b32 v6, v6, v5
	v_cmp_lt_i32_e32 vcc, v7, v9
	s_nop 1
	v_cndmask_b32_e32 v7, v7, v3, vcc
	v_cmp_lt_i32_e32 vcc, 3, v0
	v_lshlrev_b32_e32 v7, 2, v7
	s_waitcnt lgkmcnt(0)
	v_cndmask_b32_e32 v12, 0, v6, vcc
	v_add_u32_e32 v5, v12, v5
	ds_bpermute_b32 v6, v7, v5
	v_cmp_lt_i32_e32 vcc, v13, v9
	s_nop 1
	v_cndmask_b32_e32 v7, v13, v3, vcc
	v_cmp_lt_i32_e32 vcc, 7, v0
	v_lshlrev_b32_e32 v7, 2, v7
	s_waitcnt lgkmcnt(0)
	v_cndmask_b32_e32 v13, 0, v6, vcc
	v_add_u32_e32 v5, v13, v5
	ds_bpermute_b32 v6, v7, v5
	v_cmp_lt_i32_e32 vcc, v14, v9
	s_nop 1
	v_cndmask_b32_e32 v3, v14, v3, vcc
	v_cmp_lt_i32_e32 vcc, 15, v0
	v_lshlrev_b32_e32 v3, 2, v3
	s_waitcnt lgkmcnt(0)
	v_cndmask_b32_e32 v14, 0, v6, vcc
	v_add_u32_e32 v5, v14, v5
	ds_bpermute_b32 v3, v3, v5
	v_cmp_lt_i32_e32 vcc, 31, v0
	v_sub_u32_e32 v2, v5, v1
	s_waitcnt lgkmcnt(0)
	v_cndmask_b32_e32 v15, 0, v3, vcc
	v_add_u32_e32 v2, v2, v15
	v_cmp_lt_i32_e32 vcc, 0, v1
	ds_write_b32 v16, v2
	s_and_saveexec_b64 s[0:1], vcc
	s_cbranch_execz .LBB0_2049
	v_cmp_lt_u32_e32 vcc, 7, v1
	s_mov_b64 s[12:13], -1
	v_mov_b32_e32 v2, 0
	s_and_saveexec_b64 s[10:11], vcc
	s_cbranch_execz .LBB0_2046
	s_mov_b32 s2, 0x4040404
	v_add_u32_e32 v2, -8, v1
	v_perm_b32 v6, v0, v0, s2
	v_lshrrev_b32_e32 v3, 3, v2
	v_mov_b32_e32 v7, v6
	v_add_u32_e32 v16, 1, v3
	v_cmp_lt_u32_e32 vcc, 55, v2
	v_mov_b32_e32 v19, 0
	s_and_saveexec_b64 s[12:13], vcc
	s_cbranch_execz .LBB0_2042
	v_add3_u32 v2, v10, v15, v14
	v_add3_u32 v2, v2, v13, v12
	v_and_b32_e32 v17, 0x3ffffff8, v16
	s_mov_b32 s2, 0
	v_add3_u32 v18, v2, v11, 0
	s_mov_b64 s[14:15], 0
	v_mov_b32_e32 v2, v6
	v_mov_b32_e32 v3, v6
	v_mov_b32_e32 v4, v6
	v_mov_b32_e32 v5, v6
